# v53 + latent attention: m0 save/restore around LDS-DMA dropped; MoE gate/up K-loop: DMA source addresses computed inside the preceding MFMA block
# speedup vs baseline: 1.0060x; 1.0060x over previous
; __device__ __forceinline__ int tid_from_wave(int wave) { unsigned l_; asm volatile("v_mbcnt_lo_u32_b32 %0, -1, 0\n\tv_mbcnt_hi_u32_b32 %0, -1, %0" : "=v"(l_)); return wave * 64 + (int)l_; }
; template <int THRL, bool LATE> __device__ __forceinline__ void unit_stag(int b, int h, int qb, const unsigned short* Q, const unsigned short* KV, const unsigned short* KPE, unsigned short* O, char* shm, const int wave_) {
;     int tid_ = tid_from_wave(wave_); asm volatile("" : "+v"(tid_));
;     const int tid = tid_, lane = tid & 63, r32 = lane & 31, hi = lane >> 5; const int wid = __builtin_amdgcn_readfirstlane(tid >> 6);
;     const long rowbase = (long)b * SEQ; const int q0 = qb * QB;
;     const unsigned short* Qw = Q + (rowbase + q0 + wid * QBLK) * QP + h * 96;
;     const unsigned short* Kh = KV + rowbase * KVP + h * 128; const unsigned short* Vh = Kh + 64; const unsigned short* Ph = KPE + rowbase * PEP;
;     const unsigned lds0 = (unsigned)(uintptr_t)shm;
;     __attribute__((address_space(3))) float* wsf = (__attribute__((address_space(3))) float*)((lds_cptr)shm + S4_WS) + wid * 64;
;     const unsigned short* ksrc = Kh + (long)lane * KVP + wid * 8;
;     const unsigned short* psrc = Ph + (long)(32 * (wid & 1) + r32) * PEP + (wid >> 1) * 8;
;     const unsigned short* vsrc = Vh + (long)(16 * (wid & 3) + (lane >> 2)) * KVP + (wid >> 2) * 32 + (lane & 3) * 8;
;     const unsigned kdst = lds0 + LDS_K + wid * 1024, pdst = lds0 + LDS_K + (8 + (wid >> 1)) * 1024 + (wid & 1) * 512, vdst = lds0 + S4_V + wid * 1024;
;     const int vb0 = (int)(lds0 + S4_V) + ((lane >> 4) & 1) * 32 + (lane & 3) * 8 + (4 * hi + ((lane & 15) >> 2)) * 64;
;     const lds_cptr kp0 = (lds_cptr)shm + LDS_K + hi * 1024 + r32 * 16;
;     const int NT = (q0 + QB) / KVBLK;
;     bf16x8 qr[6];
; #pragma unroll
;     for (int d0 = 0; d0 < 6; ++d0) qr[d0] = *reinterpret_cast<const bf16x8*>(&Qw[(long)r32 * QP + d0 * 16 + hi * 8]);
;     asm volatile("s_waitcnt vmcnt(0)" ::: "memory");
;     glds16(ksrc, (unsigned)__builtin_amdgcn_readfirstlane(kdst)); if (lane < 32) glds16(psrc, (unsigned)__builtin_amdgcn_readfirstlane(pdst));
;     glds16(ksrc + (long)KVBLK * KVP, (unsigned)__builtin_amdgcn_readfirstlane(kdst + KSLOT)); if (lane < 32) glds16(psrc + (long)KVBLK * PEP, (unsigned)__builtin_amdgcn_readfirstlane(pdst + KSLOT)); glds16(vsrc, (unsigned)__builtin_amdgcn_readfirstlane(vdst));
.LBB0_1093:
	s_cmp_lg_u32 s2, 0
	s_cbranch_scc0 .LBB0_1123
	s_lshl_b32 s46, s2, 8
	s_add_u32 s47, s34, s46
	s_addc_u32 s69, s35, 0
	s_mov_b64 s[0:1], -1
	s_and_b64 vcc, exec, s[8:9]
	s_cbranch_vccz .LBB0_1145
	v_mbcnt_lo_u32_b32 v0, -1, 0
	v_mbcnt_hi_u32_b32 v0, -1, v0
	s_nop 0
	v_add_u32_e32 v82, s96, v0
	s_nop 0
	v_readfirstlane_b32 s10, v82
	s_ashr_i32 s68, s10, 6
	s_lshl_b32 s75, s68, 5
	s_ashr_i32 s0, s75, 31
	s_add_u32 s40, s47, s75
	s_addc_u32 s41, s69, s0
	v_and_b32_e32 v169, 31, v82
	s_mul_i32 s0, s41, 0x600
	s_mul_hi_u32 s1, s40, 0x600
	s_add_i32 s1, s1, s0
	s_mul_i32 s0, s40, 0x600
	v_mul_u32_u24_e32 v0, 0x300, v169
	v_bfe_u32 v170, v82, 5, 1
	s_add_u32 s0, s63, s0
	v_lshlrev_b32_e32 v0, 1, v0
	s_addc_u32 s1, s64, s1
	v_lshl_or_b32 v0, v170, 4, v0
	global_load_dwordx4 v[150:153], v0, s[0:1]
	global_load_dwordx4 v[146:149], v0, s[0:1] offset:32
	global_load_dwordx4 v[142:145], v0, s[0:1] offset:64
	global_load_dwordx4 v[138:141], v0, s[0:1] offset:96
	global_load_dwordx4 v[134:137], v0, s[0:1] offset:128
	global_load_dwordx4 v[130:133], v0, s[0:1] offset:160
	s_ashr_i32 s44, s10, 7
	s_lshl_b32 s0, s68, 3
	s_lshl_b32 s2, s44, 3
	v_and_b32_e32 v155, 63, v82
	s_ashr_i32 s1, s0, 31
	s_and_b32 s43, s68, 1
	s_ashr_i32 s3, s2, 31
	s_lshl_b32 s42, s68, 10
	s_lshl_b32 s44, s44, 10
	s_cmp_lg_u32 0, -1
	v_lshlrev_b32_e32 v0, 11, v155
	s_cselect_b32 s45, 0, 0
	v_lshl_add_u64 v[2:3], s[36:37], 0, v[0:1]
	v_lshlrev_b32_e32 v0, 6, v169
	s_waitcnt vmcnt(0)
	s_add_i32 s44, s45, s44
	s_lshl_b32 s70, s43, 9
	v_lshl_add_u64 v[160:161], s[0:1], 1, v[2:3]
	v_lshl_or_b32 v0, s43, 11, v0
	s_add_i32 s76, s42, s45
	s_mov_b32 m0, s76
	s_nop 0
	global_load_lds_dwordx4 v[160:161], off
	s_add_i32 s71, s44, s70
	v_lshl_add_u64 v[2:3], s[38:39], 0, v[0:1]
	s_addk_i32 s71, 0x2000
	v_lshl_add_u64 v[158:159], s[2:3], 1, v[2:3]
	v_cmp_gt_u32_e64 s[2:3], 32, v155
	s_and_saveexec_b64 s[0:1], s[2:3]
	s_cbranch_execz .LBB0_1097
	s_mov_b32 m0, s71
	s_nop 0
	global_load_lds_dwordx4 v[158:159], off
.LBB0_1097:
	s_or_b64 exec, exec, s[0:1]
	s_cmp_lg_u32 0, -1
	s_cselect_b32 s0, 0, 0
	s_add_i32 s0, s0, s42
	v_lshl_add_u64 v[2:3], v[160:161], 0, s[12:13]
	s_addk_i32 s0, 0x3000
	s_mov_b32 m0, s0
	s_nop 0
	global_load_lds_dwordx4 v[2:3], off
	s_and_saveexec_b64 s[0:1], s[2:3]
	s_cbranch_execz .LBB0_1099
	v_lshl_add_u64 v[2:3], v[158:159], 0, s[14:15]
	s_add_i32 s43, s71, 0x3000
	s_mov_b32 m0, s43
	s_nop 0
	global_load_lds_dwordx4 v[2:3], off
.LBB0_1099:
	s_or_b64 exec, exec, s[0:1]
	s_lshl_b32 s0, s68, 4
	v_lshrrev_b32_e32 v0, 2, v155
	v_and_or_b32 v0, s0, 48, v0
	s_ashr_i32 s0, s10, 3
	s_andn2_b32 s0, s0, 31
	s_ashr_i32 s1, s0, 31
	v_lshlrev_b32_e32 v168, 3, v82
	v_lshlrev_b32_e32 v0, 11, v0
	v_and_b32_e32 v83, 24, v168
	v_lshl_add_u64 v[2:3], s[36:37], 0, v[0:1]
	s_cmp_lg_u32 0, -1
	v_lshl_add_u64 v[2:3], s[0:1], 1, v[2:3]
	v_lshlrev_b32_e32 v0, 1, v83
	s_cselect_b32 s0, 0, 0
	v_lshl_add_u64 v[2:3], v[2:3], 0, v[0:1]
	s_add_i32 s0, s0, s42
	v_lshl_add_u64 v[156:157], v[2:3], 0, s[16:17]
	s_add_i32 s72, s0, 0x9000
	s_mov_b32 m0, s72
	s_nop 0
	global_load_lds_dwordx4 v[156:157], off
	v_lshl_add_u64 v[2:3], v[160:161], 0, s[18:19]
	s_addk_i32 s0, 0x6000
	s_mov_b32 m0, s0
	s_nop 0
	global_load_lds_dwordx4 v[2:3], off
	s_and_saveexec_b64 s[0:1], s[2:3]
	s_cbranch_execz .LBB0_1101
	v_lshl_add_u64 v[2:3], v[158:159], 0, s[20:21]
	s_add_i32 s43, s71, 0x6000
	s_mov_b32 m0, s43
	s_nop 0
	global_load_lds_dwordx4 v[2:3], off
.LBB0_1101:
	s_or_b64 exec, exec, s[0:1]
	s_cmp_lg_u32 0, -1
	v_lshlrev_b32_e32 v0, 10, v170
	v_lshlrev_b32_e32 v2, 4, v169
	s_cselect_b32 s0, 0, 0
	v_add3_u32 v173, 0, v0, v2
	v_lshl_add_u64 v[2:3], v[156:157], 0, s[12:13]
	s_add_i32 s0, s0, s42
	s_add_i32 s0, s0, 0xb000
	s_mov_b32 m0, s0
	s_nop 0
	global_load_lds_dwordx4 v[2:3], off
	v_mov_b32_e32 v2, v1
	v_mov_b32_e32 v3, v1
	v_mov_b32_e32 v4, v1
	v_mov_b32_e32 v5, v1
	v_mov_b32_e32 v6, v1
	v_mov_b32_e32 v7, v1
	v_mov_b32_e32 v8, v1
	v_mov_b32_e32 v9, v1
	v_mov_b32_e32 v10, v1
	v_mov_b32_e32 v11, v1
	v_mov_b32_e32 v12, v1
	v_mov_b32_e32 v13, v1
	v_mov_b32_e32 v14, v1
	v_mov_b32_e32 v15, v1
	v_mov_b32_e32 v0, v1
	v_mov_b64_e32 v[16:17], v[14:15]
	v_mov_b64_e32 v[14:15], v[12:13]
	v_mov_b64_e32 v[12:13], v[10:11]
	v_mov_b64_e32 v[10:11], v[8:9]
	v_mov_b64_e32 v[8:9], v[6:7]
	v_mov_b64_e32 v[6:7], v[4:5]
	v_mov_b64_e32 v[4:5], v[2:3]
	v_mov_b64_e32 v[2:3], v[0:1]
	s_waitcnt vmcnt(6) lgkmcnt(0)
	s_barrier
; #define MLA_PIN(x) asm volatile("" : "+v"(x))
; #define MLA_LDK(kp, d0, h) (*(const __attribute__((address_space(3))) bf16x8*)((kp) + (d0) * 2048 + (h) * 512))
; #define MLA_MF(C, K, Q) C = __builtin_amdgcn_mfma_f32_32x32x16_bf16(K, Q, C, 0, 0, 0)
; template <int THRL, bool LATE> __device__ __forceinline__ void unit_stag(int b, int h, int qb, const unsigned short* Q, const unsigned short* KV, const unsigned short* KPE, unsigned short* O, char* shm, const int wave_) {
;     ...
;     { const lds_cptr kp = kp0;
;       pA0 = f32x16{}; pA1 = f32x16{};
; #pragma unroll
;       for (int d0 = 0; d0 < 6; ++d0) { const bf16x8 k0 = MLA_LDK(kp, d0, 0), k1 = MLA_LDK(kp, d0, 1); MLA_MF(pA0, k0, qr[d0]); MLA_MF(pA1, k1, qr[d0]); } }
;     { const float rm_ = rowmax(pA0, pA1); mhat = rm_;
; #pragma unroll
;       for (int r = 0; r < 16; ++r) { pA0[r] -= rm_; pA1[r] -= rm_; negm[r] = -mhat; }
;       MLA_PIN(negm); }
;     int t = 0;
;     MLA_STEPS(pB0, pB1, pA0, pA1, t, -1, 3, true, true, false); ++t;
	ds_read_b128 v[2:5], v173
	ds_read_b128 v[6:9], v173 offset:512
	s_waitcnt vmcnt(5) lgkmcnt(1)
	v_mfma_f32_32x32x16_bf16 v[18:33], v[2:5], v[150:153], 0
	ds_read_b128 v[34:37], v173 offset:2048
	ds_read_b128 v[38:41], v173 offset:2560
	v_lshl_add_u64 v[50:51], v[160:161], 0, s[22:23]
	s_waitcnt lgkmcnt(2)
	v_mfma_f32_32x32x16_bf16 v[2:17], v[6:9], v[150:153], 0
	s_waitcnt vmcnt(4) lgkmcnt(1)
	v_mfma_f32_32x32x16_bf16 v[18:33], v[34:37], v[146:149], v[18:33]
	s_waitcnt lgkmcnt(0)
	v_mfma_f32_32x32x16_bf16 v[2:17], v[38:41], v[146:149], v[2:17]
	ds_read_b128 v[34:37], v173 offset:4096
	ds_read_b128 v[38:41], v173 offset:4608
	s_waitcnt vmcnt(3) lgkmcnt(1)
	v_mfma_f32_32x32x16_bf16 v[18:33], v[34:37], v[142:145], v[18:33]
	s_waitcnt lgkmcnt(0)
	v_mfma_f32_32x32x16_bf16 v[2:17], v[38:41], v[142:145], v[2:17]
	ds_read_b128 v[34:37], v173 offset:6144
	ds_read_b128 v[38:41], v173 offset:6656
	s_waitcnt vmcnt(2) lgkmcnt(1)
	v_mfma_f32_32x32x16_bf16 v[18:33], v[34:37], v[138:141], v[18:33]
	s_waitcnt lgkmcnt(0)
	v_mfma_f32_32x32x16_bf16 v[2:17], v[38:41], v[138:141], v[2:17]
	ds_read_b128 v[34:37], v173 offset:8192
	ds_read_b128 v[38:41], v173 offset:8704
	s_waitcnt vmcnt(1) lgkmcnt(1)
	v_mfma_f32_32x32x16_bf16 v[18:33], v[34:37], v[134:137], v[18:33]
	s_waitcnt lgkmcnt(0)
	v_mfma_f32_32x32x16_bf16 v[2:17], v[38:41], v[134:137], v[2:17]
	ds_read_b128 v[34:37], v173 offset:10240
	ds_read_b128 v[38:41], v173 offset:10752
	s_waitcnt vmcnt(0) lgkmcnt(1)
	v_mfma_f32_32x32x16_bf16 v[18:33], v[34:37], v[130:133], v[18:33]
	s_waitcnt lgkmcnt(0)
	v_mfma_f32_32x32x16_bf16 v[2:17], v[38:41], v[130:133], v[2:17]
	v_max3_f32 v0, v18, v19, v2
	v_max3_f32 v34, v20, v21, v3
	s_nop 0
	v_max3_f32 v0, v0, v4, v5
	v_max3_f32 v34, v34, v24, v25
	s_nop 0
	v_max3_f32 v0, v0, v22, v23
	v_max3_f32 v34, v34, v8, v9
	s_nop 0
	v_max3_f32 v0, v0, v6, v7
	v_max3_f32 v34, v34, v28, v29
	s_nop 0
	v_max3_f32 v0, v0, v26, v27
	v_max3_f32 v34, v34, v12, v13
	s_nop 0
	v_max3_f32 v0, v0, v10, v11
	v_max3_f32 v34, v34, v32, v33
	s_nop 0
	v_max3_f32 v0, v0, v30, v31
	v_max3_f32 v34, v34, v16, v17
	s_nop 0
	v_max3_f32 v0, v0, v14, v15
	v_max_f32_e32 v34, v34, v34
	v_max_f32_e32 v0, v0, v0
	v_max_f32_e32 v0, v0, v34
	v_mov_b32_e32 v34, v0
	s_nop 1
	v_permlane32_swap_b32_e32 v0, v34
	v_max_f32_e32 v34, v34, v34
	v_max_f32_e32 v0, v0, v0
	v_max_f32_e32 v154, v0, v34
	v_xor_b32_e32 v34, 0x80000000, v154
	v_mov_b32_e32 v35, v34
	v_mov_b32_e32 v36, v34
	v_mov_b32_e32 v37, v34
	v_mov_b32_e32 v38, v34
	v_mov_b32_e32 v39, v34
	v_mov_b32_e32 v40, v34
	v_mov_b32_e32 v41, v34
	v_mov_b32_e32 v42, v34
	v_mov_b32_e32 v43, v34
	v_mov_b32_e32 v44, v34
	v_mov_b32_e32 v45, v34
	v_mov_b32_e32 v46, v34
	v_mov_b32_e32 v47, v34
	v_mov_b32_e32 v48, v34
	v_mov_b32_e32 v49, v34
	s_waitcnt vmcnt(3) lgkmcnt(0)
	s_barrier
	s_mov_b32 m0, s76
	s_nop 0
	global_load_lds_dwordx4 v[50:51], off
	s_and_saveexec_b64 s[0:1], s[2:3]
	s_cbranch_execz .LBB0_1103
	v_lshl_add_u64 v[50:51], v[158:159], 0, s[26:27]
	s_mov_b32 m0, s71
	s_nop 0
	global_load_lds_dwordx4 v[50:51], off
.LBB0_1103:
	s_or_b64 exec, exec, s[0:1]
	s_and_b32 s0, s10, 0x3fffffc0
	s_lshl_b32 s0, s0, 2
	s_add_i32 s74, s0, 0
	s_add_i32 s74, s74, 0x11000
	s_cmp_lg_u32 0, -1
	s_cselect_b32 s0, 0, 0
	s_add_i32 s0, s0, s42
	v_sub_f32_e32 v96, v2, v154
	v_sub_f32_e32 v97, v3, v154
	v_lshl_add_u64 v[2:3], v[156:157], 0, s[18:19]
	s_add_i32 s0, s0, 0xd000
	s_mov_b32 m0, s0
	s_nop 0
	global_load_lds_dwordx4 v[2:3], off
	v_sub_f32_e32 v0, v18, v154
	v_sub_f32_e32 v19, v19, v154
	v_sub_f32_e32 v20, v20, v154
	v_sub_f32_e32 v98, v4, v154
	v_sub_f32_e32 v4, v21, v154
	v_sub_f32_e32 v99, v5, v154
	v_pk_add_f32 v[22:23], v[22:23], v[154:155] op_sel_hi:[1,0] neg_lo:[0,1] neg_hi:[0,1]
	v_pk_add_f32 v[6:7], v[6:7], v[154:155] op_sel_hi:[1,0] neg_lo:[0,1] neg_hi:[0,1]
	v_pk_add_f32 v[24:25], v[24:25], v[154:155] op_sel_hi:[1,0] neg_lo:[0,1] neg_hi:[0,1]
	v_pk_add_f32 v[8:9], v[8:9], v[154:155] op_sel_hi:[1,0] neg_lo:[0,1] neg_hi:[0,1]
	v_pk_add_f32 v[26:27], v[26:27], v[154:155] op_sel_hi:[1,0] neg_lo:[0,1] neg_hi:[0,1]
	v_pk_add_f32 v[10:11], v[10:11], v[154:155] op_sel_hi:[1,0] neg_lo:[0,1] neg_hi:[0,1]
	v_pk_add_f32 v[28:29], v[28:29], v[154:155] op_sel_hi:[1,0] neg_lo:[0,1] neg_hi:[0,1]
	v_pk_add_f32 v[12:13], v[12:13], v[154:155] op_sel_hi:[1,0] neg_lo:[0,1] neg_hi:[0,1]
	v_pk_add_f32 v[30:31], v[30:31], v[154:155] op_sel_hi:[1,0] neg_lo:[0,1] neg_hi:[0,1]
	v_pk_add_f32 v[14:15], v[14:15], v[154:155] op_sel_hi:[1,0] neg_lo:[0,1] neg_hi:[0,1]
	v_pk_add_f32 v[32:33], v[32:33], v[154:155] op_sel_hi:[1,0] neg_lo:[0,1] neg_hi:[0,1]
	v_pk_add_f32 v[16:17], v[16:17], v[154:155] op_sel_hi:[1,0] neg_lo:[0,1] neg_hi:[0,1]
	s_setprio 1
	v_exp_f32_e32 v21, v4
	ds_read_b128 v[2:5], v173 offset:12288
	ds_read_b128 v[84:87], v173 offset:12800
	v_exp_f32_e32 v18, v0
	v_exp_f32_e32 v19, v19
	v_exp_f32_e32 v20, v20
	s_nop 0
	v_exp_f32_e32 v22, v22
	v_exp_f32_e32 v23, v23
	v_exp_f32_e32 v24, v24
	v_exp_f32_e32 v25, v25
	s_waitcnt lgkmcnt(1)
	v_mfma_f32_32x32x16_bf16 v[66:81], v[2:5], v[150:153], v[34:49]
	ds_read_b128 v[88:91], v173 offset:14336
	ds_read_b128 v[92:95], v173 offset:14848
	v_exp_f32_e32 v26, v26
	v_exp_f32_e32 v27, v27
	v_exp_f32_e32 v28, v28
	v_exp_f32_e32 v29, v29
	v_mov_b64_e32 v[64:65], v[48:49]
	v_mov_b64_e32 v[62:63], v[46:47]
	v_mov_b64_e32 v[60:61], v[44:45]
	v_mov_b64_e32 v[58:59], v[42:43]
	v_mov_b64_e32 v[56:57], v[40:41]
	v_mov_b64_e32 v[54:55], v[38:39]
	v_mov_b64_e32 v[52:53], v[36:37]
	v_mov_b64_e32 v[50:51], v[34:35]
	v_exp_f32_e32 v30, v30
	v_exp_f32_e32 v31, v31
	s_waitcnt lgkmcnt(2)
	v_mfma_f32_32x32x16_bf16 v[50:65], v[84:87], v[150:153], v[50:65]
	v_exp_f32_e32 v32, v32
	v_exp_f32_e32 v33, v33
	s_nop 0
	v_add_f32_e32 v0, 0, v18
	v_add_f32_e32 v0, v19, v0
	v_add_f32_e32 v0, v20, v0
	v_add_f32_e32 v0, v21, v0
	s_waitcnt lgkmcnt(1)
	v_mfma_f32_32x32x16_bf16 v[66:81], v[88:91], v[146:149], v[66:81]
	v_exp_f32_e32 v2, v96
	v_exp_f32_e32 v3, v97
	v_exp_f32_e32 v4, v98
	v_exp_f32_e32 v5, v99
	ds_read_b128 v[84:87], v173 offset:16384
	ds_read_b128 v[96:99], v173 offset:16896
	v_add_f32_e32 v0, v0, v22
	v_add_f32_e32 v0, v23, v0
	v_add_f32_e32 v0, v24, v0
	v_add_f32_e32 v0, v25, v0
	s_waitcnt lgkmcnt(2)
	v_mfma_f32_32x32x16_bf16 v[50:65], v[92:95], v[146:149], v[50:65]
	v_add_f32_e32 v0, v26, v0
	v_add_f32_e32 v0, v27, v0
	v_add_f32_e32 v0, v28, v0
	v_exp_f32_e32 v6, v6
	v_exp_f32_e32 v7, v7
	v_exp_f32_e32 v8, v8
	v_exp_f32_e32 v9, v9
	v_add_f32_e32 v0, v29, v0
	v_cvt_pk_bf16_f32 v114, v18, v19
	v_cvt_pk_bf16_f32 v115, v20, v21
	s_waitcnt lgkmcnt(1)
	v_mfma_f32_32x32x16_bf16 v[66:81], v[84:87], v[142:145], v[66:81]
	ds_read_b128 v[18:21], v173 offset:18432
	ds_read_b128 v[88:91], v173 offset:18944
	v_add_f32_e32 v0, v30, v0
	v_add_f32_e32 v0, v31, v0
	v_add_f32_e32 v0, v32, v0
	v_exp_f32_e32 v10, v10
	v_exp_f32_e32 v11, v11
	v_exp_f32_e32 v12, v12
	v_exp_f32_e32 v13, v13
	v_add_f32_e32 v0, v33, v0
	v_cvt_pk_bf16_f32 v116, v22, v23
	v_cvt_pk_bf16_f32 v117, v24, v25
	s_waitcnt lgkmcnt(2)
	v_mfma_f32_32x32x16_bf16 v[50:65], v[96:99], v[142:145], v[50:65]
	v_exp_f32_e32 v14, v14
	v_exp_f32_e32 v15, v15
	v_exp_f32_e32 v16, v16
	v_exp_f32_e32 v17, v17
	v_cvt_pk_bf16_f32 v118, v26, v27
	v_add_f32_e32 v0, v0, v2
	v_add_f32_e32 v0, v3, v0
	v_add_f32_e32 v0, v4, v0
	v_add_f32_e32 v0, v5, v0
	v_cvt_pk_bf16_f32 v119, v28, v29
	s_waitcnt lgkmcnt(1)
	v_mfma_f32_32x32x16_bf16 v[66:81], v[18:21], v[138:141], v[66:81]
	ds_read_b128 v[22:25], v173 offset:20480
	ds_read_b128 v[26:29], v173 offset:20992
	v_add_f32_e32 v0, v0, v6
	v_add_f32_e32 v0, v7, v0
	v_add_f32_e32 v0, v8, v0
	v_add_f32_e32 v0, v9, v0
	v_cvt_pk_bf16_f32 v120, v30, v31
	v_cvt_pk_bf16_f32 v121, v32, v33
	s_waitcnt lgkmcnt(2)
	v_mfma_f32_32x32x16_bf16 v[50:65], v[88:91], v[138:141], v[50:65]
	v_add_f32_e32 v0, v10, v0
	v_add_f32_e32 v0, v11, v0
	v_add_f32_e32 v0, v12, v0
	v_add_f32_e32 v0, v13, v0
	v_cvt_pk_bf16_f32 v122, v2, v3
	v_cvt_pk_bf16_f32 v123, v4, v5
	s_waitcnt lgkmcnt(1)
	v_mfma_f32_32x32x16_bf16 v[66:81], v[22:25], v[134:137], v[66:81]
	ds_read_b128 v[2:5], v173 offset:22528
	ds_read_b128 v[18:21], v173 offset:23040
	v_add_f32_e32 v0, v14, v0
	v_add_f32_e32 v0, v15, v0
	v_add_f32_e32 v0, v16, v0
	v_add_f32_e32 v0, v17, v0
	v_cvt_pk_bf16_f32 v124, v6, v7
	v_cvt_pk_bf16_f32 v125, v8, v9
	s_waitcnt lgkmcnt(2)
	v_mfma_f32_32x32x16_bf16 v[50:65], v[26:29], v[134:137], v[50:65]
	v_cvt_pk_bf16_f32 v126, v10, v11
	v_cvt_pk_bf16_f32 v127, v12, v13
	s_waitcnt lgkmcnt(1)
	v_mfma_f32_32x32x16_bf16 v[66:81], v[2:5], v[130:133], v[66:81]
	v_cvt_pk_bf16_f32 v128, v14, v15
	v_cvt_pk_bf16_f32 v129, v16, v17
	s_waitcnt lgkmcnt(0)
	v_mfma_f32_32x32x16_bf16 v[50:65], v[18:21], v[130:133], v[50:65]
	v_add_f32_e32 v175, 0, v0
	s_setprio 0
	v_max3_f32 v0, v66, v67, v50
	v_max3_f32 v2, v68, v69, v51
	s_nop 0
	v_max3_f32 v0, v0, v52, v53
	v_max3_f32 v2, v2, v72, v73
	s_nop 0
	v_max3_f32 v0, v0, v70, v71
	v_max3_f32 v2, v2, v56, v57
	s_nop 0
	v_max3_f32 v0, v0, v54, v55
	v_max3_f32 v2, v2, v76, v77
	s_nop 0
	v_max3_f32 v0, v0, v74, v75
	v_max3_f32 v2, v2, v60, v61
	s_nop 0
	v_max3_f32 v0, v0, v58, v59
	v_max3_f32 v2, v2, v80, v81
	s_nop 0
	v_max3_f32 v0, v0, v78, v79
	v_max3_f32 v2, v2, v64, v65
	s_nop 0
	v_max3_f32 v0, v0, v62, v63
	v_max_f32_e32 v2, v2, v2
	v_max_f32_e32 v0, v0, v0
	v_max_f32_e32 v0, v0, v2
	v_mov_b32_e32 v2, v0
	s_nop 1
	v_permlane32_swap_b32_e32 v0, v2
	v_max_f32_e32 v2, v2, v2
	v_max_f32_e32 v0, v0, v0
	v_max_f32_e32 v0, v0, v2
	v_cmp_lt_f32_e32 vcc, s54, v0
	s_cmp_lg_u64 vcc, 0
	s_cselect_b64 s[42:43], -1, 0
	s_cbranch_vccnz .LBB0_1205

.LBB0_1107:
	v_lshl_add_u64 v[164:165], v[160:161], 0, s[0:1]
	s_mul_i32 s77, s81, 0x3000
	v_lshl_add_u64 v[82:83], v[164:165], 0, s[12:13]
	s_add_i32 s78, s77, s76
	s_mov_b32 m0, s78
	s_nop 0
	global_load_lds_dwordx4 v[82:83], off
	s_and_saveexec_b64 s[42:43], s[2:3]
	s_cbranch_execz .LBB0_1109
	s_add_i32 s44, s77, s71
	v_lshl_add_u64 v[82:83], v[162:163], 0, s[30:31]
	s_mov_b32 m0, s44
	s_nop 0
	global_load_lds_dwordx4 v[82:83], off
.LBB0_1109:
	s_or_b64 exec, exec, s[42:43]
	s_add_i32 s42, s82, 0xffffe000
	s_and_b32 s70, s42, 0x6000
	v_lshl_add_u64 v[166:167], v[156:157], 0, s[0:1]
	s_add_i32 s73, s70, s72
	s_mov_b32 m0, s73
	s_nop 0
	global_load_lds_dwordx4 v[166:167], off
	s_mul_i32 s86, s83, 0x3000
	v_add_u32_e32 v185, s86, v173
	s_setprio 1
	ds_read_b128 v[82:85], v185
	ds_read_b128 v[176:179], v185 offset:512
	v_exp_f32_e32 v66, v66
	v_exp_f32_e32 v67, v67
	v_exp_f32_e32 v68, v68
	v_exp_f32_e32 v69, v69
	s_nop 0
	v_exp_f32_e32 v70, v70
	v_exp_f32_e32 v71, v71
	v_exp_f32_e32 v72, v72
	v_exp_f32_e32 v73, v73
	s_waitcnt lgkmcnt(1)
	v_mfma_f32_32x32x16_bf16 v[98:113], v[82:85], v[150:153], v[34:49]
	ds_read_b128 v[186:189], v185 offset:2048
	ds_read_b128 v[190:193], v185 offset:2560
	v_exp_f32_e32 v74, v74
	v_exp_f32_e32 v75, v75
	v_exp_f32_e32 v76, v76
	v_exp_f32_e32 v77, v77
	s_waitcnt lgkmcnt(2)
	v_mfma_f32_32x32x16_bf16 v[82:97], v[176:179], v[150:153], v[34:49]
	v_exp_f32_e32 v78, v78
	v_exp_f32_e32 v79, v79
	v_exp_f32_e32 v80, v80
	v_exp_f32_e32 v81, v81
	s_nop 0
	v_add_f32_e32 v0, 0, v66
	v_add_f32_e32 v0, v67, v0
	v_add_f32_e32 v0, v68, v0
	v_add_f32_e32 v0, v69, v0
	s_waitcnt lgkmcnt(1)
	v_mfma_f32_32x32x16_bf16 v[98:113], v[186:189], v[146:149], v[98:113]
	ds_read_b128 v[176:179], v185 offset:4096
	ds_read_b128 v[194:197], v185 offset:4608
	v_add_f32_e32 v0, v0, v70
	v_add_f32_e32 v0, v71, v0
	v_add_f32_e32 v0, v72, v0
	v_exp_f32_e32 v50, v50
	v_exp_f32_e32 v51, v51
	v_exp_f32_e32 v52, v52
	v_exp_f32_e32 v53, v53
	v_add_f32_e32 v0, v73, v0
	s_waitcnt lgkmcnt(2)
	v_mfma_f32_32x32x16_bf16 v[82:97], v[190:193], v[146:149], v[82:97]
	v_add_f32_e32 v0, v74, v0
	v_add_f32_e32 v0, v75, v0
	v_add_f32_e32 v0, v76, v0
	v_exp_f32_e32 v54, v54
	v_exp_f32_e32 v55, v55
	v_exp_f32_e32 v56, v56
	v_exp_f32_e32 v57, v57
	v_add_f32_e32 v0, v77, v0
	v_cvt_pk_bf16_f32 v114, v66, v67
	v_cvt_pk_bf16_f32 v115, v68, v69
	s_waitcnt lgkmcnt(1)
	v_mfma_f32_32x32x16_bf16 v[98:113], v[176:179], v[142:145], v[98:113]
	ds_read_b128 v[66:69], v185 offset:6144
	ds_read_b128 v[186:189], v185 offset:6656
	v_add_f32_e32 v0, v78, v0
	v_add_f32_e32 v0, v79, v0
	v_add_f32_e32 v0, v80, v0
	v_exp_f32_e32 v58, v58
	v_exp_f32_e32 v59, v59
	v_exp_f32_e32 v60, v60
	v_exp_f32_e32 v61, v61
	v_add_f32_e32 v0, v81, v0
	v_cvt_pk_bf16_f32 v116, v70, v71
	v_cvt_pk_bf16_f32 v117, v72, v73
	s_waitcnt lgkmcnt(2)
	v_mfma_f32_32x32x16_bf16 v[82:97], v[194:197], v[142:145], v[82:97]
	v_exp_f32_e32 v62, v62
	v_exp_f32_e32 v63, v63
	v_exp_f32_e32 v64, v64
	v_exp_f32_e32 v65, v65
	v_cvt_pk_bf16_f32 v118, v74, v75
	v_add_f32_e32 v0, v0, v50
	v_add_f32_e32 v0, v51, v0
	v_add_f32_e32 v0, v52, v0
	v_add_f32_e32 v0, v53, v0
	v_cvt_pk_bf16_f32 v119, v76, v77
	s_waitcnt lgkmcnt(1)
	v_mfma_f32_32x32x16_bf16 v[98:113], v[66:69], v[138:141], v[98:113]
	ds_read_b128 v[70:73], v185 offset:8192
	ds_read_b128 v[74:77], v185 offset:8704
	v_add_f32_e32 v0, v0, v54
	v_add_f32_e32 v0, v55, v0
	v_add_f32_e32 v0, v56, v0
	v_add_f32_e32 v0, v57, v0
	v_cvt_pk_bf16_f32 v120, v78, v79
	v_cvt_pk_bf16_f32 v121, v80, v81
	s_waitcnt lgkmcnt(2)
	v_mfma_f32_32x32x16_bf16 v[82:97], v[186:189], v[138:141], v[82:97]
	v_add_f32_e32 v0, v58, v0
	v_add_f32_e32 v0, v59, v0
	v_add_f32_e32 v0, v60, v0
	v_add_f32_e32 v0, v61, v0
	v_cvt_pk_bf16_f32 v122, v50, v51
	v_cvt_pk_bf16_f32 v123, v52, v53
	s_waitcnt lgkmcnt(1)
	v_mfma_f32_32x32x16_bf16 v[98:113], v[70:73], v[134:137], v[98:113]
	ds_read_b128 v[50:53], v185 offset:10240
	ds_read_b128 v[66:69], v185 offset:10752
	v_add_f32_e32 v0, v62, v0
	v_add_f32_e32 v0, v63, v0
	v_add_f32_e32 v0, v64, v0
	v_add_f32_e32 v0, v65, v0
	v_cvt_pk_bf16_f32 v124, v54, v55
	v_cvt_pk_bf16_f32 v125, v56, v57
	s_waitcnt lgkmcnt(2)
	v_mfma_f32_32x32x16_bf16 v[82:97], v[74:77], v[134:137], v[82:97]
	v_cvt_pk_bf16_f32 v126, v58, v59
	v_cvt_pk_bf16_f32 v127, v60, v61
	s_waitcnt lgkmcnt(1)
	v_mfma_f32_32x32x16_bf16 v[98:113], v[50:53], v[130:133], v[98:113]
	v_cvt_pk_bf16_f32 v128, v62, v63
	v_cvt_pk_bf16_f32 v129, v64, v65
	s_waitcnt lgkmcnt(0)
	v_mfma_f32_32x32x16_bf16 v[82:97], v[66:69], v[130:133], v[82:97]
	v_add_f32_e32 v0, v175, v0
	s_setprio 0
	v_max3_f32 v50, v98, v99, v82
	v_max3_f32 v51, v100, v101, v83
	s_nop 0
	v_max3_f32 v50, v50, v84, v85
	v_max3_f32 v51, v51, v104, v105
	s_nop 0
	v_max3_f32 v50, v50, v102, v103
	v_max3_f32 v51, v51, v88, v89
	s_nop 0
	v_max3_f32 v50, v50, v86, v87
	v_max3_f32 v51, v51, v108, v109
	s_nop 0
	v_max3_f32 v50, v50, v106, v107
	v_max3_f32 v51, v51, v92, v93
	s_nop 0
	v_max3_f32 v50, v50, v90, v91
	v_max3_f32 v51, v51, v112, v113
	s_nop 0
	v_max3_f32 v50, v50, v110, v111
	v_max3_f32 v51, v51, v96, v97
	s_nop 0
	v_max3_f32 v50, v50, v94, v95
	v_max_f32_e32 v51, v51, v51
	v_max_f32_e32 v50, v50, v50
	v_max_f32_e32 v50, v50, v51
	v_mov_b32_e32 v51, v50
	s_nop 1
	v_permlane32_swap_b32_e32 v50, v51
	v_max_f32_e32 v51, v51, v51
	v_max_f32_e32 v50, v50, v50
	v_max_f32_e32 v50, v50, v51
	v_cmp_lt_f32_e32 vcc, s54, v50
	s_cmp_lg_u64 vcc, 0
	s_cselect_b64 s[42:43], -1, 0
	s_cbranch_vccnz .LBB0_1117

.LBB0_1112:
	v_lshl_add_u64 v[50:51], v[164:165], 0, s[18:19]
	s_add_i32 s42, s86, s76
	s_mov_b32 m0, s42
	s_nop 0
	global_load_lds_dwordx4 v[50:51], off
	s_and_saveexec_b64 s[42:43], s[2:3]
	s_cbranch_execz .LBB0_1114
	s_add_i32 s44, s86, s71
	s_mov_b32 m0, s44
	s_nop 0
	global_load_lds_dwordx4 v[162:163], off
.LBB0_1114:
	s_or_b64 exec, exec, s[42:43]
	v_lshl_add_u64 v[50:51], v[166:167], 0, s[12:13]
	s_add_i32 s42, s84, s72
	s_mov_b32 m0, s42
	s_nop 0
	global_load_lds_dwordx4 v[50:51], off
	s_mul_i32 s86, s10, 0x3000
	v_add_u32_e32 v184, s86, v173
	s_setprio 1
	ds_read_b128 v[50:53], v184
	ds_read_b128 v[164:167], v184 offset:512
	v_exp_f32_e32 v98, v98
	v_exp_f32_e32 v99, v99
	v_exp_f32_e32 v100, v100
	v_exp_f32_e32 v101, v101
	s_nop 0
	v_exp_f32_e32 v102, v102
	v_exp_f32_e32 v103, v103
	v_exp_f32_e32 v104, v104
	v_exp_f32_e32 v105, v105
	s_waitcnt lgkmcnt(1)
	v_mfma_f32_32x32x16_bf16 v[66:81], v[50:53], v[150:153], v[34:49]
	ds_read_b128 v[176:179], v184 offset:2048
	ds_read_b128 v[186:189], v184 offset:2560
	v_exp_f32_e32 v106, v106
	v_exp_f32_e32 v107, v107
	v_exp_f32_e32 v108, v108
	v_exp_f32_e32 v109, v109
	s_waitcnt lgkmcnt(2)
	v_mfma_f32_32x32x16_bf16 v[50:65], v[164:167], v[150:153], v[34:49]
	v_exp_f32_e32 v110, v110
	v_exp_f32_e32 v111, v111
	v_exp_f32_e32 v112, v112
	v_exp_f32_e32 v113, v113
	s_nop 0
	v_add_f32_e32 v114, 0, v98
	v_add_f32_e32 v114, v99, v114
	v_add_f32_e32 v114, v100, v114
	v_add_f32_e32 v114, v101, v114
	s_waitcnt lgkmcnt(1)
	v_mfma_f32_32x32x16_bf16 v[66:81], v[176:179], v[146:149], v[66:81]
	ds_read_b128 v[164:167], v184 offset:4096
	ds_read_b128 v[190:193], v184 offset:4608
	v_add_f32_e32 v114, v114, v102
	v_add_f32_e32 v114, v103, v114
	v_add_f32_e32 v114, v104, v114
	v_exp_f32_e32 v82, v82
	v_exp_f32_e32 v83, v83
	v_exp_f32_e32 v84, v84
	v_exp_f32_e32 v85, v85
	v_add_f32_e32 v114, v105, v114
	s_waitcnt lgkmcnt(2)
	v_mfma_f32_32x32x16_bf16 v[50:65], v[186:189], v[146:149], v[50:65]
	v_add_f32_e32 v114, v106, v114
	v_add_f32_e32 v114, v107, v114
	v_add_f32_e32 v114, v108, v114
	v_exp_f32_e32 v86, v86
	v_exp_f32_e32 v87, v87
	v_exp_f32_e32 v88, v88
	v_exp_f32_e32 v89, v89
	v_add_f32_e32 v118, v109, v114
	v_cvt_pk_bf16_f32 v114, v98, v99
	v_cvt_pk_bf16_f32 v115, v100, v101
	s_waitcnt lgkmcnt(1)
	v_mfma_f32_32x32x16_bf16 v[66:81], v[164:167], v[142:145], v[66:81]
	ds_read_b128 v[98:101], v184 offset:6144
	ds_read_b128 v[176:179], v184 offset:6656
	v_add_f32_e32 v116, v110, v118
	v_add_f32_e32 v116, v111, v116
	v_add_f32_e32 v116, v112, v116
	v_exp_f32_e32 v90, v90
	v_exp_f32_e32 v91, v91
	v_exp_f32_e32 v92, v92
	v_exp_f32_e32 v93, v93
	v_add_f32_e32 v118, v113, v116
	v_cvt_pk_bf16_f32 v116, v102, v103
	v_cvt_pk_bf16_f32 v117, v104, v105
	s_waitcnt lgkmcnt(2)
	v_mfma_f32_32x32x16_bf16 v[50:65], v[190:193], v[142:145], v[50:65]
	v_exp_f32_e32 v94, v94
	v_exp_f32_e32 v95, v95
	v_exp_f32_e32 v96, v96
	v_exp_f32_e32 v97, v97
	v_cvt_pk_bf16_f32 v119, v108, v109
	v_add_f32_e32 v102, v118, v82
	v_add_f32_e32 v102, v83, v102
	v_add_f32_e32 v102, v84, v102
	v_add_f32_e32 v122, v85, v102
	v_cvt_pk_bf16_f32 v118, v106, v107
	s_waitcnt lgkmcnt(1)
	v_mfma_f32_32x32x16_bf16 v[66:81], v[98:101], v[138:141], v[66:81]
	ds_read_b128 v[102:105], v184 offset:8192
	ds_read_b128 v[106:109], v184 offset:8704
	v_add_f32_e32 v120, v122, v86
	v_add_f32_e32 v120, v87, v120
	v_add_f32_e32 v120, v88, v120
	v_add_f32_e32 v122, v89, v120
	v_cvt_pk_bf16_f32 v120, v110, v111
	v_cvt_pk_bf16_f32 v121, v112, v113
	s_waitcnt lgkmcnt(2)
	v_mfma_f32_32x32x16_bf16 v[50:65], v[176:179], v[138:141], v[50:65]
	v_add_f32_e32 v98, v90, v122
	v_add_f32_e32 v98, v91, v98
	v_add_f32_e32 v98, v92, v98
	v_add_f32_e32 v110, v93, v98
	v_cvt_pk_bf16_f32 v122, v82, v83
	v_cvt_pk_bf16_f32 v123, v84, v85
	s_waitcnt lgkmcnt(1)
	v_mfma_f32_32x32x16_bf16 v[66:81], v[102:105], v[134:137], v[66:81]
	ds_read_b128 v[82:85], v184 offset:10240
	ds_read_b128 v[98:101], v184 offset:10752
	v_add_f32_e32 v110, v94, v110
	v_add_f32_e32 v110, v95, v110
	v_add_f32_e32 v110, v96, v110
	v_add_f32_e32 v110, v97, v110
	v_cvt_pk_bf16_f32 v124, v86, v87
	v_cvt_pk_bf16_f32 v125, v88, v89
	s_waitcnt lgkmcnt(2)
	v_mfma_f32_32x32x16_bf16 v[50:65], v[106:109], v[134:137], v[50:65]
	v_cvt_pk_bf16_f32 v126, v90, v91
	v_cvt_pk_bf16_f32 v127, v92, v93
	s_waitcnt lgkmcnt(1)
	v_mfma_f32_32x32x16_bf16 v[66:81], v[82:85], v[130:133], v[66:81]
	v_cvt_pk_bf16_f32 v128, v94, v95
	v_cvt_pk_bf16_f32 v129, v96, v97
	s_waitcnt lgkmcnt(0)
	v_mfma_f32_32x32x16_bf16 v[50:65], v[98:101], v[130:133], v[50:65]
	v_add_f32_e32 v175, v0, v110
	s_setprio 0
	v_max3_f32 v0, v66, v67, v50
	v_max3_f32 v82, v68, v69, v51
	s_nop 0
	v_max3_f32 v0, v0, v52, v53
	v_max3_f32 v82, v82, v72, v73
	s_nop 0
	v_max3_f32 v0, v0, v70, v71
	v_max3_f32 v82, v82, v56, v57
	s_nop 0
	v_max3_f32 v0, v0, v54, v55
	v_max3_f32 v82, v82, v76, v77
	s_nop 0
	v_max3_f32 v0, v0, v74, v75
	v_max3_f32 v82, v82, v60, v61
	s_nop 0
	v_max3_f32 v0, v0, v58, v59
	v_max3_f32 v82, v82, v80, v81
	s_nop 0
	v_max3_f32 v0, v0, v78, v79
	v_max3_f32 v82, v82, v64, v65
	s_nop 0
	v_max3_f32 v0, v0, v62, v63
	v_max_f32_e32 v82, v82, v82
	v_max_f32_e32 v0, v0, v0
	v_max_f32_e32 v0, v0, v82
	v_mov_b32_e32 v82, v0
	s_nop 1
	v_permlane32_swap_b32_e32 v0, v82
	v_max_f32_e32 v82, v82, v82
	v_max_f32_e32 v0, v0, v0
	v_max_f32_e32 v0, v0, v82
	v_cmp_lt_f32_e32 vcc, s54, v0
	s_cmp_lg_u64 vcc, 0
	s_cselect_b64 s[42:43], -1, 0
	s_cbranch_vccnz .LBB0_1120

.LBB0_1126:
	s_lshl_b64 s[42:43], s[10:11], 17
	v_lshl_add_u64 v[82:83], v[160:161], 0, s[42:43]
	s_add_i32 s44, s86, s76
	s_mov_b32 m0, s44
	s_nop 0
	global_load_lds_dwordx4 v[82:83], off
	s_and_saveexec_b64 s[44:45], s[2:3]
	s_cbranch_execz .LBB0_1128
	s_lshl_b64 s[80:81], s[10:11], 12
	s_add_i32 s76, s86, s71
	v_lshl_add_u64 v[82:83], v[158:159], 0, s[80:81]
	s_mov_b32 m0, s76
	s_nop 0
	global_load_lds_dwordx4 v[82:83], off
.LBB0_1128:
	s_or_b64 exec, exec, s[44:45]
	v_lshl_add_u64 v[82:83], v[156:157], 0, s[0:1]
	s_add_i32 s0, s85, s72
	s_mov_b32 m0, s0
	s_nop 0
	global_load_lds_dwordx4 v[82:83], off
	v_or_b32_e32 v182, s75, v169
	v_add_u32_e32 v183, s77, v173
	s_setprio 1
	ds_read_b128 v[98:101], v183
	ds_read_b128 v[162:165], v183 offset:512
	v_exp_f32_e32 v66, v66
	v_exp_f32_e32 v67, v67
	v_exp_f32_e32 v68, v68
	v_exp_f32_e32 v69, v69
	s_nop 0
	v_exp_f32_e32 v70, v70
	v_exp_f32_e32 v71, v71
	v_exp_f32_e32 v72, v72
	v_exp_f32_e32 v73, v73
	s_waitcnt lgkmcnt(1)
	v_mfma_f32_32x32x16_bf16 v[82:97], v[98:101], v[150:153], v[34:49]
	ds_read_b128 v[176:179], v183 offset:2048
	ds_read_b128 v[186:189], v183 offset:2560
	v_exp_f32_e32 v74, v74
	v_exp_f32_e32 v75, v75
	v_exp_f32_e32 v76, v76
	v_exp_f32_e32 v77, v77
	s_nop 0
	v_exp_f32_e32 v78, v78
	v_exp_f32_e32 v79, v79
	v_exp_f32_e32 v80, v80
	v_exp_f32_e32 v81, v81
	s_waitcnt lgkmcnt(2)
	v_mfma_f32_32x32x16_bf16 v[98:113], v[162:165], v[150:153], v[34:49]
	v_add_f32_e32 v0, 0, v66
	v_add_f32_e32 v0, v67, v0
	v_add_f32_e32 v0, v68, v0
	v_add_f32_e32 v0, v69, v0
	s_waitcnt lgkmcnt(1)
	v_mfma_f32_32x32x16_bf16 v[82:97], v[176:179], v[146:149], v[82:97]
	ds_read_b128 v[162:165], v183 offset:4096
	ds_read_b128 v[190:193], v183 offset:4608
	v_add_f32_e32 v0, v0, v70
	v_add_f32_e32 v0, v71, v0
	v_add_f32_e32 v0, v72, v0
	v_exp_f32_e32 v50, v50
	v_exp_f32_e32 v51, v51
	v_exp_f32_e32 v52, v52
	v_exp_f32_e32 v53, v53
	v_add_f32_e32 v0, v73, v0
	s_nop 0
	v_add_f32_e32 v0, v74, v0
	v_add_f32_e32 v0, v75, v0
	v_add_f32_e32 v0, v76, v0
	v_exp_f32_e32 v54, v54
	v_exp_f32_e32 v55, v55
	v_exp_f32_e32 v56, v56
	v_exp_f32_e32 v57, v57
	v_add_f32_e32 v0, v77, v0
	v_cvt_pk_bf16_f32 v114, v66, v67
	v_cvt_pk_bf16_f32 v115, v68, v69
	s_waitcnt lgkmcnt(2)
	v_mfma_f32_32x32x16_bf16 v[98:113], v[186:189], v[146:149], v[98:113]
	s_waitcnt lgkmcnt(1)
	v_mfma_f32_32x32x16_bf16 v[82:97], v[162:165], v[142:145], v[82:97]
	ds_read_b128 v[66:69], v183 offset:6144
	ds_read_b128 v[176:179], v183 offset:6656
	v_add_f32_e32 v0, v78, v0
	v_add_f32_e32 v0, v79, v0
	v_add_f32_e32 v0, v80, v0
	v_exp_f32_e32 v58, v58
	v_exp_f32_e32 v59, v59
	v_exp_f32_e32 v60, v60
	v_exp_f32_e32 v61, v61
	v_add_f32_e32 v0, v81, v0
	v_cvt_pk_bf16_f32 v116, v70, v71
	v_cvt_pk_bf16_f32 v117, v72, v73
	s_nop 0
	v_exp_f32_e32 v62, v62
	v_exp_f32_e32 v63, v63
	v_exp_f32_e32 v64, v64
	v_exp_f32_e32 v65, v65
	v_cvt_pk_bf16_f32 v118, v74, v75
	v_add_f32_e32 v0, v0, v50
	v_add_f32_e32 v0, v51, v0
	v_add_f32_e32 v0, v52, v0
	v_add_f32_e32 v0, v53, v0
	v_cvt_pk_bf16_f32 v119, v76, v77
	s_waitcnt lgkmcnt(2)
	v_mfma_f32_32x32x16_bf16 v[98:113], v[190:193], v[142:145], v[98:113]
	s_waitcnt lgkmcnt(1)
	v_mfma_f32_32x32x16_bf16 v[82:97], v[66:69], v[138:141], v[82:97]
	ds_read_b128 v[70:73], v183 offset:8192
	ds_read_b128 v[74:77], v183 offset:8704
	v_add_f32_e32 v0, v0, v54
	v_add_f32_e32 v0, v55, v0
	v_add_f32_e32 v0, v56, v0
	v_add_f32_e32 v0, v57, v0
	v_cvt_pk_bf16_f32 v120, v78, v79
	v_cvt_pk_bf16_f32 v121, v80, v81
	s_nop 0
	v_add_f32_e32 v0, v58, v0
	v_add_f32_e32 v0, v59, v0
	v_add_f32_e32 v0, v60, v0
	v_add_f32_e32 v0, v61, v0
	v_cvt_pk_bf16_f32 v122, v50, v51
	v_cvt_pk_bf16_f32 v123, v52, v53
	s_waitcnt lgkmcnt(2)
	v_mfma_f32_32x32x16_bf16 v[98:113], v[176:179], v[138:141], v[98:113]
	s_waitcnt lgkmcnt(1)
	v_mfma_f32_32x32x16_bf16 v[82:97], v[70:73], v[134:137], v[82:97]
	ds_read_b128 v[50:53], v183 offset:10240
	ds_read_b128 v[66:69], v183 offset:10752
	v_add_f32_e32 v0, v62, v0
	v_add_f32_e32 v0, v63, v0
	v_add_f32_e32 v0, v64, v0
	v_add_f32_e32 v0, v65, v0
	v_cvt_pk_bf16_f32 v124, v54, v55
	v_cvt_pk_bf16_f32 v125, v56, v57
	v_cvt_pk_bf16_f32 v126, v58, v59
	v_cvt_pk_bf16_f32 v127, v60, v61
	s_waitcnt lgkmcnt(2)
	v_mfma_f32_32x32x16_bf16 v[98:113], v[74:77], v[134:137], v[98:113]
	s_waitcnt lgkmcnt(1)
	v_mfma_f32_32x32x16_bf16 v[82:97], v[50:53], v[130:133], v[82:97]
	v_cvt_pk_bf16_f32 v128, v62, v63
	v_cvt_pk_bf16_f32 v129, v64, v65
	s_waitcnt lgkmcnt(0)
; __device__ __forceinline__ float max3f(float a, float b, float c) { float r; asm("v_max3_f32 %0, %1, %2, %3" : "=v"(r) : "v"(a), "v"(b), "v"(c)); return r; }
; __device__ __forceinline__ void cmask(f32x16& p0, f32x16& p1, int jb, int qrel, int hi) {
;     const float NEG = -INFINITY; const int kb = 64 * jb + 4 * hi;
; #pragma unroll
;     for (int r = 0; r < 16; ++r) { const int kv = kb + (r & 3) + 8 * (r >> 2); if (kv > qrel) p0[r] = NEG; if (kv + 32 > qrel) p1[r] = NEG; }
; }
; __device__ __forceinline__ float rowmax(const f32x16& p0, const f32x16& p1) {
;     float a = max3f(p0[0], p0[1], p1[0]), b = max3f(p0[2], p0[3], p1[1]); a = max3f(a, p1[2], p1[3]);
; #pragma unroll
;     for (int r = 4; r < 16; r += 4) { a = max3f(a, p0[r], p0[r + 1]); b = max3f(b, p0[r + 2], p0[r + 3]); a = max3f(a, p1[r], p1[r + 1]); b = max3f(b, p1[r + 2], p1[r + 3]); }
;     const float m = fmaxf(a, b);
;     auto rr = __builtin_amdgcn_permlane32_swap(__float_as_uint(m), __float_as_uint(m), false, false);
;     return fmaxf(__uint_as_float(rr[0]), __uint_as_float(rr[1]));
; }
	v_mfma_f32_32x32x16_bf16 v[98:113], v[66:69], v[130:133], v[98:113]
	v_add_f32_e32 v187, v175, v0
	s_setprio 0
	v_lshlrev_b32_e32 v186, 2, v170
	v_or_b32_e32 v0, 32, v186
	v_cmp_le_i32_e32 vcc, v0, v182
	v_or_b32_e32 v0, 33, v186
	v_or_b32_e32 v179, 2, v186
	s_nop 4
	v_cndmask_b32_e32 v50, v206, v98, vcc
	v_cmp_lt_i32_e32 vcc, v186, v182
	v_or_b32_e32 v178, 3, v186
	v_or_b32_e32 v177, 8, v186
	v_cndmask_b32_e32 v67, v206, v83, vcc
	v_cmp_le_i32_e32 vcc, v186, v182
	v_or_b32_e32 v176, 9, v186
	v_or_b32_e32 v175, 10, v186
	v_cndmask_b32_e32 v66, v206, v82, vcc
	v_cmp_le_i32_e32 vcc, v0, v182
	v_or_b32_e32 v0, 34, v186
	v_or_b32_e32 v174, 11, v186
	v_cndmask_b32_e32 v51, v206, v99, vcc
	v_cmp_le_i32_e32 vcc, v179, v182
	v_or_b32_e32 v173, 16, v186
	v_or_b32_e32 v167, 17, v186
	v_cndmask_b32_e32 v68, v206, v84, vcc
	v_cmp_le_i32_e32 vcc, v0, v182
	v_or_b32_e32 v0, 35, v186
	v_or_b32_e32 v166, 18, v186
	v_cndmask_b32_e32 v52, v206, v100, vcc
	v_cmp_le_i32_e32 vcc, v178, v182
	v_or_b32_e32 v165, 19, v186
	v_or_b32_e32 v164, 24, v186
	v_cndmask_b32_e32 v69, v206, v85, vcc
	v_cmp_le_i32_e32 vcc, v0, v182
	v_or_b32_e32 v0, 40, v186
	v_or_b32_e32 v163, 25, v186
	v_cndmask_b32_e32 v53, v206, v101, vcc
	v_cmp_le_i32_e32 vcc, v177, v182
	v_max3_f32 v82, v66, v67, v50
	v_max3_f32 v83, v68, v69, v51
	v_or_b32_e32 v162, 26, v186
	v_max3_f32 v82, v82, v52, v53
	v_or_b32_e32 v65, 59, v186
	v_cndmask_b32_e32 v70, v206, v86, vcc
	v_cmp_le_i32_e32 vcc, v0, v182
	v_or_b32_e32 v0, 41, v186
	s_nop 0
	v_cndmask_b32_e32 v54, v206, v102, vcc
	v_cmp_le_i32_e32 vcc, v176, v182
	s_nop 1
	v_cndmask_b32_e32 v71, v206, v87, vcc
	v_cmp_le_i32_e32 vcc, v0, v182
	v_or_b32_e32 v0, 42, v186
	v_max3_f32 v82, v82, v70, v71
	s_nop 0
	v_cndmask_b32_e32 v55, v206, v103, vcc
	v_cmp_le_i32_e32 vcc, v175, v182
	v_max3_f32 v82, v82, v54, v55
	s_nop 1
	v_cndmask_b32_e32 v72, v206, v88, vcc
	v_cmp_le_i32_e32 vcc, v0, v182
	v_or_b32_e32 v0, 43, v186
	s_nop 0
	v_cndmask_b32_e32 v56, v206, v104, vcc
	v_cmp_le_i32_e32 vcc, v174, v182
	s_nop 1
	v_cndmask_b32_e32 v73, v206, v89, vcc
	v_cmp_le_i32_e32 vcc, v0, v182
	v_or_b32_e32 v0, 48, v186
	v_max3_f32 v83, v83, v72, v73
	s_nop 0
	v_cndmask_b32_e32 v57, v206, v105, vcc
	v_cmp_le_i32_e32 vcc, v173, v182
	v_max3_f32 v83, v83, v56, v57
	s_nop 1
	v_cndmask_b32_e32 v74, v206, v90, vcc
	v_cmp_le_i32_e32 vcc, v0, v182
	v_or_b32_e32 v0, 49, v186
	s_nop 0
	v_cndmask_b32_e32 v58, v206, v106, vcc
	v_cmp_le_i32_e32 vcc, v167, v182
	s_nop 1
	v_cndmask_b32_e32 v75, v206, v91, vcc
	v_cmp_le_i32_e32 vcc, v0, v182
	v_or_b32_e32 v0, 50, v186
	v_max3_f32 v82, v82, v74, v75
	s_nop 0
	v_cndmask_b32_e32 v59, v206, v107, vcc
	v_cmp_le_i32_e32 vcc, v166, v182
	v_max3_f32 v82, v82, v58, v59
	s_nop 1
	v_cndmask_b32_e32 v76, v206, v92, vcc
	v_cmp_le_i32_e32 vcc, v0, v182
	v_or_b32_e32 v0, 51, v186
	s_nop 0
	v_cndmask_b32_e32 v60, v206, v108, vcc
	v_cmp_le_i32_e32 vcc, v165, v182
	s_nop 1
	v_cndmask_b32_e32 v77, v206, v93, vcc
	v_cmp_le_i32_e32 vcc, v0, v182
	v_or_b32_e32 v0, 56, v186
	v_max3_f32 v83, v83, v76, v77
	s_nop 0
	v_cndmask_b32_e32 v61, v206, v109, vcc
	v_cmp_le_i32_e32 vcc, v164, v182
	v_max3_f32 v83, v83, v60, v61
	s_nop 1
	v_cndmask_b32_e32 v78, v206, v94, vcc
	v_cmp_le_i32_e32 vcc, v0, v182
	v_or_b32_e32 v0, 57, v186
	s_nop 0
	v_cndmask_b32_e32 v62, v206, v110, vcc
	v_cmp_le_i32_e32 vcc, v163, v182
	s_nop 1
	v_cndmask_b32_e32 v79, v206, v95, vcc
	v_cmp_le_i32_e32 vcc, v0, v182
	v_or_b32_e32 v0, 58, v186
	v_max3_f32 v82, v82, v78, v79
	s_nop 0
	v_cndmask_b32_e32 v63, v206, v111, vcc
	v_cmp_le_i32_e32 vcc, v162, v182
	v_max3_f32 v82, v82, v62, v63
	s_nop 0
	v_max_f32_e32 v82, v82, v82
	v_cndmask_b32_e32 v80, v206, v96, vcc
	v_cmp_le_i32_e32 vcc, v0, v182
	v_or_b32_e32 v0, 27, v186
	s_nop 0
	v_cndmask_b32_e32 v64, v206, v112, vcc
	v_cmp_le_i32_e32 vcc, v0, v182
	s_nop 1
	v_cndmask_b32_e32 v81, v206, v97, vcc
	v_cmp_le_i32_e32 vcc, v65, v182
	v_max3_f32 v83, v83, v80, v81
	s_nop 1
	v_cndmask_b32_e32 v65, v206, v113, vcc
	v_max3_f32 v83, v83, v64, v65
	s_nop 0
	v_max_f32_e32 v83, v83, v83
	v_max_f32_e32 v82, v82, v83
	v_mov_b32_e32 v83, v82
	s_nop 1
	v_permlane32_swap_b32_e32 v82, v83
	v_max_f32_e32 v83, v83, v83
	v_max_f32_e32 v82, v82, v82
	v_max_f32_e32 v82, v82, v83
	v_cmp_lt_f32_e32 vcc, s54, v82
	s_cmp_lg_u64 vcc, 0
	s_cselect_b64 s[0:1], -1, 0
	s_cbranch_vccnz .LBB0_1208

.LBB0_1131:
	s_add_i32 s10, s84, 6
	s_lshl_b64 s[0:1], s[10:11], 17
	v_lshl_add_u64 v[82:83], v[160:161], 0, s[0:1]
	s_mov_b32 m0, s78
	s_nop 0
	global_load_lds_dwordx4 v[82:83], off
	s_and_saveexec_b64 s[44:45], s[2:3]
	s_cbranch_execz .LBB0_1133
	s_lshl_b64 s[74:75], s[10:11], 12
	s_add_i32 s71, s77, s71
	v_lshl_add_u64 v[82:83], v[158:159], 0, s[74:75]
	s_mov_b32 m0, s71
	s_nop 0
	global_load_lds_dwordx4 v[82:83], off
.LBB0_1133:
	s_or_b64 exec, exec, s[44:45]
	v_lshl_add_u64 v[82:83], v[156:157], 0, s[42:43]
	s_add_i32 s10, s79, s72
	s_mov_b32 m0, s10
	s_nop 0
	global_load_lds_dwordx4 v[82:83], off
	s_setprio 1
	ds_read_b128 v[98:101], v185
	ds_read_b128 v[158:161], v185 offset:512
	v_exp_f32_e32 v66, v66
	v_exp_f32_e32 v67, v67
	v_exp_f32_e32 v68, v68
	v_exp_f32_e32 v69, v69
	s_nop 0
	v_exp_f32_e32 v70, v70
	v_exp_f32_e32 v71, v71
	v_exp_f32_e32 v72, v72
	v_exp_f32_e32 v73, v73
	s_waitcnt lgkmcnt(1)
	v_mfma_f32_32x32x16_bf16 v[82:97], v[98:101], v[150:153], v[34:49]
	ds_read_b128 v[188:191], v185 offset:2048
	ds_read_b128 v[192:195], v185 offset:2560
	v_exp_f32_e32 v74, v74
	v_exp_f32_e32 v75, v75
	v_exp_f32_e32 v76, v76
	v_exp_f32_e32 v77, v77
	s_nop 0
	v_exp_f32_e32 v78, v78
	v_exp_f32_e32 v79, v79
	v_exp_f32_e32 v80, v80
	v_exp_f32_e32 v81, v81
	s_waitcnt lgkmcnt(2)
	v_mfma_f32_32x32x16_bf16 v[98:113], v[158:161], v[150:153], v[34:49]
	v_add_f32_e32 v114, 0, v66
	v_add_f32_e32 v114, v67, v114
	v_add_f32_e32 v114, v68, v114
	v_add_f32_e32 v114, v69, v114
	s_waitcnt lgkmcnt(1)
	v_mfma_f32_32x32x16_bf16 v[82:97], v[188:191], v[146:149], v[82:97]
	ds_read_b128 v[158:161], v185 offset:4096
	ds_read_b128 v[196:199], v185 offset:4608
	v_add_f32_e32 v114, v114, v70
	v_add_f32_e32 v114, v71, v114
	v_add_f32_e32 v114, v72, v114
	v_exp_f32_e32 v50, v50
	v_exp_f32_e32 v51, v51
	v_exp_f32_e32 v52, v52
	v_exp_f32_e32 v53, v53
	v_add_f32_e32 v114, v73, v114
	s_nop 0
	v_add_f32_e32 v114, v74, v114
	v_add_f32_e32 v114, v75, v114
	v_add_f32_e32 v114, v76, v114
	v_exp_f32_e32 v54, v54
	v_exp_f32_e32 v55, v55
	v_exp_f32_e32 v56, v56
	v_exp_f32_e32 v57, v57
	v_add_f32_e32 v118, v77, v114
	v_cvt_pk_bf16_f32 v114, v66, v67
	v_cvt_pk_bf16_f32 v115, v68, v69
	s_waitcnt lgkmcnt(2)
	v_mfma_f32_32x32x16_bf16 v[98:113], v[192:195], v[146:149], v[98:113]
	s_waitcnt lgkmcnt(1)
	v_mfma_f32_32x32x16_bf16 v[82:97], v[158:161], v[142:145], v[82:97]
	ds_read_b128 v[66:69], v185 offset:6144
	ds_read_b128 v[188:191], v185 offset:6656
	v_add_f32_e32 v116, v78, v118
	v_add_f32_e32 v116, v79, v116
	v_add_f32_e32 v116, v80, v116
	v_exp_f32_e32 v58, v58
	v_exp_f32_e32 v59, v59
	v_exp_f32_e32 v60, v60
	v_exp_f32_e32 v61, v61
	v_add_f32_e32 v118, v81, v116
	v_cvt_pk_bf16_f32 v116, v70, v71
	v_cvt_pk_bf16_f32 v117, v72, v73
	s_nop 0
	v_exp_f32_e32 v62, v62
	v_exp_f32_e32 v63, v63
	v_exp_f32_e32 v64, v64
	v_exp_f32_e32 v65, v65
	v_cvt_pk_bf16_f32 v119, v76, v77
	v_add_f32_e32 v70, v118, v50
	v_add_f32_e32 v70, v51, v70
	v_add_f32_e32 v70, v52, v70
	v_add_f32_e32 v122, v53, v70
	v_cvt_pk_bf16_f32 v118, v74, v75
	s_waitcnt lgkmcnt(2)
	v_mfma_f32_32x32x16_bf16 v[98:113], v[196:199], v[142:145], v[98:113]
	s_waitcnt lgkmcnt(1)
	v_mfma_f32_32x32x16_bf16 v[82:97], v[66:69], v[138:141], v[82:97]
	ds_read_b128 v[70:73], v185 offset:8192
	ds_read_b128 v[74:77], v185 offset:8704
	v_add_f32_e32 v120, v122, v54
	v_add_f32_e32 v120, v55, v120
	v_add_f32_e32 v120, v56, v120
	v_add_f32_e32 v122, v57, v120
	v_cvt_pk_bf16_f32 v120, v78, v79
	v_cvt_pk_bf16_f32 v121, v80, v81
	s_nop 0
	v_add_f32_e32 v66, v58, v122
	v_add_f32_e32 v66, v59, v66
	v_add_f32_e32 v66, v60, v66
	v_add_f32_e32 v78, v61, v66
	v_cvt_pk_bf16_f32 v122, v50, v51
	v_cvt_pk_bf16_f32 v123, v52, v53
	s_waitcnt lgkmcnt(2)
	v_mfma_f32_32x32x16_bf16 v[98:113], v[188:191], v[138:141], v[98:113]
	s_waitcnt lgkmcnt(1)
	v_mfma_f32_32x32x16_bf16 v[82:97], v[70:73], v[134:137], v[82:97]
	ds_read_b128 v[50:53], v185 offset:10240
	ds_read_b128 v[66:69], v185 offset:10752
	v_add_f32_e32 v78, v62, v78
	v_add_f32_e32 v78, v63, v78
	v_add_f32_e32 v78, v64, v78
	v_add_f32_e32 v78, v65, v78
	v_cvt_pk_bf16_f32 v124, v54, v55
	v_cvt_pk_bf16_f32 v125, v56, v57
	v_cvt_pk_bf16_f32 v126, v58, v59
	v_cvt_pk_bf16_f32 v127, v60, v61
	s_waitcnt lgkmcnt(2)
	v_mfma_f32_32x32x16_bf16 v[98:113], v[74:77], v[134:137], v[98:113]
	s_waitcnt lgkmcnt(1)
	v_mfma_f32_32x32x16_bf16 v[82:97], v[50:53], v[130:133], v[82:97]
	v_cvt_pk_bf16_f32 v128, v62, v63
	v_cvt_pk_bf16_f32 v129, v64, v65
	s_waitcnt lgkmcnt(0)
; __device__ __forceinline__ float max3f(float a, float b, float c) { float r; asm("v_max3_f32 %0, %1, %2, %3" : "=v"(r) : "v"(a), "v"(b), "v"(c)); return r; }
; __device__ __forceinline__ void cmask(f32x16& p0, f32x16& p1, int jb, int qrel, int hi) {
;     const float NEG = -INFINITY; const int kb = 64 * jb + 4 * hi;
; #pragma unroll
;     for (int r = 0; r < 16; ++r) { const int kv = kb + (r & 3) + 8 * (r >> 2); if (kv > qrel) p0[r] = NEG; if (kv + 32 > qrel) p1[r] = NEG; }
; }
; __device__ __forceinline__ float rowmax(const f32x16& p0, const f32x16& p1) {
;     float a = max3f(p0[0], p0[1], p1[0]), b = max3f(p0[2], p0[3], p1[1]); a = max3f(a, p1[2], p1[3]);
; #pragma unroll
;     for (int r = 4; r < 16; r += 4) { a = max3f(a, p0[r], p0[r + 1]); b = max3f(b, p0[r + 2], p0[r + 3]); a = max3f(a, p1[r], p1[r + 1]); b = max3f(b, p1[r + 2], p1[r + 3]); }
;     const float m = fmaxf(a, b);
;     auto rr = __builtin_amdgcn_permlane32_swap(__float_as_uint(m), __float_as_uint(m), false, false);
;     return fmaxf(__uint_as_float(rr[0]), __uint_as_float(rr[1]));
; }
	v_mfma_f32_32x32x16_bf16 v[98:113], v[66:69], v[130:133], v[98:113]
	v_add_f32_e32 v158, v187, v78
	s_setprio 0
	v_or_b32_e32 v50, 0x60, v186
	v_or_b32_e32 v51, 64, v186
	v_cmp_le_i32_e32 vcc, v50, v182
	v_or_b32_e32 v52, 0x42, v186
	v_or_b32_e32 v53, 0x43, v186
	s_nop 4
	v_cndmask_b32_e32 v50, v206, v98, vcc
	v_cmp_lt_i32_e32 vcc, v51, v182
	v_or_b32_e32 v54, 0x48, v186
	v_or_b32_e32 v55, 0x49, v186
	v_cndmask_b32_e32 v67, v206, v83, vcc
	v_cmp_le_i32_e32 vcc, v51, v182
	v_or_b32_e32 v51, 0x61, v186
	v_or_b32_e32 v56, 0x4a, v186
	v_cndmask_b32_e32 v66, v206, v82, vcc
	v_cmp_le_i32_e32 vcc, v51, v182
	v_or_b32_e32 v57, 0x4b, v186
	v_or_b32_e32 v58, 0x50, v186
	v_cndmask_b32_e32 v51, v206, v99, vcc
	v_cmp_le_i32_e32 vcc, v52, v182
	v_or_b32_e32 v52, 0x62, v186
	v_or_b32_e32 v59, 0x51, v186
	v_cndmask_b32_e32 v68, v206, v84, vcc
	v_cmp_le_i32_e32 vcc, v52, v182
	v_or_b32_e32 v60, 0x52, v186
	v_or_b32_e32 v61, 0x53, v186
	v_cndmask_b32_e32 v52, v206, v100, vcc
	v_cmp_le_i32_e32 vcc, v53, v182
	v_or_b32_e32 v53, 0x63, v186
	v_or_b32_e32 v62, 0x58, v186
	v_cndmask_b32_e32 v69, v206, v85, vcc
	v_cmp_le_i32_e32 vcc, v53, v182
	v_or_b32_e32 v63, 0x59, v186
	v_max3_f32 v82, v66, v67, v50
	v_max3_f32 v83, v68, v69, v51
	v_or_b32_e32 v64, 0x5a, v186
	v_cndmask_b32_e32 v53, v206, v101, vcc
	v_cmp_le_i32_e32 vcc, v54, v182
	v_or_b32_e32 v54, 0x68, v186
	v_max3_f32 v82, v82, v52, v53
	v_or_b32_e32 v65, 0x5b, v186
	v_cndmask_b32_e32 v70, v206, v86, vcc
	v_cmp_le_i32_e32 vcc, v54, v182
	s_nop 1
	v_cndmask_b32_e32 v54, v206, v102, vcc
	v_cmp_le_i32_e32 vcc, v55, v182
	v_or_b32_e32 v55, 0x69, v186
	s_nop 0
	v_cndmask_b32_e32 v71, v206, v87, vcc
	v_cmp_le_i32_e32 vcc, v55, v182
	v_max3_f32 v82, v82, v70, v71
	s_nop 1
	v_cndmask_b32_e32 v55, v206, v103, vcc
	v_cmp_le_i32_e32 vcc, v56, v182
	v_or_b32_e32 v56, 0x6a, v186
	v_max3_f32 v82, v82, v54, v55
	s_nop 0
	v_cndmask_b32_e32 v72, v206, v88, vcc
	v_cmp_le_i32_e32 vcc, v56, v182
	s_nop 1
	v_cndmask_b32_e32 v56, v206, v104, vcc
	v_cmp_le_i32_e32 vcc, v57, v182
	v_or_b32_e32 v57, 0x6b, v186
	s_nop 0
	v_cndmask_b32_e32 v73, v206, v89, vcc
	v_cmp_le_i32_e32 vcc, v57, v182
	v_max3_f32 v83, v83, v72, v73
	s_nop 1
	v_cndmask_b32_e32 v57, v206, v105, vcc
	v_cmp_le_i32_e32 vcc, v58, v182
	v_or_b32_e32 v58, 0x70, v186
	v_max3_f32 v83, v83, v56, v57
	s_nop 0
	v_cndmask_b32_e32 v74, v206, v90, vcc
	v_cmp_le_i32_e32 vcc, v58, v182
	s_nop 1
	v_cndmask_b32_e32 v58, v206, v106, vcc
	v_cmp_le_i32_e32 vcc, v59, v182
	v_or_b32_e32 v59, 0x71, v186
	s_nop 0
	v_cndmask_b32_e32 v75, v206, v91, vcc
	v_cmp_le_i32_e32 vcc, v59, v182
	v_max3_f32 v82, v82, v74, v75
	s_nop 1
	v_cndmask_b32_e32 v59, v206, v107, vcc
	v_cmp_le_i32_e32 vcc, v60, v182
	v_or_b32_e32 v60, 0x72, v186
	v_max3_f32 v82, v82, v58, v59
	s_nop 0
	v_cndmask_b32_e32 v76, v206, v92, vcc
	v_cmp_le_i32_e32 vcc, v60, v182
	s_nop 1
	v_cndmask_b32_e32 v60, v206, v108, vcc
	v_cmp_le_i32_e32 vcc, v61, v182
	v_or_b32_e32 v61, 0x73, v186
	s_nop 0
	v_cndmask_b32_e32 v77, v206, v93, vcc
	v_cmp_le_i32_e32 vcc, v61, v182
	v_max3_f32 v83, v83, v76, v77
	s_nop 1
	v_cndmask_b32_e32 v61, v206, v109, vcc
	v_cmp_le_i32_e32 vcc, v62, v182
	v_or_b32_e32 v62, 0x78, v186
	v_max3_f32 v83, v83, v60, v61
	s_nop 0
	v_cndmask_b32_e32 v78, v206, v94, vcc
	v_cmp_le_i32_e32 vcc, v62, v182
	s_nop 1
	v_cndmask_b32_e32 v62, v206, v110, vcc
	v_cmp_le_i32_e32 vcc, v63, v182
	v_or_b32_e32 v63, 0x79, v186
	s_nop 0
	v_cndmask_b32_e32 v79, v206, v95, vcc
	v_cmp_le_i32_e32 vcc, v63, v182
	v_max3_f32 v82, v82, v78, v79
	s_nop 1
	v_cndmask_b32_e32 v63, v206, v111, vcc
	v_cmp_le_i32_e32 vcc, v64, v182
	v_or_b32_e32 v64, 0x7a, v186
	v_max3_f32 v82, v82, v62, v63
	s_nop 0
	v_cndmask_b32_e32 v80, v206, v96, vcc
	v_cmp_le_i32_e32 vcc, v64, v182
	v_max_f32_e32 v82, v82, v82
	s_nop 0
	v_cndmask_b32_e32 v64, v206, v112, vcc
	v_cmp_le_i32_e32 vcc, v65, v182
	v_or_b32_e32 v65, 0x7b, v186
	s_nop 0
	v_cndmask_b32_e32 v81, v206, v97, vcc
	v_cmp_le_i32_e32 vcc, v65, v182
	v_max3_f32 v83, v83, v80, v81
	s_nop 1
	v_cndmask_b32_e32 v65, v206, v113, vcc
	v_max3_f32 v83, v83, v64, v65
	s_nop 0
	v_max_f32_e32 v83, v83, v83
	v_max_f32_e32 v82, v82, v83
	v_mov_b32_e32 v83, v82
	s_nop 1
	v_permlane32_swap_b32_e32 v82, v83
	v_max_f32_e32 v83, v83, v83
	v_max_f32_e32 v82, v82, v82
	v_max_f32_e32 v82, v82, v83
	v_cmp_lt_f32_e32 vcc, s54, v82
	s_cmp_lg_u64 vcc, 0
	s_cselect_b64 s[42:43], -1, 0
	s_cbranch_vccnz .LBB0_1211

.LBB0_1136:
	v_lshl_add_u64 v[82:83], v[156:157], 0, s[0:1]
	s_mov_b32 m0, s73
	s_nop 0
	global_load_lds_dwordx4 v[82:83], off
	s_setprio 1
	ds_read_b128 v[98:101], v184
	ds_read_b128 v[188:191], v184 offset:512
	v_exp_f32_e32 v66, v66
	v_exp_f32_e32 v67, v67
	v_exp_f32_e32 v68, v68
	v_exp_f32_e32 v69, v69
	s_nop 0
	v_exp_f32_e32 v70, v70
	v_exp_f32_e32 v71, v71
	v_exp_f32_e32 v72, v72
	v_exp_f32_e32 v73, v73
	s_waitcnt lgkmcnt(1)
	v_mfma_f32_32x32x16_bf16 v[82:97], v[98:101], v[150:153], v[34:49]
	ds_read_b128 v[192:195], v184 offset:2048
	ds_read_b128 v[196:199], v184 offset:2560
	v_exp_f32_e32 v74, v74
	v_exp_f32_e32 v75, v75
	v_exp_f32_e32 v76, v76
	v_exp_f32_e32 v77, v77
	s_nop 0
	v_exp_f32_e32 v78, v78
	v_exp_f32_e32 v79, v79
	v_exp_f32_e32 v80, v80
	v_exp_f32_e32 v81, v81
	s_waitcnt lgkmcnt(2)
	v_mfma_f32_32x32x16_bf16 v[98:113], v[188:191], v[150:153], v[34:49]
	v_add_f32_e32 v114, 0, v66
	v_add_f32_e32 v114, v67, v114
	v_add_f32_e32 v114, v68, v114
	v_add_f32_e32 v114, v69, v114
	s_waitcnt lgkmcnt(1)
	v_mfma_f32_32x32x16_bf16 v[82:97], v[192:195], v[146:149], v[82:97]
	ds_read_b128 v[188:191], v184 offset:4096
	ds_read_b128 v[200:203], v184 offset:4608
	v_add_f32_e32 v114, v114, v70
	v_add_f32_e32 v114, v71, v114
	v_add_f32_e32 v114, v72, v114
	v_exp_f32_e32 v50, v50
	v_exp_f32_e32 v51, v51
	v_exp_f32_e32 v52, v52
	v_exp_f32_e32 v53, v53
	v_add_f32_e32 v114, v73, v114
	s_nop 0
	v_add_f32_e32 v114, v74, v114
	v_add_f32_e32 v114, v75, v114
	v_add_f32_e32 v114, v76, v114
	v_exp_f32_e32 v54, v54
	v_exp_f32_e32 v55, v55
	v_exp_f32_e32 v56, v56
	v_exp_f32_e32 v57, v57
	v_add_f32_e32 v118, v77, v114
	v_cvt_pk_bf16_f32 v114, v66, v67
	v_cvt_pk_bf16_f32 v115, v68, v69
	s_waitcnt lgkmcnt(2)
	v_mfma_f32_32x32x16_bf16 v[98:113], v[196:199], v[146:149], v[98:113]
	s_waitcnt lgkmcnt(1)
	v_mfma_f32_32x32x16_bf16 v[82:97], v[188:191], v[142:145], v[82:97]
	ds_read_b128 v[66:69], v184 offset:6144
	ds_read_b128 v[192:195], v184 offset:6656
	v_add_f32_e32 v116, v78, v118
	v_add_f32_e32 v116, v79, v116
	v_add_f32_e32 v116, v80, v116
	v_exp_f32_e32 v58, v58
	v_exp_f32_e32 v59, v59
	v_exp_f32_e32 v60, v60
	v_exp_f32_e32 v61, v61
	v_add_f32_e32 v118, v81, v116
	v_cvt_pk_bf16_f32 v116, v70, v71
	v_cvt_pk_bf16_f32 v117, v72, v73
	s_nop 0
	v_exp_f32_e32 v62, v62
	v_exp_f32_e32 v63, v63
	v_exp_f32_e32 v64, v64
	v_exp_f32_e32 v65, v65
	v_cvt_pk_bf16_f32 v119, v76, v77
	v_add_f32_e32 v70, v118, v50
	v_add_f32_e32 v70, v51, v70
	v_add_f32_e32 v70, v52, v70
	v_add_f32_e32 v122, v53, v70
	v_cvt_pk_bf16_f32 v118, v74, v75
	s_waitcnt lgkmcnt(2)
	v_mfma_f32_32x32x16_bf16 v[98:113], v[200:203], v[142:145], v[98:113]
	s_waitcnt lgkmcnt(1)
	v_mfma_f32_32x32x16_bf16 v[82:97], v[66:69], v[138:141], v[82:97]
	ds_read_b128 v[70:73], v184 offset:8192
	ds_read_b128 v[74:77], v184 offset:8704
	v_add_f32_e32 v120, v122, v54
	v_add_f32_e32 v120, v55, v120
	v_add_f32_e32 v120, v56, v120
	v_add_f32_e32 v122, v57, v120
	v_cvt_pk_bf16_f32 v120, v78, v79
	v_cvt_pk_bf16_f32 v121, v80, v81
	s_nop 0
	v_add_f32_e32 v66, v58, v122
	v_add_f32_e32 v66, v59, v66
	v_add_f32_e32 v66, v60, v66
	v_add_f32_e32 v78, v61, v66
	v_cvt_pk_bf16_f32 v122, v50, v51
	v_cvt_pk_bf16_f32 v123, v52, v53
	s_waitcnt lgkmcnt(2)
	v_mfma_f32_32x32x16_bf16 v[98:113], v[192:195], v[138:141], v[98:113]
	s_waitcnt lgkmcnt(1)
	v_mfma_f32_32x32x16_bf16 v[82:97], v[70:73], v[134:137], v[82:97]
	ds_read_b128 v[50:53], v184 offset:10240
	ds_read_b128 v[66:69], v184 offset:10752
	v_add_f32_e32 v78, v62, v78
	v_add_f32_e32 v78, v63, v78
	v_add_f32_e32 v78, v64, v78
	v_add_f32_e32 v78, v65, v78
	v_cvt_pk_bf16_f32 v124, v54, v55
	v_cvt_pk_bf16_f32 v125, v56, v57
	v_cvt_pk_bf16_f32 v126, v58, v59
	v_cvt_pk_bf16_f32 v127, v60, v61
	s_waitcnt lgkmcnt(2)
	v_mfma_f32_32x32x16_bf16 v[98:113], v[74:77], v[134:137], v[98:113]
	s_waitcnt lgkmcnt(1)
	v_mfma_f32_32x32x16_bf16 v[82:97], v[50:53], v[130:133], v[82:97]
	v_cvt_pk_bf16_f32 v128, v62, v63
	v_cvt_pk_bf16_f32 v129, v64, v65
	s_waitcnt lgkmcnt(0)
; __device__ __forceinline__ float max3f(float a, float b, float c) { float r; asm("v_max3_f32 %0, %1, %2, %3" : "=v"(r) : "v"(a), "v"(b), "v"(c)); return r; }
; __device__ __forceinline__ void cmask(f32x16& p0, f32x16& p1, int jb, int qrel, int hi) {
;     const float NEG = -INFINITY; const int kb = 64 * jb + 4 * hi;
; #pragma unroll
;     for (int r = 0; r < 16; ++r) { const int kv = kb + (r & 3) + 8 * (r >> 2); if (kv > qrel) p0[r] = NEG; if (kv + 32 > qrel) p1[r] = NEG; }
; }
; __device__ __forceinline__ float rowmax(const f32x16& p0, const f32x16& p1) {
;     float a = max3f(p0[0], p0[1], p1[0]), b = max3f(p0[2], p0[3], p1[1]); a = max3f(a, p1[2], p1[3]);
; #pragma unroll
;     for (int r = 4; r < 16; r += 4) { a = max3f(a, p0[r], p0[r + 1]); b = max3f(b, p0[r + 2], p0[r + 3]); a = max3f(a, p1[r], p1[r + 1]); b = max3f(b, p1[r + 2], p1[r + 3]); }
;     const float m = fmaxf(a, b);
;     auto rr = __builtin_amdgcn_permlane32_swap(__float_as_uint(m), __float_as_uint(m), false, false);
;     return fmaxf(__uint_as_float(rr[0]), __uint_as_float(rr[1]));
; }
	v_mfma_f32_32x32x16_bf16 v[98:113], v[66:69], v[130:133], v[98:113]
	v_add_f32_e32 v156, v158, v78
	s_setprio 0
	v_or_b32_e32 v50, 0xa0, v186
	v_or_b32_e32 v51, 0x80, v186
	v_cmp_le_i32_e32 vcc, v50, v182
	v_or_b32_e32 v52, 0x82, v186
	v_or_b32_e32 v53, 0x83, v186
	s_nop 4
	v_cndmask_b32_e32 v50, v206, v98, vcc
	v_cmp_lt_i32_e32 vcc, v51, v182
	v_or_b32_e32 v54, 0x88, v186
	v_or_b32_e32 v55, 0x89, v186
	v_cndmask_b32_e32 v67, v206, v83, vcc
	v_cmp_le_i32_e32 vcc, v51, v182
	v_or_b32_e32 v51, 0xa1, v186
	v_or_b32_e32 v56, 0x8a, v186
	v_cndmask_b32_e32 v66, v206, v82, vcc
	v_cmp_le_i32_e32 vcc, v51, v182
	v_or_b32_e32 v57, 0x8b, v186
	v_or_b32_e32 v58, 0x90, v186
	v_cndmask_b32_e32 v51, v206, v99, vcc
	v_cmp_le_i32_e32 vcc, v52, v182
	v_or_b32_e32 v52, 0xa2, v186
	v_or_b32_e32 v59, 0x91, v186
	v_cndmask_b32_e32 v68, v206, v84, vcc
	v_cmp_le_i32_e32 vcc, v52, v182
	v_or_b32_e32 v60, 0x92, v186
	v_or_b32_e32 v61, 0x93, v186
	v_cndmask_b32_e32 v52, v206, v100, vcc
	v_cmp_le_i32_e32 vcc, v53, v182
	v_or_b32_e32 v53, 0xa3, v186
	v_or_b32_e32 v62, 0x98, v186
	v_cndmask_b32_e32 v69, v206, v85, vcc
	v_cmp_le_i32_e32 vcc, v53, v182
	v_or_b32_e32 v63, 0x99, v186
	v_max3_f32 v82, v66, v67, v50
	v_max3_f32 v83, v68, v69, v51
	v_or_b32_e32 v64, 0x9a, v186
	v_cndmask_b32_e32 v53, v206, v101, vcc
	v_cmp_le_i32_e32 vcc, v54, v182
	v_or_b32_e32 v54, 0xa8, v186
	v_max3_f32 v82, v82, v52, v53
	v_or_b32_e32 v65, 0x9b, v186
	v_cndmask_b32_e32 v70, v206, v86, vcc
	v_cmp_le_i32_e32 vcc, v54, v182
	s_nop 1
	v_cndmask_b32_e32 v54, v206, v102, vcc
	v_cmp_le_i32_e32 vcc, v55, v182
	v_or_b32_e32 v55, 0xa9, v186
	s_nop 0
	v_cndmask_b32_e32 v71, v206, v87, vcc
	v_cmp_le_i32_e32 vcc, v55, v182
	v_max3_f32 v82, v82, v70, v71
	s_nop 1
	v_cndmask_b32_e32 v55, v206, v103, vcc
	v_cmp_le_i32_e32 vcc, v56, v182
	v_or_b32_e32 v56, 0xaa, v186
	v_max3_f32 v82, v82, v54, v55
	s_nop 0
	v_cndmask_b32_e32 v72, v206, v88, vcc
	v_cmp_le_i32_e32 vcc, v56, v182
	s_nop 1
	v_cndmask_b32_e32 v56, v206, v104, vcc
	v_cmp_le_i32_e32 vcc, v57, v182
	v_or_b32_e32 v57, 0xab, v186
	s_nop 0
	v_cndmask_b32_e32 v73, v206, v89, vcc
	v_cmp_le_i32_e32 vcc, v57, v182
	v_max3_f32 v83, v83, v72, v73
	s_nop 1
	v_cndmask_b32_e32 v57, v206, v105, vcc
	v_cmp_le_i32_e32 vcc, v58, v182
	v_or_b32_e32 v58, 0xb0, v186
	v_max3_f32 v83, v83, v56, v57
	s_nop 0
	v_cndmask_b32_e32 v74, v206, v90, vcc
	v_cmp_le_i32_e32 vcc, v58, v182
	s_nop 1
	v_cndmask_b32_e32 v58, v206, v106, vcc
	v_cmp_le_i32_e32 vcc, v59, v182
	v_or_b32_e32 v59, 0xb1, v186
	s_nop 0
	v_cndmask_b32_e32 v75, v206, v91, vcc
	v_cmp_le_i32_e32 vcc, v59, v182
	v_max3_f32 v82, v82, v74, v75
	s_nop 1
	v_cndmask_b32_e32 v59, v206, v107, vcc
	v_cmp_le_i32_e32 vcc, v60, v182
	v_or_b32_e32 v60, 0xb2, v186
	v_max3_f32 v82, v82, v58, v59
	s_nop 0
	v_cndmask_b32_e32 v76, v206, v92, vcc
	v_cmp_le_i32_e32 vcc, v60, v182
	s_nop 1
	v_cndmask_b32_e32 v60, v206, v108, vcc
	v_cmp_le_i32_e32 vcc, v61, v182
	v_or_b32_e32 v61, 0xb3, v186
	s_nop 0
	v_cndmask_b32_e32 v77, v206, v93, vcc
	v_cmp_le_i32_e32 vcc, v61, v182
	v_max3_f32 v83, v83, v76, v77
	s_nop 1
	v_cndmask_b32_e32 v61, v206, v109, vcc
	v_cmp_le_i32_e32 vcc, v62, v182
	v_or_b32_e32 v62, 0xb8, v186
	v_max3_f32 v83, v83, v60, v61
	s_nop 0
	v_cndmask_b32_e32 v78, v206, v94, vcc
	v_cmp_le_i32_e32 vcc, v62, v182
	s_nop 1
	v_cndmask_b32_e32 v62, v206, v110, vcc
	v_cmp_le_i32_e32 vcc, v63, v182
	v_or_b32_e32 v63, 0xb9, v186
	s_nop 0
	v_cndmask_b32_e32 v79, v206, v95, vcc
	v_cmp_le_i32_e32 vcc, v63, v182
	v_max3_f32 v82, v82, v78, v79
	s_nop 1
	v_cndmask_b32_e32 v63, v206, v111, vcc
	v_cmp_le_i32_e32 vcc, v64, v182
	v_or_b32_e32 v64, 0xba, v186
	v_max3_f32 v82, v82, v62, v63
	s_nop 0
	v_cndmask_b32_e32 v80, v206, v96, vcc
	v_cmp_le_i32_e32 vcc, v64, v182
	v_max_f32_e32 v82, v82, v82
	s_nop 0
	v_cndmask_b32_e32 v64, v206, v112, vcc
	v_cmp_le_i32_e32 vcc, v65, v182
	v_or_b32_e32 v65, 0xbb, v186
	s_nop 0
	v_cndmask_b32_e32 v81, v206, v97, vcc
	v_cmp_le_i32_e32 vcc, v65, v182
	v_max3_f32 v83, v83, v80, v81
	s_nop 1
	v_cndmask_b32_e32 v65, v206, v113, vcc
	v_max3_f32 v83, v83, v64, v65
	s_nop 0
	v_max_f32_e32 v83, v83, v83
	v_max_f32_e32 v82, v82, v83
	v_mov_b32_e32 v83, v82
	s_nop 1
	v_permlane32_swap_b32_e32 v82, v83
	v_max_f32_e32 v83, v83, v83
	v_max_f32_e32 v82, v82, v82
	v_max_f32_e32 v82, v82, v83
	v_cmp_lt_f32_e32 vcc, s54, v82
	s_cmp_lg_u64 vcc, 0
	s_cselect_b64 s[0:1], -1, 0
	s_cbranch_vccnz .LBB0_1214

; __device__ __forceinline__ int tid_from_wave(int wave) { unsigned l_; asm volatile("v_mbcnt_lo_u32_b32 %0, -1, 0\n\tv_mbcnt_hi_u32_b32 %0, -1, %0" : "=v"(l_)); return wave * 64 + (int)l_; }
; template <int THRL, bool LATE> __device__ __forceinline__ void unit_stag(int b, int h, int qb, const unsigned short* Q, const unsigned short* KV, const unsigned short* KPE, unsigned short* O, char* shm, const int wave_) {
;     int tid_ = tid_from_wave(wave_); asm volatile("" : "+v"(tid_));
;     const int tid = tid_, lane = tid & 63, r32 = lane & 31, hi = lane >> 5; const int wid = __builtin_amdgcn_readfirstlane(tid >> 6);
;     const long rowbase = (long)b * SEQ; const int q0 = qb * QB;
;     const unsigned short* Qw = Q + (rowbase + q0 + wid * QBLK) * QP + h * 96;
;     const unsigned short* Kh = KV + rowbase * KVP + h * 128; const unsigned short* Vh = Kh + 64; const unsigned short* Ph = KPE + rowbase * PEP;
;     const unsigned lds0 = (unsigned)(uintptr_t)shm;
;     __attribute__((address_space(3))) float* wsf = (__attribute__((address_space(3))) float*)((lds_cptr)shm + S4_WS) + wid * 64;
;     const unsigned short* ksrc = Kh + (long)lane * KVP + wid * 8;
;     const unsigned short* psrc = Ph + (long)(32 * (wid & 1) + r32) * PEP + (wid >> 1) * 8;
;     const unsigned short* vsrc = Vh + (long)(16 * (wid & 3) + (lane >> 2)) * KVP + (wid >> 2) * 32 + (lane & 3) * 8;
;     const unsigned kdst = lds0 + LDS_K + wid * 1024, pdst = lds0 + LDS_K + (8 + (wid >> 1)) * 1024 + (wid & 1) * 512, vdst = lds0 + S4_V + wid * 1024;
;     const int vb0 = (int)(lds0 + S4_V) + ((lane >> 4) & 1) * 32 + (lane & 3) * 8 + (4 * hi + ((lane & 15) >> 2)) * 64;
;     const lds_cptr kp0 = (lds_cptr)shm + LDS_K + hi * 1024 + r32 * 16;
;     const int NT = (q0 + QB) / KVBLK;
;     bf16x8 qr[6];
; #pragma unroll
;     for (int d0 = 0; d0 < 6; ++d0) qr[d0] = *reinterpret_cast<const bf16x8*>(&Qw[(long)r32 * QP + d0 * 16 + hi * 8]);
;     asm volatile("s_waitcnt vmcnt(0)" ::: "memory");
;     glds16(ksrc, (unsigned)__builtin_amdgcn_readfirstlane(kdst)); if (lane < 32) glds16(psrc, (unsigned)__builtin_amdgcn_readfirstlane(pdst));
;     glds16(ksrc + (long)KVBLK * KVP, (unsigned)__builtin_amdgcn_readfirstlane(kdst + KSLOT)); if (lane < 32) glds16(psrc + (long)KVBLK * PEP, (unsigned)__builtin_amdgcn_readfirstlane(pdst + KSLOT)); glds16(vsrc, (unsigned)__builtin_amdgcn_readfirstlane(vdst));
.LBB0_1145:
	s_and_b64 vcc, exec, s[0:1]
	s_cbranch_vccz .LBB0_1172
	v_mbcnt_lo_u32_b32 v0, -1, 0
	v_mbcnt_hi_u32_b32 v0, -1, v0
	s_nop 0
	v_add_u32_e32 v34, s96, v0
	s_nop 0
	v_readfirstlane_b32 s10, v34
	s_ashr_i32 s68, s10, 6
	s_lshl_b32 s75, s68, 5
	s_ashr_i32 s0, s75, 31
	s_add_u32 s40, s47, s75
	s_addc_u32 s41, s69, s0
	v_and_b32_e32 v209, 31, v34
	s_mul_i32 s0, s41, 0x600
	s_mul_hi_u32 s1, s40, 0x600
	s_add_i32 s1, s1, s0
	s_mul_i32 s0, s40, 0x600
	v_mul_u32_u24_e32 v0, 0x300, v209
	v_bfe_u32 v210, v34, 5, 1
	s_add_u32 s0, s63, s0
	v_lshlrev_b32_e32 v0, 1, v0
	s_addc_u32 s1, s64, s1
	v_lshl_or_b32 v0, v210, 4, v0
	global_load_dwordx4 v[196:199], v0, s[0:1]
	global_load_dwordx4 v[192:195], v0, s[0:1] offset:32
	global_load_dwordx4 v[188:191], v0, s[0:1] offset:64
	global_load_dwordx4 v[184:187], v0, s[0:1] offset:96
	global_load_dwordx4 v[180:183], v0, s[0:1] offset:128
	global_load_dwordx4 v[176:179], v0, s[0:1] offset:160
	s_ashr_i32 s44, s10, 7
	s_lshl_b32 s0, s68, 3
	s_lshl_b32 s2, s44, 3
	s_ashr_i32 s1, s0, 31
	s_and_b32 s43, s68, 1
	s_ashr_i32 s3, s2, 31
	s_lshl_b32 s42, s68, 10
	s_lshl_b32 s44, s44, 10
	v_and_b32_e32 v207, 63, v34
	s_cmp_lg_u32 0, -1
	s_cselect_b32 s45, 0, 0
	v_lshlrev_b32_e32 v0, 11, v207
	s_add_i32 s44, s45, s44
	s_lshl_b32 s47, s43, 9
	v_lshl_add_u64 v[2:3], s[36:37], 0, v[0:1]
	v_lshlrev_b32_e32 v0, 6, v209
	s_waitcnt vmcnt(0)
	s_add_i32 s70, s44, s47
	v_lshl_add_u64 v[204:205], s[0:1], 1, v[2:3]
	v_lshl_or_b32 v0, s43, 11, v0
	s_add_i32 s44, s42, s45
	s_mov_b32 m0, s44
	s_nop 0
	global_load_lds_dwordx4 v[204:205], off
	v_lshl_add_u64 v[2:3], s[38:39], 0, v[0:1]
	s_addk_i32 s70, 0x2000
	v_lshl_add_u64 v[202:203], s[2:3], 1, v[2:3]
	v_cmp_gt_u32_e64 s[2:3], 32, v207
	s_and_saveexec_b64 s[0:1], s[2:3]
	s_cbranch_execz .LBB0_1148
	s_mov_b32 m0, s70
	s_nop 0
	global_load_lds_dwordx4 v[202:203], off
.LBB0_1148:
	s_or_b64 exec, exec, s[0:1]
	s_cmp_lg_u32 0, -1
	s_cselect_b32 s0, 0, 0
	s_add_i32 s0, s0, s42
	v_lshl_add_u64 v[2:3], v[204:205], 0, s[12:13]
	s_addk_i32 s0, 0x3000
	s_mov_b32 m0, s0
	s_nop 0
	global_load_lds_dwordx4 v[2:3], off
	s_and_saveexec_b64 s[0:1], s[2:3]
	s_cbranch_execz .LBB0_1150
	v_lshl_add_u64 v[2:3], v[202:203], 0, s[14:15]
	s_add_i32 s43, s70, 0x3000
	s_mov_b32 m0, s43
	s_nop 0
	global_load_lds_dwordx4 v[2:3], off
.LBB0_1150:
	s_or_b64 exec, exec, s[0:1]
	s_lshl_b32 s0, s68, 4
	v_lshrrev_b32_e32 v0, 2, v207
	v_and_or_b32 v0, s0, 48, v0
	s_ashr_i32 s0, s10, 3
	s_andn2_b32 s0, s0, 31
	s_ashr_i32 s1, s0, 31
	v_lshlrev_b32_e32 v208, 3, v34
	v_lshlrev_b32_e32 v0, 11, v0
	v_and_b32_e32 v35, 24, v208
	v_lshl_add_u64 v[2:3], s[36:37], 0, v[0:1]
	s_cmp_lg_u32 0, -1
	v_lshl_add_u64 v[2:3], s[0:1], 1, v[2:3]
	v_lshlrev_b32_e32 v0, 1, v35
	s_cselect_b32 s0, 0, 0
	v_lshl_add_u64 v[2:3], v[2:3], 0, v[0:1]
	s_add_i32 s0, s0, s42
	v_lshl_add_u64 v[200:201], v[2:3], 0, s[16:17]
	s_add_i32 s71, s0, 0x9000
	s_mov_b32 m0, s71
	s_nop 0
	global_load_lds_dwordx4 v[200:201], off
	v_lshl_add_u64 v[2:3], v[204:205], 0, s[18:19]
	s_addk_i32 s0, 0x6000
	s_mov_b32 m0, s0
	s_nop 0
	global_load_lds_dwordx4 v[2:3], off
	s_and_saveexec_b64 s[0:1], s[2:3]
	s_cbranch_execz .LBB0_1152
	v_lshl_add_u64 v[2:3], v[202:203], 0, s[20:21]
	s_add_i32 s43, s70, 0x6000
	s_mov_b32 m0, s43
	s_nop 0
	global_load_lds_dwordx4 v[2:3], off
.LBB0_1152:
	s_or_b64 exec, exec, s[0:1]
	s_cmp_lg_u32 0, -1
	v_lshlrev_b32_e32 v0, 10, v210
	v_lshlrev_b32_e32 v2, 4, v209
	s_cselect_b32 s0, 0, 0
	v_add3_u32 v213, 0, v0, v2
	v_lshl_add_u64 v[2:3], v[200:201], 0, s[12:13]
	s_add_i32 s0, s0, s42
	s_add_i32 s0, s0, 0xb000
	s_mov_b32 m0, s0
	s_nop 0
	global_load_lds_dwordx4 v[2:3], off
	v_mov_b32_e32 v2, v1
	v_mov_b32_e32 v3, v1
	v_mov_b32_e32 v4, v1
	v_mov_b32_e32 v5, v1
	v_mov_b32_e32 v6, v1
	v_mov_b32_e32 v7, v1
	v_mov_b32_e32 v8, v1
	v_mov_b32_e32 v9, v1
	v_mov_b32_e32 v10, v1
	v_mov_b32_e32 v11, v1
	v_mov_b32_e32 v12, v1
	v_mov_b32_e32 v13, v1
	v_mov_b32_e32 v14, v1
	v_mov_b32_e32 v15, v1
	v_mov_b32_e32 v0, v1
	v_mov_b64_e32 v[16:17], v[14:15]
	v_mov_b64_e32 v[14:15], v[12:13]
	v_mov_b64_e32 v[12:13], v[10:11]
	v_mov_b64_e32 v[10:11], v[8:9]
	v_mov_b64_e32 v[8:9], v[6:7]
	v_mov_b64_e32 v[6:7], v[4:5]
	v_mov_b64_e32 v[4:5], v[2:3]
	v_mov_b64_e32 v[2:3], v[0:1]
	s_waitcnt vmcnt(6) lgkmcnt(0)
	s_barrier
; #define MLA_PIN(x) asm volatile("" : "+v"(x))
; #define MLA_LDK(kp, d0, h) (*(const __attribute__((address_space(3))) bf16x8*)((kp) + (d0) * 2048 + (h) * 512))
; #define MLA_MF(C, K, Q) C = __builtin_amdgcn_mfma_f32_32x32x16_bf16(K, Q, C, 0, 0, 0)
; template <int THRL, bool LATE> __device__ __forceinline__ void unit_stag(int b, int h, int qb, const unsigned short* Q, const unsigned short* KV, const unsigned short* KPE, unsigned short* O, char* shm, const int wave_) {
;     ...
;     { const lds_cptr kp = kp0;
;       pA0 = f32x16{}; pA1 = f32x16{};
; #pragma unroll
;       for (int d0 = 0; d0 < 6; ++d0) { const bf16x8 k0 = MLA_LDK(kp, d0, 0), k1 = MLA_LDK(kp, d0, 1); MLA_MF(pA0, k0, qr[d0]); MLA_MF(pA1, k1, qr[d0]); } }
;     { const float rm_ = rowmax(pA0, pA1); mhat = rm_;
; #pragma unroll
;       for (int r = 0; r < 16; ++r) { pA0[r] -= rm_; pA1[r] -= rm_; negm[r] = -mhat; }
;       MLA_PIN(negm); }
;     int t = 0;
;     MLA_STEPS(pB0, pB1, pA0, pA1, t, -1, 3, true, true, false); ++t;
	ds_read_b128 v[2:5], v213
	ds_read_b128 v[6:9], v213 offset:512
	s_waitcnt vmcnt(5) lgkmcnt(1)
	v_mfma_f32_32x32x16_bf16 v[18:33], v[2:5], v[196:199], 0
	ds_read_b128 v[36:39], v213 offset:2048
	ds_read_b128 v[40:43], v213 offset:2560
	s_waitcnt lgkmcnt(2)
	v_mfma_f32_32x32x16_bf16 v[2:17], v[6:9], v[196:199], 0
	s_waitcnt vmcnt(4) lgkmcnt(1)
	v_mfma_f32_32x32x16_bf16 v[18:33], v[36:39], v[192:195], v[18:33]
	s_waitcnt lgkmcnt(0)
	v_mfma_f32_32x32x16_bf16 v[2:17], v[40:43], v[192:195], v[2:17]
	ds_read_b128 v[36:39], v213 offset:4096
	ds_read_b128 v[40:43], v213 offset:4608
	s_waitcnt vmcnt(3) lgkmcnt(1)
	v_mfma_f32_32x32x16_bf16 v[18:33], v[36:39], v[188:191], v[18:33]
	s_waitcnt lgkmcnt(0)
	v_mfma_f32_32x32x16_bf16 v[2:17], v[40:43], v[188:191], v[2:17]
	ds_read_b128 v[36:39], v213 offset:6144
	ds_read_b128 v[40:43], v213 offset:6656
	s_waitcnt vmcnt(2) lgkmcnt(1)
	v_mfma_f32_32x32x16_bf16 v[18:33], v[36:39], v[184:187], v[18:33]
	s_waitcnt lgkmcnt(0)
	v_mfma_f32_32x32x16_bf16 v[2:17], v[40:43], v[184:187], v[2:17]
	ds_read_b128 v[36:39], v213 offset:8192
	ds_read_b128 v[40:43], v213 offset:8704
	s_waitcnt vmcnt(1) lgkmcnt(1)
	v_mfma_f32_32x32x16_bf16 v[18:33], v[36:39], v[180:183], v[18:33]
	s_waitcnt lgkmcnt(0)
	v_mfma_f32_32x32x16_bf16 v[2:17], v[40:43], v[180:183], v[2:17]
	ds_read_b128 v[36:39], v213 offset:10240
	ds_read_b128 v[40:43], v213 offset:10752
	s_waitcnt vmcnt(0) lgkmcnt(1)
	v_mfma_f32_32x32x16_bf16 v[18:33], v[36:39], v[176:179], v[18:33]
	s_waitcnt lgkmcnt(0)
	v_mfma_f32_32x32x16_bf16 v[2:17], v[40:43], v[176:179], v[2:17]
	v_max3_f32 v0, v18, v19, v2
	v_max3_f32 v36, v20, v21, v3
	s_nop 0
	v_max3_f32 v0, v0, v4, v5
	v_max3_f32 v36, v36, v24, v25
	s_nop 0
	v_max3_f32 v0, v0, v22, v23
	v_max3_f32 v36, v36, v8, v9
	s_nop 0
	v_max3_f32 v0, v0, v6, v7
	v_max3_f32 v36, v36, v28, v29
	s_nop 0
	v_max3_f32 v0, v0, v26, v27
	v_max3_f32 v36, v36, v12, v13
	s_nop 0
	v_max3_f32 v0, v0, v10, v11
	v_max3_f32 v36, v36, v32, v33
	s_nop 0
	v_max3_f32 v0, v0, v30, v31
	v_max3_f32 v36, v36, v16, v17
	s_nop 0
	v_max3_f32 v0, v0, v14, v15
	v_max_f32_e32 v36, v36, v36
	v_max_f32_e32 v0, v0, v0
	v_max_f32_e32 v0, v0, v36
	v_mov_b32_e32 v36, v0
	s_nop 1
	v_permlane32_swap_b32_e32 v0, v36
	v_max_f32_e32 v36, v36, v36
	v_max_f32_e32 v0, v0, v0
	v_max_f32_e32 v0, v0, v36
	v_xor_b32_e32 v82, 0x80000000, v0
	v_mov_b32_e32 v83, v82
	v_mov_b32_e32 v84, v82
	v_mov_b32_e32 v85, v82
	v_mov_b32_e32 v86, v82
	v_mov_b32_e32 v87, v82
	v_mov_b32_e32 v88, v82
	v_mov_b32_e32 v89, v82
	v_mov_b32_e32 v90, v82
	v_mov_b32_e32 v91, v82
	v_mov_b32_e32 v92, v82
	v_mov_b32_e32 v93, v82
	v_mov_b32_e32 v94, v82
	v_mov_b32_e32 v95, v82
	v_mov_b32_e32 v96, v82
	v_mov_b32_e32 v97, v82
	s_waitcnt vmcnt(3) lgkmcnt(0)
	s_barrier
	v_sub_f32_e32 v48, v2, v0
	v_sub_f32_e32 v2, v19, v0
	v_sub_f32_e32 v18, v18, v0
	v_sub_f32_e32 v49, v3, v0
	v_sub_f32_e32 v3, v20, v0
	v_sub_f32_e32 v50, v4, v0
	v_sub_f32_e32 v4, v21, v0
	v_sub_f32_e32 v51, v5, v0
	v_pk_add_f32 v[22:23], v[22:23], v[0:1] op_sel_hi:[1,0] neg_lo:[0,1] neg_hi:[0,1]
	v_pk_add_f32 v[6:7], v[6:7], v[0:1] op_sel_hi:[1,0] neg_lo:[0,1] neg_hi:[0,1]
	v_pk_add_f32 v[24:25], v[24:25], v[0:1] op_sel_hi:[1,0] neg_lo:[0,1] neg_hi:[0,1]
	v_pk_add_f32 v[8:9], v[8:9], v[0:1] op_sel_hi:[1,0] neg_lo:[0,1] neg_hi:[0,1]
	v_pk_add_f32 v[26:27], v[26:27], v[0:1] op_sel_hi:[1,0] neg_lo:[0,1] neg_hi:[0,1]
	v_pk_add_f32 v[10:11], v[10:11], v[0:1] op_sel_hi:[1,0] neg_lo:[0,1] neg_hi:[0,1]
	v_pk_add_f32 v[28:29], v[28:29], v[0:1] op_sel_hi:[1,0] neg_lo:[0,1] neg_hi:[0,1]
	v_pk_add_f32 v[12:13], v[12:13], v[0:1] op_sel_hi:[1,0] neg_lo:[0,1] neg_hi:[0,1]
	v_pk_add_f32 v[30:31], v[30:31], v[0:1] op_sel_hi:[1,0] neg_lo:[0,1] neg_hi:[0,1]
	v_pk_add_f32 v[14:15], v[14:15], v[0:1] op_sel_hi:[1,0] neg_lo:[0,1] neg_hi:[0,1]
	v_pk_add_f32 v[32:33], v[32:33], v[0:1] op_sel_hi:[1,0] neg_lo:[0,1] neg_hi:[0,1]
	v_pk_add_f32 v[16:17], v[16:17], v[0:1] op_sel_hi:[1,0] neg_lo:[0,1] neg_hi:[0,1]
	s_setprio 1
	v_exp_f32_e32 v19, v2
	v_exp_f32_e32 v20, v3
	v_exp_f32_e32 v21, v4
	ds_read_b128 v[2:5], v213 offset:12288
	ds_read_b128 v[36:39], v213 offset:12800
	v_exp_f32_e32 v18, v18
	s_nop 0
	v_exp_f32_e32 v22, v22
	v_exp_f32_e32 v23, v23
	v_exp_f32_e32 v24, v24
	v_exp_f32_e32 v25, v25
	s_waitcnt lgkmcnt(1)
	v_mfma_f32_32x32x16_bf16 v[98:113], v[2:5], v[196:199], v[82:97]
	ds_read_b128 v[40:43], v213 offset:14336
	ds_read_b128 v[44:47], v213 offset:14848
	v_exp_f32_e32 v26, v26
	v_exp_f32_e32 v27, v27
	v_exp_f32_e32 v28, v28
	v_exp_f32_e32 v29, v29
	s_waitcnt lgkmcnt(2)
	v_mfma_f32_32x32x16_bf16 v[114:129], v[36:39], v[196:199], v[82:97]
	v_exp_f32_e32 v30, v30
	v_exp_f32_e32 v31, v31
	v_exp_f32_e32 v32, v32
	v_exp_f32_e32 v33, v33
	s_nop 0
	v_add_f32_e32 v2, 0, v18
	v_add_f32_e32 v2, v19, v2
	v_add_f32_e32 v2, v20, v2
	v_add_f32_e32 v52, v21, v2
	s_waitcnt lgkmcnt(1)
	v_mfma_f32_32x32x16_bf16 v[98:113], v[40:43], v[192:195], v[98:113]
	v_exp_f32_e32 v2, v48
	v_exp_f32_e32 v3, v49
	v_exp_f32_e32 v4, v50
	v_exp_f32_e32 v5, v51
	ds_read_b128 v[36:39], v213 offset:16384
	ds_read_b128 v[48:51], v213 offset:16896
	v_add_f32_e32 v40, v52, v22
	v_add_f32_e32 v40, v23, v40
	v_add_f32_e32 v40, v24, v40
	v_add_f32_e32 v40, v25, v40
	s_waitcnt lgkmcnt(2)
	v_mfma_f32_32x32x16_bf16 v[114:129], v[44:47], v[192:195], v[114:129]
	v_add_f32_e32 v40, v26, v40
	v_add_f32_e32 v40, v27, v40
	v_add_f32_e32 v40, v28, v40
	v_exp_f32_e32 v6, v6
	v_exp_f32_e32 v7, v7
	v_exp_f32_e32 v8, v8
	v_exp_f32_e32 v9, v9
	v_add_f32_e32 v44, v29, v40
	v_cvt_pk_bf16_f32 v160, v18, v19
	v_cvt_pk_bf16_f32 v161, v20, v21
	s_waitcnt lgkmcnt(1)
; __device__ __forceinline__ void pv(f32x16* o, int vb, bf16x8 pa0, bf16x8 pa1, bf16x8 pa2, bf16x8 pa3) {
; #pragma unroll
;     for (int d0 = 0; d0 < 2; ++d0) { s16x4 lo[4], hi[4];
; #pragma unroll
;         for (int ks = 0; ks < 4; ++ks) {
;             asm volatile("ds_read_b64_tr_b16 %0,%1 offset:%c2" : "=&v"(lo[ks]) : "v"(vb), "i"(d0 * 4096 + ks * 1024) : "memory");
;             asm volatile("ds_read_b64_tr_b16 %0,%1 offset:%c2" : "=&v"(hi[ks]) : "v"(vb), "i"(d0 * 4096 + ks * 1024 + 512) : "memory"); }
;         asm volatile("s_waitcnt lgkmcnt(0)" ::: "memory"); __builtin_amdgcn_sched_barrier(0);
;     ...
;         o[d0] = __builtin_amdgcn_mfma_f32_32x32x16_bf16(pa0, MLA_PK(0), o[d0], 0, 0, 0);
;         o[d0] = __builtin_amdgcn_mfma_f32_32x32x16_bf16(pa1, MLA_PK(1), o[d0], 0, 0, 0);
;         o[d0] = __builtin_amdgcn_mfma_f32_32x32x16_bf16(pa2, MLA_PK(2), o[d0], 0, 0, 0);
;         o[d0] = __builtin_amdgcn_mfma_f32_32x32x16_bf16(pa3, MLA_PK(3), o[d0], 0, 0, 0);
;     ...
;     }
; }
	v_mfma_f32_32x32x16_bf16 v[98:113], v[36:39], v[188:191], v[98:113]
	ds_read_b128 v[18:21], v213 offset:18432
	ds_read_b128 v[40:43], v213 offset:18944
	v_add_f32_e32 v36, v30, v44
	v_add_f32_e32 v36, v31, v36
	v_add_f32_e32 v36, v32, v36
	v_exp_f32_e32 v10, v10
	v_exp_f32_e32 v11, v11
	v_exp_f32_e32 v12, v12
	v_exp_f32_e32 v13, v13
	v_add_f32_e32 v36, v33, v36
	v_cvt_pk_bf16_f32 v162, v22, v23
	v_cvt_pk_bf16_f32 v163, v24, v25
	s_waitcnt lgkmcnt(2)
	v_mfma_f32_32x32x16_bf16 v[114:129], v[48:51], v[188:191], v[114:129]
	v_exp_f32_e32 v14, v14
	v_exp_f32_e32 v15, v15
	v_exp_f32_e32 v16, v16
	v_exp_f32_e32 v17, v17
	v_cvt_pk_bf16_f32 v164, v26, v27
	v_add_f32_e32 v22, v36, v2
	v_add_f32_e32 v22, v3, v22
	v_add_f32_e32 v22, v4, v22
	v_add_f32_e32 v36, v5, v22
	v_cvt_pk_bf16_f32 v165, v28, v29
	s_waitcnt lgkmcnt(1)
	v_mfma_f32_32x32x16_bf16 v[98:113], v[18:21], v[184:187], v[98:113]
	ds_read_b128 v[22:25], v213 offset:20480
	ds_read_b128 v[26:29], v213 offset:20992
	v_add_f32_e32 v36, v36, v6
	v_add_f32_e32 v36, v7, v36
	v_add_f32_e32 v36, v8, v36
	v_add_f32_e32 v36, v9, v36
	v_cvt_pk_bf16_f32 v166, v30, v31
	v_cvt_pk_bf16_f32 v167, v32, v33
	s_waitcnt lgkmcnt(2)
	v_mfma_f32_32x32x16_bf16 v[114:129], v[40:43], v[184:187], v[114:129]
	v_add_f32_e32 v18, v10, v36
	v_add_f32_e32 v18, v11, v18
	v_add_f32_e32 v18, v12, v18
	v_add_f32_e32 v36, v13, v18
	v_cvt_pk_bf16_f32 v168, v2, v3
	v_cvt_pk_bf16_f32 v169, v4, v5
	s_waitcnt lgkmcnt(1)
	v_mfma_f32_32x32x16_bf16 v[98:113], v[22:25], v[180:183], v[98:113]
	ds_read_b128 v[18:21], v213 offset:22528
	ds_read_b128 v[30:33], v213 offset:23040
	v_add_f32_e32 v2, v14, v36
	v_add_f32_e32 v2, v15, v2
	v_add_f32_e32 v2, v16, v2
	v_add_f32_e32 v2, v17, v2
	v_cvt_pk_bf16_f32 v170, v6, v7
	v_cvt_pk_bf16_f32 v171, v8, v9
	s_waitcnt lgkmcnt(2)
	v_mfma_f32_32x32x16_bf16 v[114:129], v[26:29], v[180:183], v[114:129]
	v_cvt_pk_bf16_f32 v172, v10, v11
	v_cvt_pk_bf16_f32 v173, v12, v13
	s_waitcnt lgkmcnt(1)
	v_mfma_f32_32x32x16_bf16 v[98:113], v[18:21], v[176:179], v[98:113]
	v_cvt_pk_bf16_f32 v174, v14, v15
	v_cvt_pk_bf16_f32 v175, v16, v17
	s_waitcnt lgkmcnt(0)
	v_mfma_f32_32x32x16_bf16 v[114:129], v[30:33], v[176:179], v[114:129]
	s_setprio 0
	v_lshl_add_u64 v[4:5], v[204:205], 0, s[22:23]
	s_mov_b32 m0, s44
	s_nop 0
	global_load_lds_dwordx4 v[4:5], off
	s_and_saveexec_b64 s[0:1], s[2:3]
	s_cbranch_execz .LBB0_1154
	v_lshl_add_u64 v[4:5], v[202:203], 0, s[26:27]
	s_mov_b32 m0, s70
	s_nop 0
	global_load_lds_dwordx4 v[4:5], off
.LBB0_1154:
	s_or_b64 exec, exec, s[0:1]
	s_and_b32 s0, s10, 0x3fffffc0
	s_cmp_lg_u32 0, -1
	v_add_f32_e32 v216, 0, v2
	v_lshlrev_b32_e32 v2, 1, v34
	s_cselect_b32 s1, 0, 0
	v_and_b32_e32 v2, 32, v2
	v_lshlrev_b32_e32 v3, 4, v34
	s_add_i32 s10, s1, 0x9000
	s_lshl_b32 s0, s0, 2
	v_and_b32_e32 v3, 0xc0, v3
	v_add3_u32 v2, v2, s10, v35
	s_add_i32 s69, s0, 0
	v_lshlrev_b32_e32 v4, 8, v210
	s_add_i32 s0, s1, s42
	v_add3_u32 v211, v2, v3, v4
	v_lshl_add_u64 v[2:3], v[200:201], 0, s[18:19]
	s_add_i32 s0, s0, 0xd000
	s_mov_b32 m0, s0
	s_nop 0
	global_load_lds_dwordx4 v[2:3], off
	ds_read_b64_tr_b16 v[2:3],v211 offset:0
	ds_read_b64_tr_b16 v[4:5],v211 offset:512
	ds_read_b64_tr_b16 v[6:7],v211 offset:1024
	ds_read_b64_tr_b16 v[8:9],v211 offset:1536
	ds_read_b64_tr_b16 v[10:11],v211 offset:2048
	ds_read_b64_tr_b16 v[12:13],v211 offset:2560
	ds_read_b64_tr_b16 v[14:15],v211 offset:3072
	ds_read_b64_tr_b16 v[16:17],v211 offset:3584
	s_waitcnt lgkmcnt(0)
	s_add_i32 s69, s69, 0x11000
	v_mfma_f32_32x32x16_bf16 v[130:145], v[160:163], v[2:5], 0
	ds_read_b64_tr_b16 v[2:3],v211 offset:4096
	ds_read_b64_tr_b16 v[4:5],v211 offset:4608
	v_mfma_f32_32x32x16_bf16 v[130:145], v[164:167], v[6:9], v[130:145]
	ds_read_b64_tr_b16 v[6:7],v211 offset:5120
	ds_read_b64_tr_b16 v[8:9],v211 offset:5632
	v_mfma_f32_32x32x16_bf16 v[130:145], v[168:171], v[10:13], v[130:145]
	ds_read_b64_tr_b16 v[10:11],v211 offset:6144
	ds_read_b64_tr_b16 v[12:13],v211 offset:6656
	ds_read_b64_tr_b16 v[218:219],v211 offset:7168
	ds_read_b64_tr_b16 v[220:221],v211 offset:7680
	s_waitcnt lgkmcnt(0)
	v_mfma_f32_32x32x16_bf16 v[130:145], v[172:175], v[14:17], v[130:145]
	v_mfma_f32_32x32x16_bf16 v[146:161], v[160:163], v[2:5], 0
	v_max3_f32 v14, v98, v99, v114
	v_max3_f32 v15, v100, v101, v115
	s_mov_b64 s[0:1], -1
	v_max3_f32 v14, v14, v116, v117
	v_max3_f32 v15, v15, v104, v105
	v_mfma_f32_32x32x16_bf16 v[146:161], v[164:167], v[6:9], v[146:161]
	v_max3_f32 v14, v14, v102, v103
	v_max3_f32 v3, v15, v120, v121
	s_nop 0
	v_max3_f32 v2, v14, v118, v119
	v_max3_f32 v3, v3, v108, v109
	s_nop 0
	v_max3_f32 v2, v2, v106, v107
	v_mfma_f32_32x32x16_bf16 v[146:161], v[168:171], v[10:13], v[146:161]
	v_max3_f32 v2, v2, v122, v123
	v_max3_f32 v3, v3, v124, v125
	s_nop 0
	v_max3_f32 v2, v2, v110, v111
	v_max3_f32 v3, v3, v112, v113
	s_nop 0
	v_max3_f32 v2, v2, v126, v127
	v_max3_f32 v3, v3, v128, v129
	v_mfma_f32_32x32x16_bf16 v[146:161], v[172:175], v[218:221], v[146:161]
	v_max_f32_e32 v3, v3, v3
	v_max_f32_e32 v2, v2, v2
	v_max_f32_e32 v2, v2, v3
	v_mov_b32_e32 v3, v2
	s_nop 1
	v_permlane32_swap_b32_e32 v2, v3
	v_max_f32_e32 v3, v3, v3
	v_max_f32_e32 v2, v2, v2
	v_max_f32_e32 v164, v2, v3
	v_cmp_lt_f32_e32 vcc, s54, v164
	s_cbranch_vccnz .LBB0_1220
	s_and_b64 vcc, exec, s[0:1]
	s_cbranch_vccz .LBB0_1157
	v_mov_b64_e32 v[66:67], v[98:99]
	v_mov_b64_e32 v[18:19], v[146:147]
	v_mov_b64_e32 v[2:3], v[130:131]
	v_mov_b64_e32 v[50:51], v[114:115]
	v_mov_b64_e32 v[34:35], v[82:83]
	v_lshlrev_b32_e32 v214, 4, v210
	v_mov_b64_e32 v[68:69], v[100:101]
	v_mov_b64_e32 v[70:71], v[102:103]
	v_mov_b64_e32 v[72:73], v[104:105]
	v_mov_b64_e32 v[74:75], v[106:107]
	v_mov_b64_e32 v[76:77], v[108:109]
	v_mov_b64_e32 v[78:79], v[110:111]
	v_mov_b64_e32 v[80:81], v[112:113]
	v_mov_b64_e32 v[20:21], v[148:149]
	v_mov_b64_e32 v[22:23], v[150:151]
	v_mov_b64_e32 v[24:25], v[152:153]
	v_mov_b64_e32 v[26:27], v[154:155]
	v_mov_b64_e32 v[28:29], v[156:157]
	v_mov_b64_e32 v[30:31], v[158:159]
	v_mov_b64_e32 v[32:33], v[160:161]
	v_mov_b64_e32 v[4:5], v[132:133]
	v_mov_b64_e32 v[6:7], v[134:135]
	v_mov_b64_e32 v[8:9], v[136:137]
	v_mov_b64_e32 v[10:11], v[138:139]
	v_mov_b64_e32 v[12:13], v[140:141]
	v_mov_b64_e32 v[14:15], v[142:143]
	v_mov_b64_e32 v[16:17], v[144:145]
	v_mov_b64_e32 v[52:53], v[116:117]
	v_mov_b64_e32 v[54:55], v[118:119]
	v_mov_b64_e32 v[56:57], v[120:121]
	v_mov_b64_e32 v[58:59], v[122:123]
	v_mov_b64_e32 v[60:61], v[124:125]
	v_mov_b64_e32 v[62:63], v[126:127]
	v_mov_b64_e32 v[64:65], v[128:129]
	v_mov_b64_e32 v[36:37], v[84:85]
	v_mov_b64_e32 v[38:39], v[86:87]
	v_mov_b64_e32 v[40:41], v[88:89]
	v_mov_b64_e32 v[42:43], v[90:91]
	v_mov_b64_e32 v[44:45], v[92:93]
	v_mov_b64_e32 v[46:47], v[94:95]
	v_mov_b64_e32 v[48:49], v[96:97]
	v_mov_b32_e32 v215, v216
	v_mov_b32_e32 v212, v0

.LBB0_1158:
	s_mov_b32 s79, s45
	s_waitcnt vmcnt(3) lgkmcnt(0)
	s_barrier
	s_mul_i32 s72, s79, 0x3000
	s_mov_b32 s45, s42
	v_add_u32_e32 v133, s72, v213
	s_setprio 1
	ds_read_b128 v[82:85], v133
	ds_read_b128 v[116:119], v133 offset:512
	v_exp_f32_e32 v66, v66
	v_exp_f32_e32 v67, v67
	v_exp_f32_e32 v68, v68
	v_exp_f32_e32 v69, v69
	s_nop 0
	v_exp_f32_e32 v70, v70
	v_exp_f32_e32 v71, v71
	v_exp_f32_e32 v72, v72
	v_exp_f32_e32 v73, v73
	s_waitcnt lgkmcnt(1)
	v_mfma_f32_32x32x16_bf16 v[98:113], v[82:85], v[196:199], v[34:49]
	ds_read_b128 v[122:125], v133 offset:2048
	ds_read_b128 v[126:129], v133 offset:2560
	v_exp_f32_e32 v74, v74
	v_exp_f32_e32 v75, v75
	v_exp_f32_e32 v76, v76
	v_exp_f32_e32 v77, v77
	s_waitcnt lgkmcnt(2)
	v_mfma_f32_32x32x16_bf16 v[82:97], v[116:119], v[196:199], v[34:49]
	v_exp_f32_e32 v78, v78
	v_exp_f32_e32 v79, v79
	v_exp_f32_e32 v80, v80
	v_exp_f32_e32 v81, v81
	s_nop 0
	v_add_f32_e32 v0, 0, v66
	v_add_f32_e32 v0, v67, v0
	v_add_f32_e32 v0, v68, v0
	v_add_f32_e32 v0, v69, v0
	s_waitcnt lgkmcnt(1)
	v_mfma_f32_32x32x16_bf16 v[98:113], v[122:125], v[192:195], v[98:113]
	ds_read_b128 v[116:119], v133 offset:4096
	ds_read_b128 v[134:137], v133 offset:4608
	v_add_f32_e32 v0, v0, v70
	v_add_f32_e32 v0, v71, v0
	v_add_f32_e32 v0, v72, v0
	v_exp_f32_e32 v50, v50
	v_exp_f32_e32 v51, v51
	v_exp_f32_e32 v52, v52
	v_exp_f32_e32 v53, v53
	v_add_f32_e32 v0, v73, v0
	s_waitcnt lgkmcnt(2)
	v_mfma_f32_32x32x16_bf16 v[82:97], v[126:129], v[192:195], v[82:97]
	v_add_f32_e32 v0, v74, v0
	v_add_f32_e32 v0, v75, v0
	v_add_f32_e32 v0, v76, v0
	v_exp_f32_e32 v54, v54
	v_exp_f32_e32 v55, v55
	v_exp_f32_e32 v56, v56
	v_exp_f32_e32 v57, v57
	v_add_f32_e32 v0, v77, v0
	v_cvt_pk_bf16_f32 v160, v66, v67
	v_cvt_pk_bf16_f32 v161, v68, v69
	s_waitcnt lgkmcnt(1)
	v_mfma_f32_32x32x16_bf16 v[98:113], v[116:119], v[188:191], v[98:113]
	ds_read_b128 v[66:69], v133 offset:6144
	ds_read_b128 v[122:125], v133 offset:6656
	v_add_f32_e32 v0, v78, v0
	v_add_f32_e32 v0, v79, v0
	v_add_f32_e32 v0, v80, v0
	v_exp_f32_e32 v58, v58
	v_exp_f32_e32 v59, v59
	v_exp_f32_e32 v60, v60
	v_exp_f32_e32 v61, v61
	v_add_f32_e32 v0, v81, v0
	v_cvt_pk_bf16_f32 v162, v70, v71
	v_cvt_pk_bf16_f32 v163, v72, v73
	s_waitcnt lgkmcnt(2)
	v_mfma_f32_32x32x16_bf16 v[82:97], v[134:137], v[188:191], v[82:97]
	v_exp_f32_e32 v62, v62
	v_exp_f32_e32 v63, v63
	v_exp_f32_e32 v64, v64
	v_exp_f32_e32 v65, v65
	v_cvt_pk_bf16_f32 v164, v74, v75
	v_add_f32_e32 v0, v0, v50
	v_add_f32_e32 v0, v51, v0
	v_add_f32_e32 v0, v52, v0
	v_add_f32_e32 v0, v53, v0
	v_cvt_pk_bf16_f32 v165, v76, v77
	s_waitcnt lgkmcnt(1)
	v_mfma_f32_32x32x16_bf16 v[98:113], v[66:69], v[184:187], v[98:113]
	ds_read_b128 v[70:73], v133 offset:8192
	ds_read_b128 v[74:77], v133 offset:8704
	v_add_f32_e32 v0, v0, v54
	v_add_f32_e32 v0, v55, v0
	v_add_f32_e32 v0, v56, v0
	v_add_f32_e32 v0, v57, v0
	v_cvt_pk_bf16_f32 v166, v78, v79
	v_cvt_pk_bf16_f32 v167, v80, v81
	s_waitcnt lgkmcnt(2)
	v_mfma_f32_32x32x16_bf16 v[82:97], v[122:125], v[184:187], v[82:97]
	v_add_f32_e32 v0, v58, v0
	v_add_f32_e32 v0, v59, v0
	v_add_f32_e32 v0, v60, v0
	v_add_f32_e32 v0, v61, v0
	v_cvt_pk_bf16_f32 v168, v50, v51
	v_cvt_pk_bf16_f32 v169, v52, v53
	s_waitcnt lgkmcnt(1)
	v_mfma_f32_32x32x16_bf16 v[98:113], v[70:73], v[180:183], v[98:113]
	ds_read_b128 v[50:53], v133 offset:10240
	ds_read_b128 v[66:69], v133 offset:10752
	v_add_f32_e32 v0, v62, v0
	v_add_f32_e32 v0, v63, v0
	v_add_f32_e32 v0, v64, v0
	v_add_f32_e32 v0, v65, v0
	v_cvt_pk_bf16_f32 v170, v54, v55
	v_cvt_pk_bf16_f32 v171, v56, v57
	s_waitcnt lgkmcnt(2)
	v_mfma_f32_32x32x16_bf16 v[82:97], v[74:77], v[180:183], v[82:97]
	v_cvt_pk_bf16_f32 v172, v58, v59
	v_cvt_pk_bf16_f32 v173, v60, v61
	s_waitcnt lgkmcnt(1)
	v_mfma_f32_32x32x16_bf16 v[98:113], v[50:53], v[176:179], v[98:113]
	v_cvt_pk_bf16_f32 v174, v62, v63
	v_cvt_pk_bf16_f32 v175, v64, v65
	s_waitcnt lgkmcnt(0)
	v_mfma_f32_32x32x16_bf16 v[82:97], v[66:69], v[176:179], v[82:97]
	s_setprio 0
	v_lshl_add_u64 v[116:117], v[204:205], 0, s[0:1]
	s_mul_i32 s76, s42, 0x3000
	v_lshl_add_u64 v[50:51], v[116:117], 0, s[12:13]
	s_add_i32 s46, s76, s44
	s_mov_b32 m0, s46
	s_nop 0
	global_load_lds_dwordx4 v[50:51], off
	s_and_saveexec_b64 s[42:43], s[2:3]
	s_cbranch_execz .LBB0_1160
	s_add_i32 s73, s76, s70
	v_lshl_add_u64 v[50:51], v[114:115], 0, s[30:31]
	s_mov_b32 m0, s73
	s_nop 0
	global_load_lds_dwordx4 v[50:51], off
.LBB0_1160:
	s_or_b64 exec, exec, s[42:43]
	s_add_i32 s42, s81, 0x2000
	s_and_b32 s73, s42, 0x6000
	v_lshl_add_u64 v[118:119], v[200:201], 0, s[0:1]
	s_add_i32 s74, s73, s71
	s_mov_b32 m0, s74
	s_nop 0
	global_load_lds_dwordx4 v[118:119], off
	s_add_i32 s42, s81, 0xffffe000
	s_and_b32 s80, s42, 0x6000
	v_add_f32_e32 v121, v215, v0
	v_add_u32_e32 v0, s80, v211
	ds_read_b64_tr_b16 v[50:51],v0 offset:0
	ds_read_b64_tr_b16 v[52:53],v0 offset:512
	ds_read_b64_tr_b16 v[54:55],v0 offset:1024
	ds_read_b64_tr_b16 v[56:57],v0 offset:1536
	ds_read_b64_tr_b16 v[58:59],v0 offset:2048
	ds_read_b64_tr_b16 v[60:61],v0 offset:2560
	ds_read_b64_tr_b16 v[62:63],v0 offset:3072
	ds_read_b64_tr_b16 v[64:65],v0 offset:3584
	s_waitcnt lgkmcnt(0)
	s_nop 0
	v_mfma_f32_32x32x16_bf16 v[2:17], v[160:163], v[50:53], v[2:17]
	ds_read_b64_tr_b16 v[50:51],v0 offset:4096
	ds_read_b64_tr_b16 v[52:53],v0 offset:4608
	v_mfma_f32_32x32x16_bf16 v[2:17], v[164:167], v[54:57], v[2:17]
	ds_read_b64_tr_b16 v[54:55],v0 offset:5120
	ds_read_b64_tr_b16 v[56:57],v0 offset:5632
	v_mfma_f32_32x32x16_bf16 v[2:17], v[168:171], v[58:61], v[2:17]
	ds_read_b64_tr_b16 v[58:59],v0 offset:6144
	ds_read_b64_tr_b16 v[60:61],v0 offset:6656
	ds_read_b64_tr_b16 v[66:67],v0 offset:7168
	ds_read_b64_tr_b16 v[68:69],v0 offset:7680
	s_waitcnt lgkmcnt(0)
	v_mfma_f32_32x32x16_bf16 v[2:17], v[172:175], v[62:65], v[2:17]
	v_mfma_f32_32x32x16_bf16 v[18:33], v[160:163], v[50:53], v[18:33]
	v_max3_f32 v0, v98, v99, v82
	v_max3_f32 v62, v100, v101, v83
	s_nop 0
	v_max3_f32 v0, v0, v84, v85
	v_max3_f32 v50, v62, v104, v105
	s_nop 0
	v_max3_f32 v0, v0, v102, v103
	v_mfma_f32_32x32x16_bf16 v[18:33], v[164:167], v[54:57], v[18:33]
	v_max3_f32 v0, v0, v86, v87
	v_max3_f32 v50, v50, v88, v89
	s_nop 0
	v_max3_f32 v0, v0, v106, v107
	v_max3_f32 v50, v50, v108, v109
	s_nop 0
	v_max3_f32 v0, v0, v90, v91
	v_mfma_f32_32x32x16_bf16 v[18:33], v[168:171], v[58:61], v[18:33]
	v_max3_f32 v50, v50, v92, v93
	v_max3_f32 v0, v0, v110, v111
	s_nop 0
	v_max3_f32 v50, v50, v112, v113
	v_max3_f32 v0, v0, v94, v95
	s_nop 0
	v_max3_f32 v50, v50, v96, v97
	v_mfma_f32_32x32x16_bf16 v[18:33], v[172:175], v[66:69], v[18:33]
	v_max_f32_e32 v50, v50, v50
	v_max_f32_e32 v0, v0, v0
	v_max_f32_e32 v0, v0, v50
	v_mov_b32_e32 v50, v0
	s_nop 1
	v_permlane32_swap_b32_e32 v0, v50
	v_max_f32_e32 v50, v50, v50
	v_max_f32_e32 v0, v0, v0
	v_max_f32_e32 v0, v0, v50
	v_cmp_lt_f32_e32 vcc, s54, v0
	s_cbranch_vccnz .LBB0_1166
.LBB0_1161:
	s_waitcnt vmcnt(3) lgkmcnt(0)
	s_barrier
	s_mul_i32 s82, s47, 0x3000
	v_add_u32_e32 v132, s82, v213
	s_setprio 1
	ds_read_b128 v[50:53], v132
	ds_read_b128 v[122:125], v132 offset:512
	v_exp_f32_e32 v98, v98
	v_exp_f32_e32 v99, v99
	v_exp_f32_e32 v100, v100
	v_exp_f32_e32 v101, v101
	s_nop 0
	v_exp_f32_e32 v102, v102
	v_exp_f32_e32 v103, v103
	v_exp_f32_e32 v104, v104
	v_exp_f32_e32 v105, v105
	s_waitcnt lgkmcnt(1)
	v_mfma_f32_32x32x16_bf16 v[66:81], v[50:53], v[196:199], v[34:49]
	ds_read_b128 v[126:129], v132 offset:2048
	ds_read_b128 v[134:137], v132 offset:2560
	v_exp_f32_e32 v106, v106
	v_exp_f32_e32 v107, v107
	v_exp_f32_e32 v108, v108
	v_exp_f32_e32 v109, v109
	s_waitcnt lgkmcnt(2)
	v_mfma_f32_32x32x16_bf16 v[50:65], v[122:125], v[196:199], v[34:49]
	v_exp_f32_e32 v110, v110
	v_exp_f32_e32 v111, v111
	v_exp_f32_e32 v112, v112
	v_exp_f32_e32 v113, v113
	s_nop 0
	v_add_f32_e32 v0, 0, v98
	v_add_f32_e32 v0, v99, v0
	v_add_f32_e32 v0, v100, v0
	v_add_f32_e32 v0, v101, v0
	s_waitcnt lgkmcnt(1)
	v_mfma_f32_32x32x16_bf16 v[66:81], v[126:129], v[192:195], v[66:81]
	ds_read_b128 v[122:125], v132 offset:4096
	ds_read_b128 v[138:141], v132 offset:4608
	v_add_f32_e32 v0, v0, v102
	v_add_f32_e32 v0, v103, v0
	v_add_f32_e32 v0, v104, v0
	v_exp_f32_e32 v82, v82
	v_exp_f32_e32 v83, v83
	v_exp_f32_e32 v84, v84
	v_exp_f32_e32 v85, v85
	v_add_f32_e32 v0, v105, v0
	s_waitcnt lgkmcnt(2)
	v_mfma_f32_32x32x16_bf16 v[50:65], v[134:137], v[192:195], v[50:65]
	v_add_f32_e32 v0, v106, v0
	v_add_f32_e32 v0, v107, v0
	v_add_f32_e32 v0, v108, v0
	v_exp_f32_e32 v86, v86
	v_exp_f32_e32 v87, v87
	v_exp_f32_e32 v88, v88
	v_exp_f32_e32 v89, v89
	v_add_f32_e32 v0, v109, v0
	v_cvt_pk_bf16_f32 v160, v98, v99
	v_cvt_pk_bf16_f32 v161, v100, v101
	s_waitcnt lgkmcnt(1)
	v_mfma_f32_32x32x16_bf16 v[66:81], v[122:125], v[188:191], v[66:81]
	ds_read_b128 v[98:101], v132 offset:6144
	ds_read_b128 v[126:129], v132 offset:6656
	v_add_f32_e32 v0, v110, v0
	v_add_f32_e32 v0, v111, v0
	v_add_f32_e32 v0, v112, v0
	v_exp_f32_e32 v90, v90
	v_exp_f32_e32 v91, v91
	v_exp_f32_e32 v92, v92
	v_exp_f32_e32 v93, v93
	v_add_f32_e32 v0, v113, v0
	v_cvt_pk_bf16_f32 v162, v102, v103
	v_cvt_pk_bf16_f32 v163, v104, v105
	s_waitcnt lgkmcnt(2)
	v_mfma_f32_32x32x16_bf16 v[50:65], v[138:141], v[188:191], v[50:65]
	v_exp_f32_e32 v94, v94
	v_exp_f32_e32 v95, v95
	v_exp_f32_e32 v96, v96
	v_exp_f32_e32 v97, v97
	v_cvt_pk_bf16_f32 v164, v106, v107
	v_add_f32_e32 v0, v0, v82
	v_add_f32_e32 v0, v83, v0
	v_add_f32_e32 v0, v84, v0
	v_add_f32_e32 v0, v85, v0
	v_cvt_pk_bf16_f32 v165, v108, v109
	s_waitcnt lgkmcnt(1)
	v_mfma_f32_32x32x16_bf16 v[66:81], v[98:101], v[184:187], v[66:81]
	ds_read_b128 v[102:105], v132 offset:8192
	ds_read_b128 v[106:109], v132 offset:8704
	v_add_f32_e32 v0, v0, v86
	v_add_f32_e32 v0, v87, v0
	v_add_f32_e32 v0, v88, v0
	v_add_f32_e32 v0, v89, v0
	v_cvt_pk_bf16_f32 v166, v110, v111
	v_cvt_pk_bf16_f32 v167, v112, v113
	s_waitcnt lgkmcnt(2)
	v_mfma_f32_32x32x16_bf16 v[50:65], v[126:129], v[184:187], v[50:65]
	v_add_f32_e32 v0, v90, v0
	v_add_f32_e32 v0, v91, v0
	v_add_f32_e32 v0, v92, v0
	v_add_f32_e32 v0, v93, v0
	v_cvt_pk_bf16_f32 v168, v82, v83
	v_cvt_pk_bf16_f32 v169, v84, v85
	s_waitcnt lgkmcnt(1)
	v_mfma_f32_32x32x16_bf16 v[66:81], v[102:105], v[180:183], v[66:81]
	ds_read_b128 v[82:85], v132 offset:10240
	ds_read_b128 v[98:101], v132 offset:10752
	v_add_f32_e32 v0, v94, v0
	v_add_f32_e32 v0, v95, v0
	v_add_f32_e32 v0, v96, v0
	v_add_f32_e32 v0, v97, v0
	v_cvt_pk_bf16_f32 v170, v86, v87
	v_cvt_pk_bf16_f32 v171, v88, v89
	s_waitcnt lgkmcnt(2)
	v_mfma_f32_32x32x16_bf16 v[50:65], v[106:109], v[180:183], v[50:65]
	v_cvt_pk_bf16_f32 v172, v90, v91
	v_cvt_pk_bf16_f32 v173, v92, v93
	s_waitcnt lgkmcnt(1)
	v_mfma_f32_32x32x16_bf16 v[66:81], v[82:85], v[176:179], v[66:81]
	v_cvt_pk_bf16_f32 v174, v94, v95
	v_cvt_pk_bf16_f32 v175, v96, v97
	s_waitcnt lgkmcnt(0)
	v_mfma_f32_32x32x16_bf16 v[50:65], v[98:101], v[176:179], v[50:65]
	s_setprio 0
	v_lshl_add_u64 v[82:83], v[116:117], 0, s[18:19]
	s_add_i32 s42, s72, s44
	s_mov_b32 m0, s42
	s_nop 0
	global_load_lds_dwordx4 v[82:83], off
	s_and_saveexec_b64 s[42:43], s[2:3]
	s_cbranch_execz .LBB0_1163
	s_add_i32 s72, s72, s70
	s_mov_b32 m0, s72
	s_nop 0
	global_load_lds_dwordx4 v[114:115], off
.LBB0_1163:
	s_or_b64 exec, exec, s[42:43]
	s_add_i32 s72, s81, 0x4000
	s_and_b32 s77, s72, 0x6000
	s_add_i32 s42, s77, s71
	v_lshl_add_u64 v[82:83], v[118:119], 0, s[12:13]
	s_mov_b32 m0, s42
	s_nop 0
	global_load_lds_dwordx4 v[82:83], off
	s_and_b32 s42, s81, 0x6000
	v_add_f32_e32 v215, v121, v0
	v_add_u32_e32 v0, s42, v211
	ds_read_b64_tr_b16 v[82:83],v0 offset:0
	ds_read_b64_tr_b16 v[84:85],v0 offset:512
	ds_read_b64_tr_b16 v[86:87],v0 offset:1024
	ds_read_b64_tr_b16 v[88:89],v0 offset:1536
	ds_read_b64_tr_b16 v[90:91],v0 offset:2048
	ds_read_b64_tr_b16 v[92:93],v0 offset:2560
	ds_read_b64_tr_b16 v[94:95],v0 offset:3072
	ds_read_b64_tr_b16 v[96:97],v0 offset:3584
	s_waitcnt lgkmcnt(0)
	s_nop 0
	v_mfma_f32_32x32x16_bf16 v[2:17], v[160:163], v[82:85], v[2:17]
	ds_read_b64_tr_b16 v[82:83],v0 offset:4096
	ds_read_b64_tr_b16 v[84:85],v0 offset:4608
	v_mfma_f32_32x32x16_bf16 v[2:17], v[164:167], v[86:89], v[2:17]
	ds_read_b64_tr_b16 v[86:87],v0 offset:5120
	ds_read_b64_tr_b16 v[88:89],v0 offset:5632
	v_mfma_f32_32x32x16_bf16 v[2:17], v[168:171], v[90:93], v[2:17]
	ds_read_b64_tr_b16 v[90:91],v0 offset:6144
	ds_read_b64_tr_b16 v[92:93],v0 offset:6656
	ds_read_b64_tr_b16 v[98:99],v0 offset:7168
	ds_read_b64_tr_b16 v[100:101],v0 offset:7680
	s_waitcnt lgkmcnt(0)
	v_mfma_f32_32x32x16_bf16 v[2:17], v[172:175], v[94:97], v[2:17]
	v_mfma_f32_32x32x16_bf16 v[18:33], v[160:163], v[82:85], v[18:33]
	v_max3_f32 v0, v66, v67, v50
	v_max3_f32 v94, v68, v69, v51
	s_nop 0
	v_max3_f32 v0, v0, v52, v53
	v_max3_f32 v82, v94, v72, v73
	s_nop 0
	v_max3_f32 v0, v0, v70, v71
	v_mfma_f32_32x32x16_bf16 v[18:33], v[164:167], v[86:89], v[18:33]
	v_max3_f32 v0, v0, v54, v55
	v_max3_f32 v82, v82, v56, v57
	s_nop 0
	v_max3_f32 v0, v0, v74, v75
	v_max3_f32 v82, v82, v76, v77
	s_nop 0
	v_max3_f32 v0, v0, v58, v59
	v_mfma_f32_32x32x16_bf16 v[18:33], v[168:171], v[90:93], v[18:33]
	v_max3_f32 v82, v82, v60, v61
	v_max3_f32 v0, v0, v78, v79
	s_nop 0
	v_max3_f32 v82, v82, v80, v81
	v_max3_f32 v0, v0, v62, v63
	s_nop 0
	v_max3_f32 v82, v82, v64, v65
	v_mfma_f32_32x32x16_bf16 v[18:33], v[172:175], v[98:101], v[18:33]
	v_max_f32_e32 v82, v82, v82
	v_max_f32_e32 v0, v0, v0
	v_max_f32_e32 v0, v0, v82
	v_mov_b32_e32 v82, v0
	s_nop 1
	v_permlane32_swap_b32_e32 v0, v82
	v_max_f32_e32 v82, v82, v82
	v_max_f32_e32 v0, v0, v0
	v_max_f32_e32 v0, v0, v82
	v_cmp_lt_f32_e32 vcc, s54, v0
	s_cbranch_vccnz .LBB0_1169

.LBB0_1173:
	s_waitcnt vmcnt(3) lgkmcnt(0)
	s_barrier
	v_add_u32_e32 v130, s76, v213
	s_setprio 1
	ds_read_b128 v[98:101], v130
	ds_read_b128 v[114:117], v130 offset:512
	v_exp_f32_e32 v66, v66
	v_exp_f32_e32 v67, v67
	v_exp_f32_e32 v68, v68
	v_exp_f32_e32 v69, v69
	s_nop 0
	v_exp_f32_e32 v70, v70
	v_exp_f32_e32 v71, v71
	v_exp_f32_e32 v72, v72
	v_exp_f32_e32 v73, v73
	s_waitcnt lgkmcnt(1)
	v_mfma_f32_32x32x16_bf16 v[82:97], v[98:101], v[196:199], v[34:49]
	ds_read_b128 v[122:125], v130 offset:2048
	ds_read_b128 v[126:129], v130 offset:2560
	v_exp_f32_e32 v74, v74
	v_exp_f32_e32 v75, v75
	v_exp_f32_e32 v76, v76
	v_exp_f32_e32 v77, v77
	s_waitcnt lgkmcnt(2)
	v_mfma_f32_32x32x16_bf16 v[98:113], v[114:117], v[196:199], v[34:49]
	v_exp_f32_e32 v78, v78
	v_exp_f32_e32 v79, v79
	v_exp_f32_e32 v80, v80
	v_exp_f32_e32 v81, v81
	s_nop 0
	v_add_f32_e32 v0, 0, v66
	v_add_f32_e32 v0, v67, v0
	v_add_f32_e32 v0, v68, v0
	v_add_f32_e32 v0, v69, v0
	s_waitcnt lgkmcnt(1)
	v_mfma_f32_32x32x16_bf16 v[82:97], v[122:125], v[192:195], v[82:97]
	ds_read_b128 v[114:117], v130 offset:4096
	ds_read_b128 v[134:137], v130 offset:4608
	v_add_f32_e32 v0, v0, v70
	v_add_f32_e32 v0, v71, v0
	v_add_f32_e32 v0, v72, v0
	v_exp_f32_e32 v50, v50
	v_exp_f32_e32 v51, v51
	v_exp_f32_e32 v52, v52
	v_exp_f32_e32 v53, v53
	v_add_f32_e32 v0, v73, v0
	s_waitcnt lgkmcnt(2)
	v_mfma_f32_32x32x16_bf16 v[98:113], v[126:129], v[192:195], v[98:113]
	v_add_f32_e32 v0, v74, v0
	v_add_f32_e32 v0, v75, v0
	v_add_f32_e32 v0, v76, v0
	v_exp_f32_e32 v54, v54
	v_exp_f32_e32 v55, v55
	v_exp_f32_e32 v56, v56
	v_exp_f32_e32 v57, v57
	v_add_f32_e32 v0, v77, v0
	v_cvt_pk_bf16_f32 v160, v66, v67
	v_cvt_pk_bf16_f32 v161, v68, v69
	s_waitcnt lgkmcnt(1)
	v_mfma_f32_32x32x16_bf16 v[82:97], v[114:117], v[188:191], v[82:97]
	ds_read_b128 v[66:69], v130 offset:6144
	ds_read_b128 v[122:125], v130 offset:6656
	v_add_f32_e32 v0, v78, v0
	v_add_f32_e32 v0, v79, v0
	v_add_f32_e32 v0, v80, v0
	v_exp_f32_e32 v58, v58
	v_exp_f32_e32 v59, v59
	v_exp_f32_e32 v60, v60
	v_exp_f32_e32 v61, v61
	v_add_f32_e32 v0, v81, v0
	v_cvt_pk_bf16_f32 v162, v70, v71
	v_cvt_pk_bf16_f32 v163, v72, v73
	s_waitcnt lgkmcnt(2)
	v_mfma_f32_32x32x16_bf16 v[98:113], v[134:137], v[188:191], v[98:113]
	v_exp_f32_e32 v62, v62
	v_exp_f32_e32 v63, v63
	v_exp_f32_e32 v64, v64
	v_exp_f32_e32 v65, v65
	v_cvt_pk_bf16_f32 v164, v74, v75
	v_add_f32_e32 v0, v0, v50
	v_add_f32_e32 v0, v51, v0
	v_add_f32_e32 v0, v52, v0
	v_add_f32_e32 v0, v53, v0
	v_cvt_pk_bf16_f32 v165, v76, v77
	s_waitcnt lgkmcnt(1)
	v_mfma_f32_32x32x16_bf16 v[82:97], v[66:69], v[184:187], v[82:97]
	ds_read_b128 v[70:73], v130 offset:8192
	ds_read_b128 v[74:77], v130 offset:8704
	v_add_f32_e32 v0, v0, v54
	v_add_f32_e32 v0, v55, v0
	v_add_f32_e32 v0, v56, v0
	v_add_f32_e32 v0, v57, v0
	v_cvt_pk_bf16_f32 v166, v78, v79
	v_cvt_pk_bf16_f32 v167, v80, v81
	s_waitcnt lgkmcnt(2)
	v_mfma_f32_32x32x16_bf16 v[98:113], v[122:125], v[184:187], v[98:113]
	v_add_f32_e32 v0, v58, v0
	v_add_f32_e32 v0, v59, v0
	v_add_f32_e32 v0, v60, v0
	v_add_f32_e32 v0, v61, v0
	v_cvt_pk_bf16_f32 v168, v50, v51
	v_cvt_pk_bf16_f32 v169, v52, v53
	s_waitcnt lgkmcnt(1)
	v_mfma_f32_32x32x16_bf16 v[82:97], v[70:73], v[180:183], v[82:97]
	ds_read_b128 v[50:53], v130 offset:10240
	ds_read_b128 v[66:69], v130 offset:10752
	v_add_f32_e32 v0, v62, v0
	v_add_f32_e32 v0, v63, v0
	v_add_f32_e32 v0, v64, v0
	v_add_f32_e32 v0, v65, v0
	v_cvt_pk_bf16_f32 v170, v54, v55
	v_cvt_pk_bf16_f32 v171, v56, v57
	s_waitcnt lgkmcnt(2)
	v_mfma_f32_32x32x16_bf16 v[98:113], v[74:77], v[180:183], v[98:113]
	v_cvt_pk_bf16_f32 v172, v58, v59
	v_cvt_pk_bf16_f32 v173, v60, v61
	s_waitcnt lgkmcnt(1)
	v_mfma_f32_32x32x16_bf16 v[82:97], v[50:53], v[176:179], v[82:97]
	v_cvt_pk_bf16_f32 v174, v62, v63
	v_cvt_pk_bf16_f32 v175, v64, v65
	s_waitcnt lgkmcnt(0)
	v_mfma_f32_32x32x16_bf16 v[98:113], v[66:69], v[176:179], v[98:113]
	s_setprio 0
	s_add_i32 s10, s81, 5
	s_lshl_b64 s[42:43], s[10:11], 17
	v_lshl_add_u64 v[50:51], v[204:205], 0, s[42:43]
	s_add_i32 s44, s82, s44
	s_mov_b32 m0, s44
	s_nop 0
	global_load_lds_dwordx4 v[50:51], off
	s_and_saveexec_b64 s[44:45], s[2:3]
	s_cbranch_execz .LBB0_1175
	s_lshl_b64 s[78:79], s[10:11], 12
	s_add_i32 s47, s82, s70
	v_lshl_add_u64 v[50:51], v[202:203], 0, s[78:79]
	s_mov_b32 m0, s47
	s_nop 0
	global_load_lds_dwordx4 v[50:51], off
; __device__ __forceinline__ float max3f(float a, float b, float c) { float r; asm("v_max3_f32 %0, %1, %2, %3" : "=v"(r) : "v"(a), "v"(b), "v"(c)); return r; }
; __device__ __forceinline__ void cmask(f32x16& p0, f32x16& p1, int jb, int qrel, int hi) {
;     const float NEG = -INFINITY; const int kb = 64 * jb + 4 * hi;
; #pragma unroll
;     for (int r = 0; r < 16; ++r) { const int kv = kb + (r & 3) + 8 * (r >> 2); if (kv > qrel) p0[r] = NEG; if (kv + 32 > qrel) p1[r] = NEG; }
; }
; __device__ __forceinline__ float rowmax(const f32x16& p0, const f32x16& p1) {
;     float a = max3f(p0[0], p0[1], p1[0]), b = max3f(p0[2], p0[3], p1[1]); a = max3f(a, p1[2], p1[3]);
; #pragma unroll
;     for (int r = 4; r < 16; r += 4) { a = max3f(a, p0[r], p0[r + 1]); b = max3f(b, p0[r + 2], p0[r + 3]); a = max3f(a, p1[r], p1[r + 1]); b = max3f(b, p1[r + 2], p1[r + 3]); }
;     const float m = fmaxf(a, b);
;     auto rr = __builtin_amdgcn_permlane32_swap(__float_as_uint(m), __float_as_uint(m), false, false);
;     return fmaxf(__uint_as_float(rr[0]), __uint_as_float(rr[1]));
; }
; __device__ __forceinline__ void pv(f32x16* o, int vb, bf16x8 pa0, bf16x8 pa1, bf16x8 pa2, bf16x8 pa3) {
; #pragma unroll
;     for (int d0 = 0; d0 < 2; ++d0) { s16x4 lo[4], hi[4];
; #pragma unroll
;         for (int ks = 0; ks < 4; ++ks) {
;             asm volatile("ds_read_b64_tr_b16 %0,%1 offset:%c2" : "=&v"(lo[ks]) : "v"(vb), "i"(d0 * 4096 + ks * 1024) : "memory");
;             asm volatile("ds_read_b64_tr_b16 %0,%1 offset:%c2" : "=&v"(hi[ks]) : "v"(vb), "i"(d0 * 4096 + ks * 1024 + 512) : "memory"); }
;         asm volatile("s_waitcnt lgkmcnt(0)" ::: "memory"); __builtin_amdgcn_sched_barrier(0);
;     ...
;         o[d0] = __builtin_amdgcn_mfma_f32_32x32x16_bf16(pa0, MLA_PK(0), o[d0], 0, 0, 0);
;         o[d0] = __builtin_amdgcn_mfma_f32_32x32x16_bf16(pa1, MLA_PK(1), o[d0], 0, 0, 0);
;         o[d0] = __builtin_amdgcn_mfma_f32_32x32x16_bf16(pa2, MLA_PK(2), o[d0], 0, 0, 0);
;         o[d0] = __builtin_amdgcn_mfma_f32_32x32x16_bf16(pa3, MLA_PK(3), o[d0], 0, 0, 0);
;     ...
;     }
; }
.LBB0_1175:
	s_or_b64 exec, exec, s[44:45]
	v_lshl_add_u64 v[50:51], v[200:201], 0, s[0:1]
	s_add_i32 s0, s80, s71
	s_mov_b32 m0, s0
	s_nop 0
	global_load_lds_dwordx4 v[50:51], off
	v_add_f32_e32 v134, v215, v0
	v_add_u32_e32 v0, s73, v211
	ds_read_b64_tr_b16 v[50:51],v0 offset:0
	ds_read_b64_tr_b16 v[52:53],v0 offset:512
	ds_read_b64_tr_b16 v[54:55],v0 offset:1024
	ds_read_b64_tr_b16 v[56:57],v0 offset:1536
	ds_read_b64_tr_b16 v[58:59],v0 offset:2048
	ds_read_b64_tr_b16 v[60:61],v0 offset:2560
	ds_read_b64_tr_b16 v[62:63],v0 offset:3072
	ds_read_b64_tr_b16 v[64:65],v0 offset:3584
	s_waitcnt lgkmcnt(0)
	v_or_b32_e32 v131, s75, v209
	v_mfma_f32_32x32x16_bf16 v[2:17], v[160:163], v[50:53], v[2:17]
	ds_read_b64_tr_b16 v[52:53],v0 offset:4096
	v_mfma_f32_32x32x16_bf16 v[2:17], v[164:167], v[54:57], v[2:17]
	ds_read_b64_tr_b16 v[54:55],v0 offset:4608
	ds_read_b64_tr_b16 v[56:57],v0 offset:5120
	v_mfma_f32_32x32x16_bf16 v[2:17], v[168:171], v[58:61], v[2:17]
	ds_read_b64_tr_b16 v[58:59],v0 offset:5632
	ds_read_b64_tr_b16 v[70:71],v0 offset:6144
	ds_read_b64_tr_b16 v[72:73],v0 offset:6656
	ds_read_b64_tr_b16 v[74:75],v0 offset:7168
	ds_read_b64_tr_b16 v[76:77],v0 offset:7680
	s_waitcnt lgkmcnt(0)
	v_mfma_f32_32x32x16_bf16 v[2:17], v[172:175], v[62:65], v[2:17]
	v_mfma_f32_32x32x16_bf16 v[18:33], v[160:163], v[52:55], v[18:33]
	v_lshlrev_b32_e32 v129, 2, v210
	v_or_b32_e32 v0, 32, v129
	v_cmp_le_i32_e32 vcc, v0, v131
	v_or_b32_e32 v0, 33, v129
	v_or_b32_e32 v125, 2, v129
	v_cndmask_b32_e32 v50, v206, v98, vcc
	v_cmp_lt_i32_e32 vcc, v129, v131
	v_mfma_f32_32x32x16_bf16 v[18:33], v[164:167], v[56:59], v[18:33]
	v_or_b32_e32 v126, 3, v129
	v_cndmask_b32_e32 v67, v206, v83, vcc
	v_cmp_le_i32_e32 vcc, v129, v131
	v_or_b32_e32 v127, 8, v129
	v_or_b32_e32 v128, 9, v129
	v_cndmask_b32_e32 v66, v206, v82, vcc
	v_cmp_le_i32_e32 vcc, v0, v131
	v_or_b32_e32 v0, 34, v129
	v_mfma_f32_32x32x16_bf16 v[18:33], v[168:171], v[70:73], v[18:33]
	v_cndmask_b32_e32 v51, v206, v99, vcc
	v_cmp_le_i32_e32 vcc, v125, v131
	v_or_b32_e32 v124, 10, v129
	v_or_b32_e32 v123, 11, v129
	v_cndmask_b32_e32 v68, v206, v84, vcc
	v_cmp_le_i32_e32 vcc, v0, v131
	v_or_b32_e32 v0, 35, v129
	v_or_b32_e32 v122, 16, v129
	v_cndmask_b32_e32 v52, v206, v100, vcc
	v_cmp_le_i32_e32 vcc, v126, v131
	v_mfma_f32_32x32x16_bf16 v[18:33], v[172:175], v[74:77], v[18:33]
	v_or_b32_e32 v121, 17, v129
	v_cndmask_b32_e32 v69, v206, v85, vcc
	v_cmp_le_i32_e32 vcc, v0, v131
	v_or_b32_e32 v0, 40, v129
	v_or_b32_e32 v119, 18, v129
	v_cndmask_b32_e32 v53, v206, v101, vcc
	v_cmp_le_i32_e32 vcc, v127, v131
	v_or_b32_e32 v118, 19, v129
	v_or_b32_e32 v117, 24, v129
	v_cndmask_b32_e32 v70, v206, v86, vcc
	v_cmp_le_i32_e32 vcc, v0, v131
	v_or_b32_e32 v0, 41, v129
	v_or_b32_e32 v116, 25, v129
	v_cndmask_b32_e32 v54, v206, v102, vcc
	v_cmp_le_i32_e32 vcc, v128, v131
	v_or_b32_e32 v115, 26, v129
	v_or_b32_e32 v114, 27, v129
	v_cndmask_b32_e32 v71, v206, v87, vcc
	v_cmp_le_i32_e32 vcc, v0, v131
	v_or_b32_e32 v0, 42, v129
	v_max3_f32 v82, v68, v69, v51
	s_nop 0
	v_cndmask_b32_e32 v55, v206, v103, vcc
	v_cmp_le_i32_e32 vcc, v124, v131
	s_nop 1
	v_cndmask_b32_e32 v72, v206, v88, vcc
	v_cmp_le_i32_e32 vcc, v0, v131
	v_or_b32_e32 v0, 43, v129
	s_nop 0
	v_cndmask_b32_e32 v56, v206, v104, vcc
	v_cmp_le_i32_e32 vcc, v123, v131
	s_nop 1
	v_cndmask_b32_e32 v73, v206, v89, vcc
	v_cmp_le_i32_e32 vcc, v0, v131
	v_or_b32_e32 v0, 48, v129
	v_max3_f32 v82, v82, v72, v73
	s_nop 0
	v_cndmask_b32_e32 v57, v206, v105, vcc
	v_cmp_le_i32_e32 vcc, v122, v131
	v_max3_f32 v82, v82, v56, v57
	s_nop 1
	v_cndmask_b32_e32 v74, v206, v90, vcc
	v_cmp_le_i32_e32 vcc, v0, v131
	v_or_b32_e32 v0, 49, v129
	s_nop 0
	v_cndmask_b32_e32 v58, v206, v106, vcc
	v_cmp_le_i32_e32 vcc, v121, v131
	s_nop 1
	v_cndmask_b32_e32 v75, v206, v91, vcc
	v_cmp_le_i32_e32 vcc, v0, v131
	v_or_b32_e32 v0, 50, v129
	s_nop 0
	v_cndmask_b32_e32 v59, v206, v107, vcc
	v_cmp_le_i32_e32 vcc, v119, v131
	s_nop 1
	v_cndmask_b32_e32 v76, v206, v92, vcc
	v_cmp_le_i32_e32 vcc, v0, v131
	v_or_b32_e32 v0, 51, v129
	s_nop 0
	v_cndmask_b32_e32 v60, v206, v108, vcc
	v_cmp_le_i32_e32 vcc, v118, v131
	s_nop 1
	v_cndmask_b32_e32 v77, v206, v93, vcc
	v_cmp_le_i32_e32 vcc, v0, v131
	v_or_b32_e32 v0, 56, v129
	v_max3_f32 v82, v82, v76, v77
	s_nop 0
	v_cndmask_b32_e32 v61, v206, v109, vcc
	v_cmp_le_i32_e32 vcc, v117, v131
	v_max3_f32 v82, v82, v60, v61
	s_nop 1
	v_cndmask_b32_e32 v78, v206, v94, vcc
	v_cmp_le_i32_e32 vcc, v0, v131
	v_or_b32_e32 v0, 57, v129
	s_nop 0
	v_cndmask_b32_e32 v62, v206, v110, vcc
	v_cmp_le_i32_e32 vcc, v116, v131
	s_nop 1
	v_cndmask_b32_e32 v79, v206, v95, vcc
	v_cmp_le_i32_e32 vcc, v0, v131
	v_or_b32_e32 v0, 58, v129
	s_nop 0
	v_cndmask_b32_e32 v63, v206, v111, vcc
	v_cmp_le_i32_e32 vcc, v115, v131
	s_nop 1
	v_cndmask_b32_e32 v80, v206, v96, vcc
	v_cmp_le_i32_e32 vcc, v0, v131
	v_or_b32_e32 v0, 59, v129
	s_nop 0
	v_cndmask_b32_e32 v64, v206, v112, vcc
	v_cmp_le_i32_e32 vcc, v114, v131
	s_nop 1
	v_cndmask_b32_e32 v81, v206, v97, vcc
	v_cmp_le_i32_e32 vcc, v0, v131
	v_max3_f32 v0, v66, v67, v50
	v_max3_f32 v82, v82, v80, v81
	s_nop 0
	v_max3_f32 v0, v0, v52, v53
	s_nop 0
	v_max3_f32 v0, v0, v70, v71
	v_cndmask_b32_e32 v65, v206, v113, vcc
	v_max3_f32 v0, v0, v54, v55
	v_max3_f32 v82, v82, v64, v65
	s_nop 0
	v_max3_f32 v0, v0, v74, v75
	v_max_f32_e32 v82, v82, v82
	v_max3_f32 v0, v0, v58, v59
	s_nop 0
	v_max3_f32 v0, v0, v78, v79
	s_nop 0
	v_max3_f32 v0, v0, v62, v63
	s_nop 0
	v_max_f32_e32 v0, v0, v0
	v_max_f32_e32 v0, v0, v82
	v_mov_b32_e32 v82, v0
	s_nop 1
	v_permlane32_swap_b32_e32 v0, v82
	v_max_f32_e32 v82, v82, v82
	v_max_f32_e32 v0, v0, v0
	v_max_f32_e32 v0, v0, v82
	v_cmp_lt_f32_e32 vcc, s54, v0
	s_cbranch_vccnz .LBB0_1223
.LBB0_1176:
	s_waitcnt vmcnt(3) lgkmcnt(0)
	s_barrier
	s_setprio 1
	ds_read_b128 v[98:101], v133
	ds_read_b128 v[136:139], v133 offset:512
	v_exp_f32_e32 v66, v66
	v_exp_f32_e32 v67, v67
	v_exp_f32_e32 v68, v68
	v_exp_f32_e32 v69, v69
	s_nop 0
	v_exp_f32_e32 v70, v70
	v_exp_f32_e32 v71, v71
	v_exp_f32_e32 v72, v72
	v_exp_f32_e32 v73, v73
	s_waitcnt lgkmcnt(1)
	v_mfma_f32_32x32x16_bf16 v[82:97], v[98:101], v[196:199], v[34:49]
	ds_read_b128 v[140:143], v133 offset:2048
	ds_read_b128 v[144:147], v133 offset:2560
	v_exp_f32_e32 v74, v74
	v_exp_f32_e32 v75, v75
	v_exp_f32_e32 v76, v76
	v_exp_f32_e32 v77, v77
	s_waitcnt lgkmcnt(2)
	v_mfma_f32_32x32x16_bf16 v[98:113], v[136:139], v[196:199], v[34:49]
	v_exp_f32_e32 v78, v78
	v_exp_f32_e32 v79, v79
	v_exp_f32_e32 v80, v80
	v_exp_f32_e32 v81, v81
	s_nop 0
	v_add_f32_e32 v0, 0, v66
	v_add_f32_e32 v0, v67, v0
	v_add_f32_e32 v0, v68, v0
	v_add_f32_e32 v0, v69, v0
	s_waitcnt lgkmcnt(1)
	v_mfma_f32_32x32x16_bf16 v[82:97], v[140:143], v[192:195], v[82:97]
	ds_read_b128 v[136:139], v133 offset:4096
	ds_read_b128 v[148:151], v133 offset:4608
	v_add_f32_e32 v0, v0, v70
	v_add_f32_e32 v0, v71, v0
	v_add_f32_e32 v0, v72, v0
	v_exp_f32_e32 v50, v50
	v_exp_f32_e32 v51, v51
	v_exp_f32_e32 v52, v52
	v_exp_f32_e32 v53, v53
	v_add_f32_e32 v0, v73, v0
	s_waitcnt lgkmcnt(2)
	v_mfma_f32_32x32x16_bf16 v[98:113], v[144:147], v[192:195], v[98:113]
	v_add_f32_e32 v0, v74, v0
	v_add_f32_e32 v0, v75, v0
	v_add_f32_e32 v0, v76, v0
	v_exp_f32_e32 v54, v54
	v_exp_f32_e32 v55, v55
	v_exp_f32_e32 v56, v56
	v_exp_f32_e32 v57, v57
	v_add_f32_e32 v0, v77, v0
	v_cvt_pk_bf16_f32 v160, v66, v67
	v_cvt_pk_bf16_f32 v161, v68, v69
	s_waitcnt lgkmcnt(1)
	v_mfma_f32_32x32x16_bf16 v[82:97], v[136:139], v[188:191], v[82:97]
	ds_read_b128 v[66:69], v133 offset:6144
	ds_read_b128 v[140:143], v133 offset:6656
	v_add_f32_e32 v0, v78, v0
	v_add_f32_e32 v0, v79, v0
	v_add_f32_e32 v0, v80, v0
	v_exp_f32_e32 v58, v58
	v_exp_f32_e32 v59, v59
	v_exp_f32_e32 v60, v60
	v_exp_f32_e32 v61, v61
	v_add_f32_e32 v0, v81, v0
	v_cvt_pk_bf16_f32 v162, v70, v71
	v_cvt_pk_bf16_f32 v163, v72, v73
	s_waitcnt lgkmcnt(2)
	v_mfma_f32_32x32x16_bf16 v[98:113], v[148:151], v[188:191], v[98:113]
	v_exp_f32_e32 v62, v62
	v_exp_f32_e32 v63, v63
	v_exp_f32_e32 v64, v64
	v_exp_f32_e32 v65, v65
	v_cvt_pk_bf16_f32 v164, v74, v75
	v_add_f32_e32 v0, v0, v50
	v_add_f32_e32 v0, v51, v0
	v_add_f32_e32 v0, v52, v0
	v_add_f32_e32 v0, v53, v0
	v_cvt_pk_bf16_f32 v165, v76, v77
	s_waitcnt lgkmcnt(1)
	v_mfma_f32_32x32x16_bf16 v[82:97], v[66:69], v[184:187], v[82:97]
	ds_read_b128 v[70:73], v133 offset:8192
	ds_read_b128 v[74:77], v133 offset:8704
	v_add_f32_e32 v0, v0, v54
	v_add_f32_e32 v0, v55, v0
	v_add_f32_e32 v0, v56, v0
	v_add_f32_e32 v0, v57, v0
	v_cvt_pk_bf16_f32 v166, v78, v79
	v_cvt_pk_bf16_f32 v167, v80, v81
	s_waitcnt lgkmcnt(2)
	v_mfma_f32_32x32x16_bf16 v[98:113], v[140:143], v[184:187], v[98:113]
	v_add_f32_e32 v0, v58, v0
	v_add_f32_e32 v0, v59, v0
	v_add_f32_e32 v0, v60, v0
	v_add_f32_e32 v0, v61, v0
	v_cvt_pk_bf16_f32 v168, v50, v51
	v_cvt_pk_bf16_f32 v169, v52, v53
	s_waitcnt lgkmcnt(1)
	v_mfma_f32_32x32x16_bf16 v[82:97], v[70:73], v[180:183], v[82:97]
	ds_read_b128 v[50:53], v133 offset:10240
	ds_read_b128 v[66:69], v133 offset:10752
	v_add_f32_e32 v0, v62, v0
	v_add_f32_e32 v0, v63, v0
	v_add_f32_e32 v0, v64, v0
	v_add_f32_e32 v0, v65, v0
	v_cvt_pk_bf16_f32 v170, v54, v55
	v_cvt_pk_bf16_f32 v171, v56, v57
	s_waitcnt lgkmcnt(2)
	v_mfma_f32_32x32x16_bf16 v[98:113], v[74:77], v[180:183], v[98:113]
	v_cvt_pk_bf16_f32 v172, v58, v59
	v_cvt_pk_bf16_f32 v173, v60, v61
	s_waitcnt lgkmcnt(1)
	v_mfma_f32_32x32x16_bf16 v[82:97], v[50:53], v[176:179], v[82:97]
	v_cvt_pk_bf16_f32 v174, v62, v63
	v_cvt_pk_bf16_f32 v175, v64, v65
	s_waitcnt lgkmcnt(0)
	v_mfma_f32_32x32x16_bf16 v[98:113], v[66:69], v[176:179], v[98:113]
	s_setprio 0
	s_add_i32 s44, s81, 6
	s_mov_b32 s45, s11
	s_lshl_b64 s[0:1], s[44:45], 17
	v_lshl_add_u64 v[50:51], v[204:205], 0, s[0:1]
	s_mov_b32 m0, s46
	s_nop 0
	global_load_lds_dwordx4 v[50:51], off
	s_and_saveexec_b64 s[46:47], s[2:3]
	s_cbranch_execz .LBB0_1178
	s_lshl_b64 s[44:45], s[44:45], 12
	s_add_i32 s70, s76, s70
	v_lshl_add_u64 v[50:51], v[202:203], 0, s[44:45]
	s_mov_b32 m0, s70
	s_nop 0
	global_load_lds_dwordx4 v[50:51], off
; __device__ __forceinline__ float max3f(float a, float b, float c) { float r; asm("v_max3_f32 %0, %1, %2, %3" : "=v"(r) : "v"(a), "v"(b), "v"(c)); return r; }
; __device__ __forceinline__ void cmask(f32x16& p0, f32x16& p1, int jb, int qrel, int hi) {
;     const float NEG = -INFINITY; const int kb = 64 * jb + 4 * hi;
; #pragma unroll
;     for (int r = 0; r < 16; ++r) { const int kv = kb + (r & 3) + 8 * (r >> 2); if (kv > qrel) p0[r] = NEG; if (kv + 32 > qrel) p1[r] = NEG; }
; }
; __device__ __forceinline__ float rowmax(const f32x16& p0, const f32x16& p1) {
;     float a = max3f(p0[0], p0[1], p1[0]), b = max3f(p0[2], p0[3], p1[1]); a = max3f(a, p1[2], p1[3]);
; #pragma unroll
;     for (int r = 4; r < 16; r += 4) { a = max3f(a, p0[r], p0[r + 1]); b = max3f(b, p0[r + 2], p0[r + 3]); a = max3f(a, p1[r], p1[r + 1]); b = max3f(b, p1[r + 2], p1[r + 3]); }
;     const float m = fmaxf(a, b);
;     auto rr = __builtin_amdgcn_permlane32_swap(__float_as_uint(m), __float_as_uint(m), false, false);
;     return fmaxf(__uint_as_float(rr[0]), __uint_as_float(rr[1]));
; }
; __device__ __forceinline__ void pv(f32x16* o, int vb, bf16x8 pa0, bf16x8 pa1, bf16x8 pa2, bf16x8 pa3) {
; #pragma unroll
;     for (int d0 = 0; d0 < 2; ++d0) { s16x4 lo[4], hi[4];
; #pragma unroll
;         for (int ks = 0; ks < 4; ++ks) {
;             asm volatile("ds_read_b64_tr_b16 %0,%1 offset:%c2" : "=&v"(lo[ks]) : "v"(vb), "i"(d0 * 4096 + ks * 1024) : "memory");
;             asm volatile("ds_read_b64_tr_b16 %0,%1 offset:%c2" : "=&v"(hi[ks]) : "v"(vb), "i"(d0 * 4096 + ks * 1024 + 512) : "memory"); }
;         asm volatile("s_waitcnt lgkmcnt(0)" ::: "memory"); __builtin_amdgcn_sched_barrier(0);
;     ...
;         o[d0] = __builtin_amdgcn_mfma_f32_32x32x16_bf16(pa0, MLA_PK(0), o[d0], 0, 0, 0);
;         o[d0] = __builtin_amdgcn_mfma_f32_32x32x16_bf16(pa1, MLA_PK(1), o[d0], 0, 0, 0);
;         o[d0] = __builtin_amdgcn_mfma_f32_32x32x16_bf16(pa2, MLA_PK(2), o[d0], 0, 0, 0);
;         o[d0] = __builtin_amdgcn_mfma_f32_32x32x16_bf16(pa3, MLA_PK(3), o[d0], 0, 0, 0);
;     ...
;     }
; }
.LBB0_1178:
	s_or_b64 exec, exec, s[46:47]
	s_lshl_b32 s10, s10, 13
	s_and_b32 s10, s10, 0x6000
	v_lshl_add_u64 v[50:51], v[200:201], 0, s[42:43]
	s_add_i32 s10, s10, s71
	s_mov_b32 m0, s10
	s_nop 0
	global_load_lds_dwordx4 v[50:51], off
	v_add_f32_e32 v133, v134, v0
	v_add_u32_e32 v0, s77, v211
	ds_read_b64_tr_b16 v[50:51],v0 offset:0
	ds_read_b64_tr_b16 v[52:53],v0 offset:512
	ds_read_b64_tr_b16 v[54:55],v0 offset:1024
	ds_read_b64_tr_b16 v[56:57],v0 offset:1536
	ds_read_b64_tr_b16 v[58:59],v0 offset:2048
	ds_read_b64_tr_b16 v[60:61],v0 offset:2560
	ds_read_b64_tr_b16 v[62:63],v0 offset:3072
	ds_read_b64_tr_b16 v[64:65],v0 offset:3584
	s_waitcnt lgkmcnt(0)
	s_nop 0
	v_mfma_f32_32x32x16_bf16 v[2:17], v[160:163], v[50:53], v[2:17]
	ds_read_b64_tr_b16 v[52:53],v0 offset:4096
	v_mfma_f32_32x32x16_bf16 v[2:17], v[164:167], v[54:57], v[2:17]
	ds_read_b64_tr_b16 v[54:55],v0 offset:4608
	ds_read_b64_tr_b16 v[56:57],v0 offset:5120
	v_mfma_f32_32x32x16_bf16 v[2:17], v[168:171], v[58:61], v[2:17]
	ds_read_b64_tr_b16 v[58:59],v0 offset:5632
	ds_read_b64_tr_b16 v[70:71],v0 offset:6144
	ds_read_b64_tr_b16 v[72:73],v0 offset:6656
	ds_read_b64_tr_b16 v[74:75],v0 offset:7168
	ds_read_b64_tr_b16 v[76:77],v0 offset:7680
	s_waitcnt lgkmcnt(0)
	v_mfma_f32_32x32x16_bf16 v[2:17], v[172:175], v[62:65], v[2:17]
	v_mfma_f32_32x32x16_bf16 v[18:33], v[160:163], v[52:55], v[18:33]
	v_or_b32_e32 v50, 0x60, v129
	v_or_b32_e32 v0, 64, v129
	v_cmp_le_i32_e32 vcc, v50, v131
	s_nop 1
	v_cndmask_b32_e32 v50, v206, v98, vcc
	v_cmp_lt_i32_e32 vcc, v0, v131
	v_mfma_f32_32x32x16_bf16 v[18:33], v[164:167], v[56:59], v[18:33]
	s_nop 0
	v_cndmask_b32_e32 v67, v206, v83, vcc
	v_cmp_le_i32_e32 vcc, v0, v131
	v_or_b32_e32 v0, 0x61, v129
	s_nop 0
	v_cndmask_b32_e32 v66, v206, v82, vcc
	v_cmp_le_i32_e32 vcc, v0, v131
	v_or_b32_e32 v0, 0x42, v129
	v_mfma_f32_32x32x16_bf16 v[18:33], v[168:171], v[70:73], v[18:33]
	v_cndmask_b32_e32 v51, v206, v99, vcc
	v_cmp_le_i32_e32 vcc, v0, v131
	v_or_b32_e32 v0, 0x62, v129
	s_nop 0
	v_cndmask_b32_e32 v68, v206, v84, vcc
	v_cmp_le_i32_e32 vcc, v0, v131
	v_or_b32_e32 v0, 0x43, v129
	v_mfma_f32_32x32x16_bf16 v[18:33], v[172:175], v[74:77], v[18:33]
	v_cndmask_b32_e32 v52, v206, v100, vcc
	v_cmp_le_i32_e32 vcc, v0, v131
	v_or_b32_e32 v0, 0x63, v129
	s_nop 0
	v_cndmask_b32_e32 v69, v206, v85, vcc
	v_cmp_le_i32_e32 vcc, v0, v131
	v_or_b32_e32 v0, 0x48, v129
	v_max3_f32 v82, v68, v69, v51
	s_nop 0
	v_cndmask_b32_e32 v53, v206, v101, vcc
	v_cmp_le_i32_e32 vcc, v0, v131
	v_or_b32_e32 v0, 0x68, v129
	s_nop 0
	v_cndmask_b32_e32 v70, v206, v86, vcc
	v_cmp_le_i32_e32 vcc, v0, v131
	v_or_b32_e32 v0, 0x49, v129
	s_nop 0
	v_cndmask_b32_e32 v54, v206, v102, vcc
	v_cmp_le_i32_e32 vcc, v0, v131
	v_or_b32_e32 v0, 0x69, v129
	s_nop 0
	v_cndmask_b32_e32 v71, v206, v87, vcc
	v_cmp_le_i32_e32 vcc, v0, v131
	v_or_b32_e32 v0, 0x4a, v129
	s_nop 0
	v_cndmask_b32_e32 v55, v206, v103, vcc
	v_cmp_le_i32_e32 vcc, v0, v131
	v_or_b32_e32 v0, 0x6a, v129
	s_nop 0
	v_cndmask_b32_e32 v72, v206, v88, vcc
	v_cmp_le_i32_e32 vcc, v0, v131
	v_or_b32_e32 v0, 0x4b, v129
	s_nop 0
	v_cndmask_b32_e32 v56, v206, v104, vcc
	v_cmp_le_i32_e32 vcc, v0, v131
	v_or_b32_e32 v0, 0x6b, v129
	s_nop 0
	v_cndmask_b32_e32 v73, v206, v89, vcc
	v_cmp_le_i32_e32 vcc, v0, v131
	v_or_b32_e32 v0, 0x50, v129
	v_max3_f32 v82, v82, v72, v73
	s_nop 0
	v_cndmask_b32_e32 v57, v206, v105, vcc
	v_cmp_le_i32_e32 vcc, v0, v131
	v_or_b32_e32 v0, 0x70, v129
	v_max3_f32 v82, v82, v56, v57
	s_nop 0
	v_cndmask_b32_e32 v74, v206, v90, vcc
	v_cmp_le_i32_e32 vcc, v0, v131
	v_or_b32_e32 v0, 0x51, v129
	s_nop 0
	v_cndmask_b32_e32 v58, v206, v106, vcc
	v_cmp_le_i32_e32 vcc, v0, v131
	v_or_b32_e32 v0, 0x71, v129
	s_nop 0
	v_cndmask_b32_e32 v75, v206, v91, vcc
	v_cmp_le_i32_e32 vcc, v0, v131
	v_or_b32_e32 v0, 0x52, v129
	s_nop 0
	v_cndmask_b32_e32 v59, v206, v107, vcc
	v_cmp_le_i32_e32 vcc, v0, v131
	v_or_b32_e32 v0, 0x72, v129
	s_nop 0
	v_cndmask_b32_e32 v76, v206, v92, vcc
	v_cmp_le_i32_e32 vcc, v0, v131
	v_or_b32_e32 v0, 0x53, v129
	s_nop 0
	v_cndmask_b32_e32 v60, v206, v108, vcc
	v_cmp_le_i32_e32 vcc, v0, v131
	v_or_b32_e32 v0, 0x73, v129
	s_nop 0
	v_cndmask_b32_e32 v77, v206, v93, vcc
	v_cmp_le_i32_e32 vcc, v0, v131
	v_or_b32_e32 v0, 0x58, v129
	v_max3_f32 v82, v82, v76, v77
	s_nop 0
	v_cndmask_b32_e32 v61, v206, v109, vcc
	v_cmp_le_i32_e32 vcc, v0, v131
	v_or_b32_e32 v0, 0x78, v129
	v_max3_f32 v82, v82, v60, v61
	s_nop 0
	v_cndmask_b32_e32 v78, v206, v94, vcc
	v_cmp_le_i32_e32 vcc, v0, v131
	v_or_b32_e32 v0, 0x59, v129
	s_nop 0
	v_cndmask_b32_e32 v62, v206, v110, vcc
	v_cmp_le_i32_e32 vcc, v0, v131
	v_or_b32_e32 v0, 0x79, v129
	s_nop 0
	v_cndmask_b32_e32 v79, v206, v95, vcc
	v_cmp_le_i32_e32 vcc, v0, v131
	v_or_b32_e32 v0, 0x5a, v129
	s_nop 0
	v_cndmask_b32_e32 v63, v206, v111, vcc
	v_cmp_le_i32_e32 vcc, v0, v131
	v_or_b32_e32 v0, 0x7a, v129
	s_nop 0
	v_cndmask_b32_e32 v80, v206, v96, vcc
	v_cmp_le_i32_e32 vcc, v0, v131
	v_or_b32_e32 v0, 0x5b, v129
	s_nop 0
	v_cndmask_b32_e32 v64, v206, v112, vcc
	v_cmp_le_i32_e32 vcc, v0, v131
	v_or_b32_e32 v0, 0x7b, v129
	s_nop 0
	v_cndmask_b32_e32 v81, v206, v97, vcc
	v_cmp_le_i32_e32 vcc, v0, v131
	v_max3_f32 v0, v66, v67, v50
	v_max3_f32 v82, v82, v80, v81
	s_nop 0
	v_max3_f32 v0, v0, v52, v53
	s_nop 0
	v_max3_f32 v0, v0, v70, v71
	v_cndmask_b32_e32 v65, v206, v113, vcc
	v_max3_f32 v0, v0, v54, v55
	v_max3_f32 v82, v82, v64, v65
	s_nop 0
	v_max3_f32 v0, v0, v74, v75
	v_max_f32_e32 v82, v82, v82
	v_max3_f32 v0, v0, v58, v59
	s_nop 0
	v_max3_f32 v0, v0, v78, v79
	s_nop 0
	v_max3_f32 v0, v0, v62, v63
	s_nop 0
	v_max_f32_e32 v0, v0, v0
	v_max_f32_e32 v0, v0, v82
	v_mov_b32_e32 v82, v0
	s_nop 1
	v_permlane32_swap_b32_e32 v0, v82
	v_max_f32_e32 v82, v82, v82
	v_max_f32_e32 v0, v0, v0
	v_max_f32_e32 v0, v0, v82
	v_cmp_lt_f32_e32 vcc, s54, v0
	s_cbranch_vccnz .LBB0_1226
; __device__ __forceinline__ void pv(f32x16* o, int vb, bf16x8 pa0, bf16x8 pa1, bf16x8 pa2, bf16x8 pa3) {
; #pragma unroll
;     for (int d0 = 0; d0 < 2; ++d0) { s16x4 lo[4], hi[4];
; #pragma unroll
;         for (int ks = 0; ks < 4; ++ks) {
;             asm volatile("ds_read_b64_tr_b16 %0,%1 offset:%c2" : "=&v"(lo[ks]) : "v"(vb), "i"(d0 * 4096 + ks * 1024) : "memory");
;             asm volatile("ds_read_b64_tr_b16 %0,%1 offset:%c2" : "=&v"(hi[ks]) : "v"(vb), "i"(d0 * 4096 + ks * 1024 + 512) : "memory"); }
;         asm volatile("s_waitcnt lgkmcnt(0)" ::: "memory"); __builtin_amdgcn_sched_barrier(0);
;     ...
;         o[d0] = __builtin_amdgcn_mfma_f32_32x32x16_bf16(pa0, MLA_PK(0), o[d0], 0, 0, 0);
;         o[d0] = __builtin_amdgcn_mfma_f32_32x32x16_bf16(pa1, MLA_PK(1), o[d0], 0, 0, 0);
;         o[d0] = __builtin_amdgcn_mfma_f32_32x32x16_bf16(pa2, MLA_PK(2), o[d0], 0, 0, 0);
;         o[d0] = __builtin_amdgcn_mfma_f32_32x32x16_bf16(pa3, MLA_PK(3), o[d0], 0, 0, 0);
;     ...
;     }
.LBB0_1179:
	s_waitcnt vmcnt(3) lgkmcnt(0)
	s_barrier
	s_setprio 1
	ds_read_b128 v[98:101], v132
	ds_read_b128 v[134:137], v132 offset:512
	v_exp_f32_e32 v66, v66
	v_exp_f32_e32 v67, v67
	v_exp_f32_e32 v68, v68
	v_exp_f32_e32 v69, v69
	s_nop 0
	v_exp_f32_e32 v70, v70
	v_exp_f32_e32 v71, v71
	v_exp_f32_e32 v72, v72
	v_exp_f32_e32 v73, v73
	ds_read_b128 v[138:141], v132 offset:2048
	ds_read_b128 v[142:145], v132 offset:2560
	v_exp_f32_e32 v74, v74
	v_exp_f32_e32 v75, v75
	v_exp_f32_e32 v76, v76
	v_exp_f32_e32 v77, v77
	s_waitcnt lgkmcnt(3)
	v_mfma_f32_32x32x16_bf16 v[82:97], v[98:101], v[196:199], v[34:49]
	s_nop 0
	v_exp_f32_e32 v78, v78
	v_exp_f32_e32 v79, v79
	v_exp_f32_e32 v80, v80
	v_exp_f32_e32 v81, v81
	s_waitcnt lgkmcnt(2)
	v_mfma_f32_32x32x16_bf16 v[98:113], v[134:137], v[196:199], v[34:49]
	v_add_f32_e32 v0, 0, v66
	v_add_f32_e32 v0, v67, v0
	v_add_f32_e32 v0, v68, v0
	v_add_f32_e32 v0, v69, v0
	ds_read_b128 v[134:137], v132 offset:4096
	ds_read_b128 v[146:149], v132 offset:4608
	v_add_f32_e32 v0, v0, v70
	v_add_f32_e32 v0, v71, v0
	v_add_f32_e32 v0, v72, v0
	v_exp_f32_e32 v50, v50
	v_exp_f32_e32 v51, v51
	v_exp_f32_e32 v52, v52
	v_exp_f32_e32 v53, v53
	v_add_f32_e32 v0, v73, v0
	s_waitcnt lgkmcnt(3)
	v_mfma_f32_32x32x16_bf16 v[82:97], v[138:141], v[192:195], v[82:97]
	s_nop 0
	v_add_f32_e32 v0, v74, v0
	v_add_f32_e32 v0, v75, v0
	v_add_f32_e32 v0, v76, v0
	v_exp_f32_e32 v54, v54
	v_exp_f32_e32 v55, v55
	v_exp_f32_e32 v56, v56
	v_exp_f32_e32 v57, v57
	v_add_f32_e32 v0, v77, v0
	v_cvt_pk_bf16_f32 v160, v66, v67
	v_cvt_pk_bf16_f32 v161, v68, v69
	s_waitcnt lgkmcnt(2)
	v_mfma_f32_32x32x16_bf16 v[98:113], v[142:145], v[192:195], v[98:113]
	ds_read_b128 v[66:69], v132 offset:6144
	ds_read_b128 v[138:141], v132 offset:6656
	v_add_f32_e32 v0, v78, v0
	v_add_f32_e32 v0, v79, v0
	v_add_f32_e32 v0, v80, v0
	v_exp_f32_e32 v58, v58
	v_exp_f32_e32 v59, v59
	v_exp_f32_e32 v60, v60
	v_exp_f32_e32 v61, v61
	v_add_f32_e32 v0, v81, v0
	v_cvt_pk_bf16_f32 v162, v70, v71
	v_cvt_pk_bf16_f32 v163, v72, v73
	s_waitcnt lgkmcnt(3)
	v_mfma_f32_32x32x16_bf16 v[82:97], v[134:137], v[188:191], v[82:97]
	s_nop 0
	v_exp_f32_e32 v62, v62
	v_exp_f32_e32 v63, v63
	v_exp_f32_e32 v64, v64
	v_exp_f32_e32 v65, v65
	v_cvt_pk_bf16_f32 v164, v74, v75
	v_add_f32_e32 v0, v0, v50
	v_add_f32_e32 v0, v51, v0
	v_add_f32_e32 v0, v52, v0
	v_add_f32_e32 v0, v53, v0
	v_cvt_pk_bf16_f32 v165, v76, v77
	s_waitcnt lgkmcnt(2)
	v_mfma_f32_32x32x16_bf16 v[98:113], v[146:149], v[188:191], v[98:113]
	ds_read_b128 v[70:73], v132 offset:8192
	ds_read_b128 v[74:77], v132 offset:8704
	v_add_f32_e32 v0, v0, v54
	v_add_f32_e32 v0, v55, v0
	v_add_f32_e32 v0, v56, v0
	v_add_f32_e32 v0, v57, v0
	v_cvt_pk_bf16_f32 v166, v78, v79
	v_cvt_pk_bf16_f32 v167, v80, v81
	s_waitcnt lgkmcnt(3)
	v_mfma_f32_32x32x16_bf16 v[82:97], v[66:69], v[184:187], v[82:97]
	s_nop 0
	v_add_f32_e32 v0, v58, v0
	v_add_f32_e32 v0, v59, v0
	v_add_f32_e32 v0, v60, v0
	v_add_f32_e32 v0, v61, v0
	v_cvt_pk_bf16_f32 v168, v50, v51
	v_cvt_pk_bf16_f32 v169, v52, v53
	s_waitcnt lgkmcnt(2)
	v_mfma_f32_32x32x16_bf16 v[98:113], v[138:141], v[184:187], v[98:113]
	ds_read_b128 v[50:53], v132 offset:10240
	ds_read_b128 v[66:69], v132 offset:10752
	v_add_f32_e32 v0, v62, v0
	v_add_f32_e32 v0, v63, v0
	v_add_f32_e32 v0, v64, v0
	v_add_f32_e32 v0, v65, v0
	v_cvt_pk_bf16_f32 v170, v54, v55
	v_cvt_pk_bf16_f32 v171, v56, v57
	s_waitcnt lgkmcnt(3)
	v_mfma_f32_32x32x16_bf16 v[82:97], v[70:73], v[180:183], v[82:97]
	v_cvt_pk_bf16_f32 v172, v58, v59
	v_cvt_pk_bf16_f32 v173, v60, v61
	s_waitcnt lgkmcnt(2)
	v_mfma_f32_32x32x16_bf16 v[98:113], v[74:77], v[180:183], v[98:113]
	v_cvt_pk_bf16_f32 v174, v62, v63
	v_cvt_pk_bf16_f32 v175, v64, v65
	s_waitcnt lgkmcnt(1)
	v_mfma_f32_32x32x16_bf16 v[82:97], v[50:53], v[176:179], v[82:97]
	s_waitcnt lgkmcnt(0)
	v_mfma_f32_32x32x16_bf16 v[98:113], v[66:69], v[176:179], v[98:113]
	v_add_f32_e32 v132, v133, v0
	s_setprio 0
	v_lshl_add_u64 v[50:51], v[200:201], 0, s[0:1]
	s_mov_b32 m0, s74
	s_nop 0
	global_load_lds_dwordx4 v[50:51], off
	s_xor_b32 s0, s73, 0x4000
	v_add_u32_e32 v0, s0, v211
	ds_read_b64_tr_b16 v[50:51],v0 offset:0
	ds_read_b64_tr_b16 v[52:53],v0 offset:512
	ds_read_b64_tr_b16 v[54:55],v0 offset:1024
	ds_read_b64_tr_b16 v[56:57],v0 offset:1536
	ds_read_b64_tr_b16 v[58:59],v0 offset:2048
	ds_read_b64_tr_b16 v[60:61],v0 offset:2560
	ds_read_b64_tr_b16 v[62:63],v0 offset:3072
	ds_read_b64_tr_b16 v[64:65],v0 offset:3584
	s_waitcnt lgkmcnt(0)
	s_nop 0
	v_mfma_f32_32x32x16_bf16 v[2:17], v[160:163], v[50:53], v[2:17]
	ds_read_b64_tr_b16 v[52:53],v0 offset:4096
	v_mfma_f32_32x32x16_bf16 v[2:17], v[164:167], v[54:57], v[2:17]
	ds_read_b64_tr_b16 v[54:55],v0 offset:4608
	ds_read_b64_tr_b16 v[56:57],v0 offset:5120
	v_mfma_f32_32x32x16_bf16 v[2:17], v[168:171], v[58:61], v[2:17]
	ds_read_b64_tr_b16 v[58:59],v0 offset:5632
	ds_read_b64_tr_b16 v[70:71],v0 offset:6144
	ds_read_b64_tr_b16 v[72:73],v0 offset:6656
	ds_read_b64_tr_b16 v[74:75],v0 offset:7168
	ds_read_b64_tr_b16 v[76:77],v0 offset:7680
	s_waitcnt lgkmcnt(0)
; __device__ __forceinline__ float max3f(float a, float b, float c) { float r; asm("v_max3_f32 %0, %1, %2, %3" : "=v"(r) : "v"(a), "v"(b), "v"(c)); return r; }
; __device__ __forceinline__ void cmask(f32x16& p0, f32x16& p1, int jb, int qrel, int hi) {
;     const float NEG = -INFINITY; const int kb = 64 * jb + 4 * hi;
; #pragma unroll
;     for (int r = 0; r < 16; ++r) { const int kv = kb + (r & 3) + 8 * (r >> 2); if (kv > qrel) p0[r] = NEG; if (kv + 32 > qrel) p1[r] = NEG; }
; }
; __device__ __forceinline__ float rowmax(const f32x16& p0, const f32x16& p1) {
;     float a = max3f(p0[0], p0[1], p1[0]), b = max3f(p0[2], p0[3], p1[1]); a = max3f(a, p1[2], p1[3]);
; #pragma unroll
;     for (int r = 4; r < 16; r += 4) { a = max3f(a, p0[r], p0[r + 1]); b = max3f(b, p0[r + 2], p0[r + 3]); a = max3f(a, p1[r], p1[r + 1]); b = max3f(b, p1[r + 2], p1[r + 3]); }
;     const float m = fmaxf(a, b);
;     auto rr = __builtin_amdgcn_permlane32_swap(__float_as_uint(m), __float_as_uint(m), false, false);
;     return fmaxf(__uint_as_float(rr[0]), __uint_as_float(rr[1]));
; }
	v_mfma_f32_32x32x16_bf16 v[2:17], v[172:175], v[62:65], v[2:17]
	v_mfma_f32_32x32x16_bf16 v[18:33], v[160:163], v[52:55], v[18:33]
	v_or_b32_e32 v50, 0xa0, v129
	v_or_b32_e32 v0, 0x80, v129
	v_cmp_le_i32_e32 vcc, v50, v131
	s_nop 1
	v_cndmask_b32_e32 v50, v206, v98, vcc
	v_cmp_lt_i32_e32 vcc, v0, v131
	v_mfma_f32_32x32x16_bf16 v[18:33], v[164:167], v[56:59], v[18:33]
	s_nop 0
	v_cndmask_b32_e32 v67, v206, v83, vcc
	v_cmp_le_i32_e32 vcc, v0, v131
	v_or_b32_e32 v0, 0xa1, v129
	s_nop 0
	v_cndmask_b32_e32 v66, v206, v82, vcc
	v_cmp_le_i32_e32 vcc, v0, v131
	v_or_b32_e32 v0, 0x82, v129
	v_mfma_f32_32x32x16_bf16 v[18:33], v[168:171], v[70:73], v[18:33]
	v_cndmask_b32_e32 v51, v206, v99, vcc
	v_cmp_le_i32_e32 vcc, v0, v131
	v_or_b32_e32 v0, 0xa2, v129
	s_nop 0
	v_cndmask_b32_e32 v68, v206, v84, vcc
	v_cmp_le_i32_e32 vcc, v0, v131
	v_or_b32_e32 v0, 0x83, v129
	v_mfma_f32_32x32x16_bf16 v[18:33], v[172:175], v[74:77], v[18:33]
	v_cndmask_b32_e32 v52, v206, v100, vcc
	v_cmp_le_i32_e32 vcc, v0, v131
	v_or_b32_e32 v0, 0xa3, v129
	s_nop 0
	v_cndmask_b32_e32 v69, v206, v85, vcc
	v_cmp_le_i32_e32 vcc, v0, v131
	v_or_b32_e32 v0, 0x88, v129
	v_max3_f32 v82, v68, v69, v51
	s_nop 0
	v_cndmask_b32_e32 v53, v206, v101, vcc
	v_cmp_le_i32_e32 vcc, v0, v131
	v_or_b32_e32 v0, 0xa8, v129
	s_nop 0
	v_cndmask_b32_e32 v70, v206, v86, vcc
	v_cmp_le_i32_e32 vcc, v0, v131
	v_or_b32_e32 v0, 0x89, v129
	s_nop 0
	v_cndmask_b32_e32 v54, v206, v102, vcc
	v_cmp_le_i32_e32 vcc, v0, v131
	v_or_b32_e32 v0, 0xa9, v129
	s_nop 0
	v_cndmask_b32_e32 v71, v206, v87, vcc
	v_cmp_le_i32_e32 vcc, v0, v131
	v_or_b32_e32 v0, 0x8a, v129
	s_nop 0
	v_cndmask_b32_e32 v55, v206, v103, vcc
	v_cmp_le_i32_e32 vcc, v0, v131
	v_or_b32_e32 v0, 0xaa, v129
	s_nop 0
	v_cndmask_b32_e32 v72, v206, v88, vcc
	v_cmp_le_i32_e32 vcc, v0, v131
	v_or_b32_e32 v0, 0x8b, v129
	s_nop 0
	v_cndmask_b32_e32 v56, v206, v104, vcc
	v_cmp_le_i32_e32 vcc, v0, v131
	v_or_b32_e32 v0, 0xab, v129
	s_nop 0
	v_cndmask_b32_e32 v73, v206, v89, vcc
	v_cmp_le_i32_e32 vcc, v0, v131
	v_or_b32_e32 v0, 0x90, v129
	v_max3_f32 v82, v82, v72, v73
	s_nop 0
	v_cndmask_b32_e32 v57, v206, v105, vcc
	v_cmp_le_i32_e32 vcc, v0, v131
	v_or_b32_e32 v0, 0xb0, v129
	v_max3_f32 v82, v82, v56, v57
	s_nop 0
	v_cndmask_b32_e32 v74, v206, v90, vcc
	v_cmp_le_i32_e32 vcc, v0, v131
	v_or_b32_e32 v0, 0x91, v129
	s_nop 0
	v_cndmask_b32_e32 v58, v206, v106, vcc
	v_cmp_le_i32_e32 vcc, v0, v131
	v_or_b32_e32 v0, 0xb1, v129
	s_nop 0
	v_cndmask_b32_e32 v75, v206, v91, vcc
	v_cmp_le_i32_e32 vcc, v0, v131
	v_or_b32_e32 v0, 0x92, v129
	s_nop 0
	v_cndmask_b32_e32 v59, v206, v107, vcc
	v_cmp_le_i32_e32 vcc, v0, v131
	v_or_b32_e32 v0, 0xb2, v129
	s_nop 0
	v_cndmask_b32_e32 v76, v206, v92, vcc
	v_cmp_le_i32_e32 vcc, v0, v131
	v_or_b32_e32 v0, 0x93, v129
	s_nop 0
	v_cndmask_b32_e32 v60, v206, v108, vcc
	v_cmp_le_i32_e32 vcc, v0, v131
	v_or_b32_e32 v0, 0xb3, v129
	s_nop 0
	v_cndmask_b32_e32 v77, v206, v93, vcc
	v_cmp_le_i32_e32 vcc, v0, v131
	v_or_b32_e32 v0, 0x98, v129
	v_max3_f32 v82, v82, v76, v77
	s_nop 0
	v_cndmask_b32_e32 v61, v206, v109, vcc
	v_cmp_le_i32_e32 vcc, v0, v131
	v_or_b32_e32 v0, 0xb8, v129
	v_max3_f32 v82, v82, v60, v61
	s_nop 0
	v_cndmask_b32_e32 v78, v206, v94, vcc
	v_cmp_le_i32_e32 vcc, v0, v131
	v_or_b32_e32 v0, 0x99, v129
	s_nop 0
	v_cndmask_b32_e32 v62, v206, v110, vcc
	v_cmp_le_i32_e32 vcc, v0, v131
	v_or_b32_e32 v0, 0xb9, v129
	s_nop 0
	v_cndmask_b32_e32 v79, v206, v95, vcc
	v_cmp_le_i32_e32 vcc, v0, v131
	v_or_b32_e32 v0, 0x9a, v129
	s_nop 0
	v_cndmask_b32_e32 v63, v206, v111, vcc
	v_cmp_le_i32_e32 vcc, v0, v131
	v_or_b32_e32 v0, 0xba, v129
	s_nop 0
	v_cndmask_b32_e32 v80, v206, v96, vcc
	v_cmp_le_i32_e32 vcc, v0, v131
	v_or_b32_e32 v0, 0x9b, v129
	s_nop 0
	v_cndmask_b32_e32 v64, v206, v112, vcc
	v_cmp_le_i32_e32 vcc, v0, v131
	v_or_b32_e32 v0, 0xbb, v129
	s_nop 0
	v_cndmask_b32_e32 v81, v206, v97, vcc
	v_cmp_le_i32_e32 vcc, v0, v131
	v_max3_f32 v0, v66, v67, v50
	v_max3_f32 v82, v82, v80, v81
	s_nop 0
	v_max3_f32 v0, v0, v52, v53
	s_nop 0
	v_max3_f32 v0, v0, v70, v71
	v_cndmask_b32_e32 v65, v206, v113, vcc
	v_max3_f32 v0, v0, v54, v55
	v_max3_f32 v82, v82, v64, v65
	s_nop 0
	v_max3_f32 v0, v0, v74, v75
	v_max_f32_e32 v82, v82, v82
	v_max3_f32 v0, v0, v58, v59
	s_nop 0
	v_max3_f32 v0, v0, v78, v79
	s_nop 0
	v_max3_f32 v0, v0, v62, v63
	s_nop 0
	v_max_f32_e32 v0, v0, v0
	v_max_f32_e32 v0, v0, v82
	v_mov_b32_e32 v82, v0
	s_nop 1
	v_permlane32_swap_b32_e32 v0, v82
	v_max_f32_e32 v82, v82, v82
	v_max_f32_e32 v0, v0, v0
	v_max_f32_e32 v0, v0, v82
	v_cmp_lt_f32_e32 vcc, s54, v0
	s_cbranch_vccnz .LBB0_1229

; __device__ __forceinline__ int tid_from_wave(int wave) { unsigned l_; asm volatile("v_mbcnt_lo_u32_b32 %0, -1, 0\n\tv_mbcnt_hi_u32_b32 %0, -1, %0" : "=v"(l_)); return wave * 64 + (int)l_; }
; __device__ __forceinline__ void unit(int b, int h, int qb, const unsigned short* Q, const unsigned short* KV, const unsigned short* KPE, unsigned short* O, char* shm, const int wave_) {
;     int tid_ = tid_from_wave(wave_); asm volatile("" : "+v"(tid_));
;     const int tid = tid_, lane = tid & 63, r32 = lane & 31, hi = lane >> 5; const int wid = __builtin_amdgcn_readfirstlane(tid >> 6);
;     const long rowbase = (long)b * SEQ; const int q0 = qb * QB;
;     const unsigned short* Qw = Q + (rowbase + q0 + wid * QBLK) * QP + h * 96;
;     const unsigned short* Kh = KV + rowbase * KVP + h * 128; const unsigned short* Vh = Kh + 64; const unsigned short* Ph = KPE + rowbase * PEP;
;     const unsigned lds0 = (unsigned)(uintptr_t)shm;
;     __attribute__((address_space(3))) float* wsf = (__attribute__((address_space(3))) float*)((lds_cptr)shm + LDS_WS) + wid * 64;
;     const unsigned short* ksrc = Kh + (long)lane * KVP + wid * 8;
;     const unsigned short* psrc = Ph + (long)(32 * (wid & 1) + r32) * PEP + (wid >> 1) * 8;
;     const unsigned short* vsrc = Vh + (long)(16 * (wid & 3) + (lane >> 2)) * KVP + (wid >> 2) * 32 + (lane & 3) * 8;
;     const unsigned kdst = lds0 + LDS_K + wid * 1024, pdst = lds0 + LDS_K + (8 + (wid >> 1)) * 1024 + (wid & 1) * 512, vdst = lds0 + LDS_V + wid * 1024;
;     ...
;     const int vb0 = (int)(lds0 + LDS_V) + ((lane >> 4) & 1) * 32 + (lane & 3) * 8 + (4 * hi + ((lane & 15) >> 2)) * 64;
;     const lds_cptr kp0 = (lds_cptr)shm + LDS_K + hi * 1024 + r32 * 16;
;     const int NT = (q0 + QB) / KVBLK;
;     bf16x8 qr[6];
; #pragma unroll
;     for (int d0 = 0; d0 < 6; ++d0) qr[d0] = *reinterpret_cast<const bf16x8*>(&Qw[(long)r32 * QP + d0 * 16 + hi * 8]);
;     asm volatile("s_waitcnt vmcnt(0)" ::: "memory");
;     MLA_DMA(0, 0); MLA_DMA(1, 1);
;     float m = -INFINITY, l = 0.f; f32x16 o[2]; o[0] = f32x16{}; o[1] = f32x16{};
;     const int qrel = wid * QBLK + r32;
;     int slot = 0, slot2 = 2;
.LBB0_1184:
	v_mbcnt_lo_u32_b32 v0, -1, 0
	v_mbcnt_hi_u32_b32 v0, -1, v0
	s_nop 0
	v_add_u32_e32 v8, s96, v0
	s_nop 0
	v_readfirstlane_b32 s45, v8
	s_ashr_i32 s10, s45, 6
	s_lshl_b32 s47, s10, 5
	s_ashr_i32 s1, s47, 31
	s_add_u32 s0, s34, s47
	s_addc_u32 s1, s35, s1
	v_and_b32_e32 v98, 31, v8
	s_mul_i32 s2, s1, 0x600
	s_mul_hi_u32 s3, s0, 0x600
	s_add_i32 s3, s3, s2
	s_mul_i32 s2, s0, 0x600
	v_mul_u32_u24_e32 v0, 0x300, v98
	v_bfe_u32 v99, v8, 5, 1
	s_add_u32 s2, s63, s2
	v_lshlrev_b32_e32 v0, 1, v0
	s_addc_u32 s3, s64, s3
	v_lshl_or_b32 v0, v99, 4, v0
	global_load_dwordx4 v[66:69], v0, s[2:3]
	global_load_dwordx4 v[70:73], v0, s[2:3] offset:32
	global_load_dwordx4 v[74:77], v0, s[2:3] offset:64
	global_load_dwordx4 v[78:81], v0, s[2:3] offset:96
	global_load_dwordx4 v[82:85], v0, s[2:3] offset:128
	global_load_dwordx4 v[86:89], v0, s[2:3] offset:160
	s_ashr_i32 s42, s45, 7
	s_lshl_b32 s2, s10, 3
	s_lshl_b32 s40, s42, 3
	v_and_b32_e32 v96, 63, v8
	s_ashr_i32 s3, s2, 31
	s_and_b32 s43, s10, 1
	s_ashr_i32 s41, s40, 31
	s_lshl_b32 s68, s10, 10
	s_lshl_b32 s42, s42, 10
	s_cmp_lg_u32 0, -1
	v_lshlrev_b32_e32 v0, 11, v96
	s_cselect_b32 s44, 0, 0
	v_lshl_add_u64 v[2:3], s[36:37], 0, v[0:1]
	v_lshlrev_b32_e32 v0, 6, v98
	s_waitcnt vmcnt(0)
	s_add_i32 s42, s44, s42
	s_lshl_b32 s46, s43, 9
	v_lshl_add_u64 v[2:3], s[2:3], 1, v[2:3]
	v_lshl_or_b32 v0, s43, 11, v0
	s_add_i32 s43, s68, s44
	s_mov_b32 m0, s43
	s_nop 0
	global_load_lds_dwordx4 v[2:3], off
	s_add_i32 s42, s42, s46
	v_lshl_add_u64 v[4:5], s[38:39], 0, v[0:1]
	s_addk_i32 s42, 0x2000
	v_lshl_add_u64 v[4:5], s[40:41], 1, v[4:5]
	v_cmp_gt_u32_e64 s[2:3], 32, v96
	s_and_saveexec_b64 s[40:41], s[2:3]
	s_cbranch_execz .LBB0_1186
	s_mov_b32 m0, s42
	s_nop 0
	global_load_lds_dwordx4 v[4:5], off
.LBB0_1186:
	s_or_b64 exec, exec, s[40:41]
	s_lshl_b32 s40, s10, 4
	v_lshrrev_b32_e32 v0, 2, v96
	v_and_or_b32 v0, s40, 48, v0
	s_ashr_i32 s40, s45, 3
	s_andn2_b32 s40, s40, 31
	s_ashr_i32 s41, s40, 31
	v_lshlrev_b32_e32 v97, 3, v8
	v_lshlrev_b32_e32 v0, 11, v0
	v_and_b32_e32 v9, 24, v97
	v_lshl_add_u64 v[6:7], s[36:37], 0, v[0:1]
	s_cmp_lg_u32 0, -1
	v_lshl_add_u64 v[6:7], s[40:41], 1, v[6:7]
	v_lshlrev_b32_e32 v0, 1, v9
	s_cselect_b32 s40, 0, 0
	v_lshl_add_u64 v[6:7], v[6:7], 0, v[0:1]
	s_add_i32 s40, s40, s68
	v_lshl_add_u64 v[6:7], v[6:7], 0, s[16:17]
	s_add_i32 s44, s40, 0x9000
	s_mov_b32 m0, s44
	s_nop 0
	global_load_lds_dwordx4 v[6:7], off
	v_lshl_add_u64 v[10:11], v[2:3], 0, s[12:13]
	s_addk_i32 s40, 0x3000
	s_mov_b32 m0, s40
	s_nop 0
	global_load_lds_dwordx4 v[10:11], off
	s_and_saveexec_b64 s[40:41], s[2:3]
	s_cbranch_execz .LBB0_1188
	v_lshl_add_u64 v[10:11], v[4:5], 0, s[14:15]
	s_add_i32 s46, s42, 0x3000
	s_mov_b32 m0, s46
	s_nop 0
	global_load_lds_dwordx4 v[10:11], off
.LBB0_1188:
	s_or_b64 exec, exec, s[40:41]
	s_and_b32 s40, s45, 0x3fffffc0
	s_lshl_b32 s40, s40, 2
	s_add_i32 s40, s40, 0
	v_lshlrev_b32_e32 v0, 1, v8
	v_lshlrev_b32_e32 v8, 4, v8
	s_cmp_lg_u32 0, -1
	v_lshlrev_b32_e32 v10, 10, v99
	v_lshlrev_b32_e32 v11, 4, v98
	v_lshlrev_b32_e32 v12, 8, v99
	v_and_b32_e32 v8, 0xc0, v8
	s_cselect_b32 s41, 0, 0
	v_and_b32_e32 v0, 32, v0
	v_add3_u32 v102, 0, v10, v11
	v_lshl_add_u64 v[10:11], v[6:7], 0, s[12:13]
	s_add_i32 s68, s41, s68
	v_or3_b32 v8, v8, v12, v9
	s_add_i32 s41, s41, 0x9000
	v_mov_b32_e32 v14, v1
	v_mov_b32_e32 v15, v1
	s_add_i32 s68, s68, 0xb000
	s_mov_b32 m0, s68
	s_nop 0
	global_load_lds_dwordx4 v[10:11], off
	v_add3_u32 v105, v0, s41, v8
	v_lshl_add_u64 v[90:91], v[4:5], 0, s[20:21]
	v_lshl_add_u64 v[92:93], v[6:7], 0, s[18:19]
	v_lshl_add_u64 v[94:95], v[2:3], 0, s[18:19]
	v_mov_b32_e32 v0, v1
	v_mov_b32_e32 v2, v1
	v_mov_b32_e32 v3, v1
	v_mov_b32_e32 v4, v1
	v_mov_b32_e32 v5, v1
	v_mov_b32_e32 v6, v1
	v_mov_b32_e32 v7, v1
	v_mov_b32_e32 v8, v1
	v_mov_b32_e32 v9, v1
	v_mov_b32_e32 v10, v1
	v_mov_b32_e32 v11, v1
	v_mov_b32_e32 v12, v1
	v_mov_b32_e32 v13, v1
	v_mov_b64_e32 v[32:33], v[14:15]
	v_mov_b64_e32 v[30:31], v[12:13]
	v_mov_b64_e32 v[28:29], v[10:11]
	v_mov_b64_e32 v[26:27], v[8:9]
	v_mov_b64_e32 v[24:25], v[6:7]
	v_mov_b64_e32 v[22:23], v[4:5]
	v_mov_b64_e32 v[20:21], v[2:3]
	v_mov_b64_e32 v[18:19], v[0:1]
	v_mov_b64_e32 v[16:17], v[14:15]
	s_mov_b32 s45, 2
	s_mov_b32 s46, 0
	v_or_b32_e32 v103, s47, v98
	v_lshlrev_b32_e32 v104, 2, v99
	v_lshl_add_u32 v101, v98, 2, s40
	v_lshl_add_u32 v100, v99, 4, s40
	v_mov_b32_e32 v106, 0
	v_mov_b32_e32 v119, 0xff800000
	s_mov_b32 s47, 0
	s_mov_b32 s68, 0
	v_mov_b64_e32 v[14:15], v[12:13]
	v_mov_b64_e32 v[12:13], v[10:11]
	v_mov_b64_e32 v[10:11], v[8:9]
	v_mov_b64_e32 v[8:9], v[6:7]
	v_mov_b64_e32 v[6:7], v[4:5]
	v_mov_b64_e32 v[4:5], v[2:3]
	v_mov_b64_e32 v[2:3], v[0:1]
	s_cmpk_eq_i32 s46, 0xc0
	s_mov_b64 s[40:41], -1
	s_cbranch_scc0 .LBB0_1190
	s_branch .LBB0_1192

; #define MLA_DMA(t, s) do { glds16(ksrc + (long)(t) * KVBLK * KVP, (unsigned)__builtin_amdgcn_readfirstlane(kdst + (s) * KSLOT)); \
;         if (lane < 32) glds16(psrc + (long)(t) * KVBLK * PEP, (unsigned)__builtin_amdgcn_readfirstlane(pdst + (s) * KSLOT)); \
;         glds16(vsrc + (long)(t) * KVBLK * KVP, (unsigned)__builtin_amdgcn_readfirstlane(vdst + (s) * VSLOT)); } while (0)
; __device__ __forceinline__ void unit(int b, int h, int qb, const unsigned short* Q, const unsigned short* KV, const unsigned short* KPE, unsigned short* O, char* shm, const int wave_) {
;     ...
;         if (t + 2 < NT) MLA_DMA(t + 2, slot2);
.LBB0_1194:
	s_mul_i32 s69, s45, 0x3000
	s_add_i32 s40, s69, s43
	s_mov_b32 m0, s40
	s_nop 0
	global_load_lds_dwordx4 v[94:95], off
	s_and_saveexec_b64 s[40:41], s[2:3]
	s_cbranch_execz .LBB0_1196
	s_add_i32 s69, s69, s42
	s_mov_b32 m0, s69
	s_nop 0
	global_load_lds_dwordx4 v[90:91], off
.LBB0_1196:
	s_or_b64 exec, exec, s[40:41]
	s_lshl_b32 s40, s45, 13
	s_add_i32 s40, s40, s44
	s_mov_b32 m0, s40
	s_nop 0
	global_load_lds_dwordx4 v[92:93], off

; #define PG8_LDA(dst, b, h) do { _Pragma("unroll") for (int m = 0; m < 4; ++m) _Pragma("unroll") for (int k = 0; k < 2; ++k) dst[m][k] = *(const PG8_LAS bf16x8*)(lds + PG8_SA(b, h) + aoff + m * 2048 + k * 1024); } while (0)
; #define PG8_LDB(dst, b, h) do { _Pragma("unroll") for (int n = 0; n < 2; ++n) _Pragma("unroll") for (int k = 0; k < 2; ++k) dst[n][k] = *(const PG8_LAS bf16x8*)(lds + PG8_SB(b, h) + boff + n * 2048 + k * 1024); } while (0)
; #define PG8_WAIT_V(n) asm volatile("s_waitcnt vmcnt(" #n ")" ::: "memory")
; #define PG8_WAIT_L(n) asm volatile("s_waitcnt lgkmcnt(" #n ")" ::: "memory")
; #define PG8_BAR __builtin_amdgcn_s_barrier()
; #define PG8_SCHED __builtin_amdgcn_sched_barrier(0)
; template <class Epi, class Sched, bool ALIGN_EPI = false, bool SP2 = false, bool F8 = false, bool I8 = false, bool PF = false>
; __device__ __forceinline__ void gemm_phase(PG8_LAS unsigned char* lds, const Gemm g, const Sched& S, const Epi& E, const int wave_) {
;     ...
;             if constexpr (SP2) {
;             PG8_LDB(B0, 0, 0); PG8_LDB(B1, 0, 1); PG8_SCHED; PG8_LDA(At, 0, 0); PG8_STAGE(PG8_SA(1, 1), a1 + hstep, voffA);
;             PG8_WAIT_V(8); PG8_WAIT_L(0); PG8_BAR; PG8_MMA(0, 0, At, B0); PG8_MMA(0, 1, At, B1); PG8_BAR; PG8_SCHED;
;             PG8_LDA(At, 0, 1); PG8_STAGE(PG8_SB(0, 0), b2, voffB); PG8_STAGE(PG8_SB(0, 1), b2 + hstep, voffB); PG8_STAGE(PG8_SA(0, 0), a2, voffA);
;             PG8_WAIT_V(8); PG8_WAIT_L(0); PG8_BAR; PG8_MMA(1, 0, At, B0); PG8_MMA(1, 1, At, B1); PG8_BAR; PG8_SCHED;
;             PG8_LDB(B0, 1, 0); PG8_LDB(B1, 1, 1); PG8_SCHED; PG8_LDA(At, 1, 0); PG8_STAGE(PG8_SA(0, 1), a2 + hstep, voffA);
;             PG8_WAIT_V(8); PG8_WAIT_L(0); PG8_BAR; PG8_MMA(0, 0, At, B0); PG8_MMA(0, 1, At, B1); PG8_BAR; PG8_SCHED;
;             PG8_LDA(At, 1, 1); PG8_STAGE(PG8_SB(1, 0), b3, voffB); PG8_STAGE(PG8_SB(1, 1), b3 + hstep, voffB); PG8_STAGE(PG8_SA(1, 0), a3, voffA);
;             PG8_WAIT_V(8); PG8_WAIT_L(0); PG8_BAR; PG8_MMA(1, 0, At, B0); PG8_MMA(1, 1, At, B1); PG8_BAR; PG8_SCHED;
.LBB0_1540:
	ds_read_b128 v[24:27], v181
	ds_read_b128 v[28:31], v181 offset:1024
	ds_read_b128 v[16:19], v181 offset:2048
	ds_read_b128 v[20:23], v181 offset:3072
	ds_read_b128 v[8:11], v182
	ds_read_b128 v[12:15], v182 offset:1024
	ds_read_b128 v[0:3], v182 offset:2048
	ds_read_b128 v[4:7], v182 offset:3072
	s_add_u32 s34, s30, 0xfffe0080
	s_addc_u32 s35, s31, -1
	s_cmp_eq_u32 s74, 4
	s_cselect_b32 s37, s19, s35
	s_cselect_b32 s36, s21, s34
	s_cselect_b32 s35, s17, s73
	s_cselect_b32 s34, s71, s72
	v_lshl_add_u64 v[210:211], s[30:31], 0, v[168:169]
	s_add_i32 m0, s29, 0xc000
	ds_read_b128 v[172:175], v183
	ds_read_b128 v[176:179], v183 offset:1024
	ds_read_b128 v[186:189], v183 offset:2048
	ds_read_b128 v[190:193], v183 offset:3072
	ds_read_b128 v[194:197], v183 offset:4096
	ds_read_b128 v[198:201], v183 offset:5120
	ds_read_b128 v[202:205], v183 offset:6144
	ds_read_b128 v[206:209], v183 offset:7168
	global_load_lds_dwordx4 v[210:211], off
	v_lshl_add_u64 v[210:211], s[30:31], 0, v[170:171]
	s_add_i32 m0, s29, 0xe000
	s_nop 0
	global_load_lds_dwordx4 v[210:211], off
	s_waitcnt vmcnt(8)
	s_waitcnt lgkmcnt(0)
	s_barrier
	s_waitcnt lgkmcnt(0)
	v_mfma_f32_16x16x128_f8f6f4 v[156:159], v[24:31], v[172:179], v[156:159]
	v_lshl_add_u64 v[222:223], s[34:35], 0, v[160:161]
	v_mfma_f32_16x16x128_f8f6f4 v[148:151], v[16:23], v[172:179], v[148:151]
	v_lshl_add_u64 v[224:225], s[34:35], 0, v[166:167]
	v_mfma_f32_16x16x128_f8f6f4 v[140:143], v[24:31], v[186:193], v[140:143]
	s_add_u32 s76, s34, 0x20000
	s_addc_u32 s77, s35, 0
	v_mfma_f32_16x16x128_f8f6f4 v[132:135], v[16:23], v[186:193], v[132:135]
	v_lshl_add_u64 v[226:227], s[76:77], 0, v[160:161]
	v_mfma_f32_16x16x128_f8f6f4 v[124:127], v[24:31], v[194:201], v[124:127]
	v_lshl_add_u64 v[228:229], s[76:77], 0, v[166:167]
	v_mfma_f32_16x16x128_f8f6f4 v[116:119], v[16:23], v[194:201], v[116:119]
	v_lshl_add_u64 v[230:231], s[36:37], 0, v[162:163]
	v_mfma_f32_16x16x128_f8f6f4 v[108:111], v[24:31], v[202:209], v[108:111]
	v_lshl_add_u64 v[232:233], s[36:37], 0, v[164:165]
	v_mfma_f32_16x16x128_f8f6f4 v[100:103], v[16:23], v[202:209], v[100:103]
	v_mfma_f32_16x16x128_f8f6f4 v[152:155], v[8:15], v[172:179], v[152:155]
	v_mfma_f32_16x16x128_f8f6f4 v[144:147], v[0:7], v[172:179], v[144:147]
	v_mfma_f32_16x16x128_f8f6f4 v[136:139], v[8:15], v[186:193], v[136:139]
	v_mfma_f32_16x16x128_f8f6f4 v[128:131], v[0:7], v[186:193], v[128:131]
	v_mfma_f32_16x16x128_f8f6f4 v[120:123], v[8:15], v[194:201], v[120:123]
	v_mfma_f32_16x16x128_f8f6f4 v[112:115], v[0:7], v[194:201], v[112:115]
	v_mfma_f32_16x16x128_f8f6f4 v[104:107], v[8:15], v[202:209], v[104:107]
	v_mfma_f32_16x16x128_f8f6f4 v[96:99], v[0:7], v[202:209], v[96:99]
	s_barrier
	s_add_i32 s75, s55, s39
	s_mov_b32 m0, s75
	ds_read_b128 v[186:189], v183 offset:16384
	ds_read_b128 v[190:193], v183 offset:17408
	ds_read_b128 v[194:197], v183 offset:18432
	ds_read_b128 v[198:201], v183 offset:19456
	ds_read_b128 v[202:205], v183 offset:20480
	ds_read_b128 v[206:209], v183 offset:21504
	ds_read_b128 v[210:213], v183 offset:22528
	ds_read_b128 v[214:217], v183 offset:23552
	global_load_lds_dwordx4 v[222:223], off
	s_add_i32 m0, s75, 0x2000
	s_add_i32 s75, s64, s39
	global_load_lds_dwordx4 v[224:225], off
	s_mov_b32 m0, s75
	s_nop 0
	global_load_lds_dwordx4 v[226:227], off
	s_add_i32 m0, s75, 0x2000
	s_nop 0
	global_load_lds_dwordx4 v[228:229], off
	s_mov_b32 m0, s29
	s_nop 0
	global_load_lds_dwordx4 v[230:231], off
	s_mov_b32 m0, s42
	s_nop 0
	global_load_lds_dwordx4 v[232:233], off
	s_waitcnt vmcnt(8)
	s_waitcnt lgkmcnt(0)
	s_barrier
	s_waitcnt lgkmcnt(0)
	v_mfma_f32_16x16x128_f8f6f4 v[92:95], v[24:31], v[186:193], v[92:95]
	v_mfma_f32_16x16x128_f8f6f4 v[84:87], v[16:23], v[186:193], v[84:87]
	v_mfma_f32_16x16x128_f8f6f4 v[76:79], v[24:31], v[194:201], v[76:79]
	v_mfma_f32_16x16x128_f8f6f4 v[68:71], v[16:23], v[194:201], v[68:71]
	v_mfma_f32_16x16x128_f8f6f4 v[60:63], v[24:31], v[202:209], v[60:63]
	v_mfma_f32_16x16x128_f8f6f4 v[52:55], v[16:23], v[202:209], v[52:55]
	v_mfma_f32_16x16x128_f8f6f4 v[44:47], v[24:31], v[210:217], v[44:47]
	v_mfma_f32_16x16x128_f8f6f4 v[36:39], v[16:23], v[210:217], v[36:39]
	v_mfma_f32_16x16x128_f8f6f4 v[88:91], v[8:15], v[186:193], v[88:91]
	v_mfma_f32_16x16x128_f8f6f4 v[80:83], v[0:7], v[186:193], v[80:83]
	v_mfma_f32_16x16x128_f8f6f4 v[72:75], v[8:15], v[194:201], v[72:75]
	v_mfma_f32_16x16x128_f8f6f4 v[64:67], v[0:7], v[194:201], v[64:67]
	v_mfma_f32_16x16x128_f8f6f4 v[56:59], v[8:15], v[202:209], v[56:59]
	v_mfma_f32_16x16x128_f8f6f4 v[48:51], v[0:7], v[202:209], v[48:51]
	v_mfma_f32_16x16x128_f8f6f4 v[40:43], v[8:15], v[210:217], v[40:43]
	v_mfma_f32_16x16x128_f8f6f4 v[32:35], v[0:7], v[210:217], v[32:35]
	s_barrier
; #define PG8_LDA(dst, b, h) do { _Pragma("unroll") for (int m = 0; m < 4; ++m) _Pragma("unroll") for (int k = 0; k < 2; ++k) dst[m][k] = *(const PG8_LAS bf16x8*)(lds + PG8_SA(b, h) + aoff + m * 2048 + k * 1024); } while (0)
; #define PG8_LDB(dst, b, h) do { _Pragma("unroll") for (int n = 0; n < 2; ++n) _Pragma("unroll") for (int k = 0; k < 2; ++k) dst[n][k] = *(const PG8_LAS bf16x8*)(lds + PG8_SB(b, h) + boff + n * 2048 + k * 1024); } while (0)
; #define PG8_WAIT_V(n) asm volatile("s_waitcnt vmcnt(" #n ")" ::: "memory")
; #define PG8_WAIT_L(n) asm volatile("s_waitcnt lgkmcnt(" #n ")" ::: "memory")
; #define PG8_BAR __builtin_amdgcn_s_barrier()
; #define PG8_SCHED __builtin_amdgcn_sched_barrier(0)
; template <class Epi, class Sched, bool ALIGN_EPI = false, bool SP2 = false, bool F8 = false, bool I8 = false, bool PF = false>
; __device__ __forceinline__ void gemm_phase(PG8_LAS unsigned char* lds, const Gemm g, const Sched& S, const Epi& E, const int wave_) {
;     ...
;             if constexpr (SP2) {
;             PG8_LDB(B0, 0, 0); PG8_LDB(B1, 0, 1); PG8_SCHED; PG8_LDA(At, 0, 0); PG8_STAGE(PG8_SA(1, 1), a1 + hstep, voffA);
;             PG8_WAIT_V(8); PG8_WAIT_L(0); PG8_BAR; PG8_MMA(0, 0, At, B0); PG8_MMA(0, 1, At, B1); PG8_BAR; PG8_SCHED;
;             PG8_LDA(At, 0, 1); PG8_STAGE(PG8_SB(0, 0), b2, voffB); PG8_STAGE(PG8_SB(0, 1), b2 + hstep, voffB); PG8_STAGE(PG8_SA(0, 0), a2, voffA);
;             PG8_WAIT_V(8); PG8_WAIT_L(0); PG8_BAR; PG8_MMA(1, 0, At, B0); PG8_MMA(1, 1, At, B1); PG8_BAR; PG8_SCHED;
;             PG8_LDB(B0, 1, 0); PG8_LDB(B1, 1, 1); PG8_SCHED; PG8_LDA(At, 1, 0); PG8_STAGE(PG8_SA(0, 1), a2 + hstep, voffA);
;             PG8_WAIT_V(8); PG8_WAIT_L(0); PG8_BAR; PG8_MMA(0, 0, At, B0); PG8_MMA(0, 1, At, B1); PG8_BAR; PG8_SCHED;
;             PG8_LDA(At, 1, 1); PG8_STAGE(PG8_SB(1, 0), b3, voffB); PG8_STAGE(PG8_SB(1, 1), b3 + hstep, voffB); PG8_STAGE(PG8_SA(1, 0), a3, voffA);
;             PG8_WAIT_V(8); PG8_WAIT_L(0); PG8_BAR; PG8_MMA(1, 0, At, B0); PG8_MMA(1, 1, At, B1); PG8_BAR; PG8_SCHED;
	s_add_i32 s75, 0, 0x18000
	s_add_i32 s76, 0, 0x1c000
	v_add_u32_e32 v12, s75, v180
	v_add_u32_e32 v28, s76, v180
	ds_read_b128 v[0:3], v12
	ds_read_b128 v[4:7], v12 offset:1024
	ds_read_b128 v[8:11], v12 offset:2048
	ds_read_b128 v[12:15], v12 offset:3072
	ds_read_b128 v[16:19], v28
	ds_read_b128 v[20:23], v28 offset:1024
	ds_read_b128 v[24:27], v28 offset:2048
	ds_read_b128 v[28:31], v28 offset:3072
	s_add_u32 s36, s36, 0x20000
	s_addc_u32 s37, s37, 0
	s_mov_b32 m0, s43
	v_lshl_add_u64 v[218:219], s[36:37], 0, v[162:163]
	ds_read_b128 v[186:189], v183 offset:32768
	ds_read_b128 v[190:193], v183 offset:33792
	ds_read_b128 v[194:197], v183 offset:34816
	ds_read_b128 v[198:201], v183 offset:35840
	ds_read_b128 v[202:205], v183 offset:36864
	ds_read_b128 v[206:209], v183 offset:37888
	ds_read_b128 v[210:213], v183 offset:38912
	ds_read_b128 v[214:217], v183 offset:39936
	global_load_lds_dwordx4 v[218:219], off
	v_lshl_add_u64 v[218:219], s[36:37], 0, v[164:165]
	s_mov_b32 m0, s44
	s_nop 0
	global_load_lds_dwordx4 v[218:219], off
	s_waitcnt vmcnt(8)
	s_waitcnt lgkmcnt(0)
	s_barrier
	s_waitcnt lgkmcnt(0)
	v_mfma_f32_16x16x128_f8f6f4 v[156:159], v[0:7], v[186:193], v[156:159]
	v_lshl_add_u64 v[222:223], v[222:223], 0, s[8:9]
	v_mfma_f32_16x16x128_f8f6f4 v[148:151], v[8:15], v[186:193], v[148:151]
	v_lshl_add_u64 v[224:225], v[224:225], 0, s[8:9]
	v_mfma_f32_16x16x128_f8f6f4 v[140:143], v[0:7], v[194:201], v[140:143]
	v_lshl_add_u64 v[226:227], v[226:227], 0, s[8:9]
	v_mfma_f32_16x16x128_f8f6f4 v[132:135], v[8:15], v[194:201], v[132:135]
	v_lshl_add_u64 v[228:229], v[228:229], 0, s[8:9]
	v_mfma_f32_16x16x128_f8f6f4 v[124:127], v[0:7], v[202:209], v[124:127]
	v_lshl_add_u64 v[230:231], v[230:231], 0, s[8:9]
	v_mfma_f32_16x16x128_f8f6f4 v[116:119], v[8:15], v[202:209], v[116:119]
	v_lshl_add_u64 v[232:233], v[232:233], 0, s[8:9]
	v_mfma_f32_16x16x128_f8f6f4 v[108:111], v[0:7], v[210:217], v[108:111]
	v_mfma_f32_16x16x128_f8f6f4 v[100:103], v[8:15], v[210:217], v[100:103]
	v_mfma_f32_16x16x128_f8f6f4 v[152:155], v[16:23], v[186:193], v[152:155]
	v_mfma_f32_16x16x128_f8f6f4 v[144:147], v[24:31], v[186:193], v[144:147]
	v_mfma_f32_16x16x128_f8f6f4 v[136:139], v[16:23], v[194:201], v[136:139]
	v_mfma_f32_16x16x128_f8f6f4 v[128:131], v[24:31], v[194:201], v[128:131]
	v_mfma_f32_16x16x128_f8f6f4 v[120:123], v[16:23], v[202:209], v[120:123]
	v_mfma_f32_16x16x128_f8f6f4 v[112:115], v[24:31], v[202:209], v[112:115]
	v_mfma_f32_16x16x128_f8f6f4 v[104:107], v[16:23], v[210:217], v[104:107]
	v_mfma_f32_16x16x128_f8f6f4 v[96:99], v[24:31], v[210:217], v[96:99]
	s_barrier
	s_add_i32 s36, s75, s39
	s_mov_b32 m0, s36
	ds_read_b128 v[186:189], v183 offset:49152
	ds_read_b128 v[190:193], v183 offset:50176
	ds_read_b128 v[194:197], v183 offset:51200
	ds_read_b128 v[198:201], v183 offset:52224
	ds_read_b128 v[202:205], v183 offset:53248
	ds_read_b128 v[206:209], v183 offset:54272
	ds_read_b128 v[210:213], v183 offset:55296
	ds_read_b128 v[214:217], v183 offset:56320
	global_load_lds_dwordx4 v[222:223], off
	s_add_i32 m0, s36, 0x2000
	s_add_u32 s34, s34, 0x20080
	s_addc_u32 s35, s35, 0
	s_add_i32 s36, s76, s39
	global_load_lds_dwordx4 v[224:225], off
	s_mov_b32 m0, s36
	s_nop 0
	global_load_lds_dwordx4 v[226:227], off
	s_add_i32 m0, s36, 0x2000
	s_nop 0
	global_load_lds_dwordx4 v[228:229], off
	s_mov_b32 m0, s48
	s_nop 0
	global_load_lds_dwordx4 v[230:231], off
	s_mov_b32 m0, s49
	s_nop 0
	global_load_lds_dwordx4 v[232:233], off
	s_waitcnt vmcnt(8)
	s_waitcnt lgkmcnt(0)
	s_barrier
	s_waitcnt lgkmcnt(0)
	v_mfma_f32_16x16x128_f8f6f4 v[92:95], v[0:7], v[186:193], v[92:95]
	v_mfma_f32_16x16x128_f8f6f4 v[84:87], v[8:15], v[186:193], v[84:87]
	v_mfma_f32_16x16x128_f8f6f4 v[76:79], v[0:7], v[194:201], v[76:79]
	v_mfma_f32_16x16x128_f8f6f4 v[68:71], v[8:15], v[194:201], v[68:71]
	v_mfma_f32_16x16x128_f8f6f4 v[60:63], v[0:7], v[202:209], v[60:63]
	v_mfma_f32_16x16x128_f8f6f4 v[52:55], v[8:15], v[202:209], v[52:55]
	v_mfma_f32_16x16x128_f8f6f4 v[44:47], v[0:7], v[210:217], v[44:47]
	v_mfma_f32_16x16x128_f8f6f4 v[36:39], v[8:15], v[210:217], v[36:39]
	v_mfma_f32_16x16x128_f8f6f4 v[88:91], v[16:23], v[186:193], v[88:91]
	v_mfma_f32_16x16x128_f8f6f4 v[80:83], v[24:31], v[186:193], v[80:83]
	v_mfma_f32_16x16x128_f8f6f4 v[72:75], v[16:23], v[194:201], v[72:75]
	v_mfma_f32_16x16x128_f8f6f4 v[64:67], v[24:31], v[194:201], v[64:67]
	v_mfma_f32_16x16x128_f8f6f4 v[56:59], v[16:23], v[202:209], v[56:59]
	v_mfma_f32_16x16x128_f8f6f4 v[48:51], v[24:31], v[202:209], v[48:51]
	v_mfma_f32_16x16x128_f8f6f4 v[40:43], v[16:23], v[210:217], v[40:43]
	v_mfma_f32_16x16x128_f8f6f4 v[32:35], v[24:31], v[210:217], v[32:35]
	s_barrier
	s_add_i32 s74, s74, 2
	s_add_u32 s30, s30, 0x100
	s_addc_u32 s31, s31, 0
	s_add_u32 s72, s72, 0x100
	s_addc_u32 s73, s73, 0
	s_cmp_gt_u32 s74, 5
	s_cbranch_scc0 .LBB0_1540
	s_and_b64 vcc, exec, s[10:11]
	s_cbranch_vccz .LBB0_1543
	s_barrier
